# combined: vectorised expert search + P12 EpiY store ladder de-serialised + P11 A-gather LDS-DMA deferred to next load segment + 15 mid-burst LDS waits removed in GEMM loops
# speedup vs baseline: 1.0008x; 1.0008x over previous
.LBB0_136:
	s_setprio 0
	s_barrier
	s_add_i32 s40, 0, 0x18000
	s_add_i32 s41, 0, 0x1c000
	v_add_u32_e32 v142, s40, v241
	v_add_u32_e32 v158, s41, v241
	ds_read_b128 v[130:133], v142
	ds_read_b128 v[134:137], v142 offset:1024
	ds_read_b128 v[138:141], v142 offset:2048
	ds_read_b128 v[142:145], v142 offset:3072
	ds_read_b128 v[146:149], v158
	ds_read_b128 v[150:153], v158 offset:1024
	ds_read_b128 v[154:157], v158 offset:2048
	ds_read_b128 v[158:161], v158 offset:3072
	s_add_u32 s38, s38, 0x80000
	s_addc_u32 s39, s39, 0
	s_mov_b32 m0, s52
	v_lshl_add_u64 v[244:245], s[38:39], 0, v[198:199]
	ds_read_b128 v[162:165], v242 offset:32768
	ds_read_b128 v[166:169], v242 offset:33792
	ds_read_b128 v[170:173], v242 offset:34816
	ds_read_b128 v[174:177], v242 offset:35840
	ds_read_b128 v[178:181], v242 offset:36864
	ds_read_b128 v[182:185], v242 offset:37888
	ds_read_b128 v[186:189], v242 offset:38912
	ds_read_b128 v[190:193], v242 offset:39936
	global_load_lds_dwordx4 v[244:245], off
	v_lshl_add_u64 v[244:245], s[38:39], 0, v[202:203]
	s_mov_b32 m0, s53
	s_nop 0
	global_load_lds_dwordx4 v[244:245], off
	s_waitcnt vmcnt(8)
	s_waitcnt lgkmcnt(0)
	s_barrier
	s_setprio 1
	s_waitcnt lgkmcnt(0)
	v_mfma_f32_16x16x32_bf16 v[126:129], v[130:133], v[162:165], v[126:129]
	v_mfma_f32_16x16x32_bf16 v[122:125], v[138:141], v[162:165], v[122:125]
	v_mfma_f32_16x16x32_bf16 v[118:121], v[130:133], v[170:173], v[118:121]
	v_mfma_f32_16x16x32_bf16 v[114:117], v[138:141], v[170:173], v[114:117]
	v_mfma_f32_16x16x32_bf16 v[110:113], v[130:133], v[178:181], v[110:113]
	v_mfma_f32_16x16x32_bf16 v[106:109], v[138:141], v[178:181], v[106:109]
	v_mfma_f32_16x16x32_bf16 v[102:105], v[130:133], v[186:189], v[102:105]
	v_mfma_f32_16x16x32_bf16 v[98:101], v[138:141], v[186:189], v[98:101]
	v_mfma_f32_16x16x32_bf16 v[126:129], v[134:137], v[166:169], v[126:129]
	v_mfma_f32_16x16x32_bf16 v[122:125], v[142:145], v[166:169], v[122:125]
	v_mfma_f32_16x16x32_bf16 v[118:121], v[134:137], v[174:177], v[118:121]
	v_mfma_f32_16x16x32_bf16 v[114:117], v[142:145], v[174:177], v[114:117]
	v_mfma_f32_16x16x32_bf16 v[110:113], v[134:137], v[182:185], v[110:113]
	v_mfma_f32_16x16x32_bf16 v[106:109], v[142:145], v[182:185], v[106:109]
	v_mfma_f32_16x16x32_bf16 v[102:105], v[134:137], v[190:193], v[102:105]
	v_mfma_f32_16x16x32_bf16 v[98:101], v[142:145], v[190:193], v[98:101]
	s_setprio 0
	s_setprio 1
	v_mfma_f32_16x16x32_bf16 v[94:97], v[146:149], v[162:165], v[94:97]
	v_mfma_f32_16x16x32_bf16 v[90:93], v[154:157], v[162:165], v[90:93]
	v_mfma_f32_16x16x32_bf16 v[86:89], v[146:149], v[170:173], v[86:89]
	v_mfma_f32_16x16x32_bf16 v[82:85], v[154:157], v[170:173], v[82:85]
	v_mfma_f32_16x16x32_bf16 v[78:81], v[146:149], v[178:181], v[78:81]
	v_mfma_f32_16x16x32_bf16 v[74:77], v[154:157], v[178:181], v[74:77]
	v_mfma_f32_16x16x32_bf16 v[70:73], v[146:149], v[186:189], v[70:73]
	v_mfma_f32_16x16x32_bf16 v[66:69], v[154:157], v[186:189], v[66:69]
	v_mfma_f32_16x16x32_bf16 v[94:97], v[150:153], v[166:169], v[94:97]
	v_mfma_f32_16x16x32_bf16 v[90:93], v[158:161], v[166:169], v[90:93]
	v_mfma_f32_16x16x32_bf16 v[86:89], v[150:153], v[174:177], v[86:89]
	v_mfma_f32_16x16x32_bf16 v[82:85], v[158:161], v[174:177], v[82:85]
	v_mfma_f32_16x16x32_bf16 v[78:81], v[150:153], v[182:185], v[78:81]
	v_mfma_f32_16x16x32_bf16 v[74:77], v[158:161], v[182:185], v[74:77]
	v_mfma_f32_16x16x32_bf16 v[70:73], v[150:153], v[190:193], v[70:73]
	v_mfma_f32_16x16x32_bf16 v[66:69], v[158:161], v[190:193], v[66:69]
	s_setprio 0
	s_barrier
	s_add_i32 s38, s40, s43
	v_lshl_add_u64 v[228:229], v[228:229], 0, s[18:19]
	s_mov_b32 m0, s38
	ds_read_b128 v[162:165], v242 offset:49152
	ds_read_b128 v[166:169], v242 offset:50176
	ds_read_b128 v[170:173], v242 offset:51200
	ds_read_b128 v[174:177], v242 offset:52224
	ds_read_b128 v[178:181], v242 offset:53248
	ds_read_b128 v[182:185], v242 offset:54272
	ds_read_b128 v[186:189], v242 offset:55296
	ds_read_b128 v[190:193], v242 offset:56320
	global_load_lds_dwordx4 v[228:229], off
	s_add_i32 m0, s38, 0x2000
	s_add_u32 s34, s34, 0x80080
	v_lshl_add_u64 v[226:227], v[226:227], 0, s[18:19]
	s_addc_u32 s35, s35, 0
	s_add_i32 s38, s41, s43
	global_load_lds_dwordx4 v[226:227], off
	v_lshl_add_u64 v[226:227], s[34:35], 0, v[200:201]
	s_mov_b32 m0, s38
	v_lshl_add_u64 v[222:223], v[222:223], 0, s[18:19]
	global_load_lds_dwordx4 v[226:227], off
	v_lshl_add_u64 v[226:227], s[34:35], 0, v[204:205]
	s_add_i32 m0, s38, 0x2000
	s_nop 0
	global_load_lds_dwordx4 v[226:227], off
	s_mov_b32 m0, s66
	s_nop 0
	global_load_lds_dwordx4 v[222:223], off
	v_lshl_add_u64 v[222:223], v[224:225], 0, s[18:19]
	s_mov_b32 m0, s67
	s_nop 0
	global_load_lds_dwordx4 v[222:223], off
	s_waitcnt vmcnt(8)
	s_waitcnt lgkmcnt(0)
	s_barrier
	s_setprio 1
	s_waitcnt lgkmcnt(0)
	v_mfma_f32_16x16x32_bf16 v[62:65], v[130:133], v[162:165], v[62:65]
	v_mfma_f32_16x16x32_bf16 v[58:61], v[138:141], v[162:165], v[58:61]
	v_mfma_f32_16x16x32_bf16 v[54:57], v[130:133], v[170:173], v[54:57]
	v_mfma_f32_16x16x32_bf16 v[50:53], v[138:141], v[170:173], v[50:53]
	v_mfma_f32_16x16x32_bf16 v[46:49], v[130:133], v[178:181], v[46:49]
	v_mfma_f32_16x16x32_bf16 v[42:45], v[138:141], v[178:181], v[42:45]
	v_mfma_f32_16x16x32_bf16 v[38:41], v[130:133], v[186:189], v[38:41]
	v_mfma_f32_16x16x32_bf16 v[34:37], v[138:141], v[186:189], v[34:37]
	v_mfma_f32_16x16x32_bf16 v[62:65], v[134:137], v[166:169], v[62:65]
	v_mfma_f32_16x16x32_bf16 v[58:61], v[142:145], v[166:169], v[58:61]
	v_mfma_f32_16x16x32_bf16 v[54:57], v[134:137], v[174:177], v[54:57]
	v_mfma_f32_16x16x32_bf16 v[50:53], v[142:145], v[174:177], v[50:53]
	v_mfma_f32_16x16x32_bf16 v[46:49], v[134:137], v[182:185], v[46:49]
	v_mfma_f32_16x16x32_bf16 v[42:45], v[142:145], v[182:185], v[42:45]
	v_mfma_f32_16x16x32_bf16 v[38:41], v[134:137], v[190:193], v[38:41]
	v_mfma_f32_16x16x32_bf16 v[34:37], v[142:145], v[190:193], v[34:37]
	s_setprio 0
	s_setprio 1
	v_mfma_f32_16x16x32_bf16 v[30:33], v[146:149], v[162:165], v[30:33]
	v_mfma_f32_16x16x32_bf16 v[26:29], v[154:157], v[162:165], v[26:29]
	v_mfma_f32_16x16x32_bf16 v[22:25], v[146:149], v[170:173], v[22:25]
	v_mfma_f32_16x16x32_bf16 v[18:21], v[154:157], v[170:173], v[18:21]
	v_mfma_f32_16x16x32_bf16 v[14:17], v[146:149], v[178:181], v[14:17]
	v_mfma_f32_16x16x32_bf16 v[10:13], v[154:157], v[178:181], v[10:13]
	v_mfma_f32_16x16x32_bf16 v[6:9], v[146:149], v[186:189], v[6:9]
	v_mfma_f32_16x16x32_bf16 v[2:5], v[154:157], v[186:189], v[2:5]
	v_mfma_f32_16x16x32_bf16 v[30:33], v[150:153], v[166:169], v[30:33]
	v_mfma_f32_16x16x32_bf16 v[26:29], v[158:161], v[166:169], v[26:29]
	v_mfma_f32_16x16x32_bf16 v[22:25], v[150:153], v[174:177], v[22:25]
	v_mfma_f32_16x16x32_bf16 v[18:21], v[158:161], v[174:177], v[18:21]
	v_mfma_f32_16x16x32_bf16 v[14:17], v[150:153], v[182:185], v[14:17]
	v_mfma_f32_16x16x32_bf16 v[10:13], v[158:161], v[182:185], v[10:13]
	v_mfma_f32_16x16x32_bf16 v[6:9], v[150:153], v[190:193], v[6:9]
	v_mfma_f32_16x16x32_bf16 v[2:5], v[158:161], v[190:193], v[2:5]
	s_setprio 0
	s_barrier
	s_add_i32 s75, s75, 2
	s_add_u32 s30, s30, 0x100
	s_addc_u32 s31, s31, 0
	s_cmp_gt_u32 s75, 29
	s_cbranch_scc1 .LBB0_144

.LBB0_180:
	s_setprio 0
	s_barrier
	v_add_u32_e32 v142, s40, v219
	v_add_u32_e32 v158, s41, v219
	ds_read_b128 v[130:133], v142
	ds_read_b128 v[134:137], v142 offset:1024
	ds_read_b128 v[138:141], v142 offset:2048
	ds_read_b128 v[142:145], v142 offset:3072
	ds_read_b128 v[146:149], v158
	ds_read_b128 v[150:153], v158 offset:1024
	ds_read_b128 v[154:157], v158 offset:2048
	ds_read_b128 v[158:161], v158 offset:3072
	s_add_u32 s14, s14, 0x80000
	s_addc_u32 s15, s15, 0
	s_mov_b32 m0, s27
	v_lshl_add_u64 v[224:225], s[14:15], 0, v[198:199]
	ds_read_b128 v[162:165], v222 offset:32768
	ds_read_b128 v[166:169], v222 offset:33792
	ds_read_b128 v[170:173], v222 offset:34816
	ds_read_b128 v[174:177], v222 offset:35840
	ds_read_b128 v[178:181], v222 offset:36864
	ds_read_b128 v[182:185], v222 offset:37888
	ds_read_b128 v[186:189], v222 offset:38912
	ds_read_b128 v[190:193], v222 offset:39936
	global_load_lds_dwordx4 v[224:225], off
	v_lshl_add_u64 v[224:225], s[14:15], 0, v[202:203]
	s_mov_b32 m0, s28
	s_nop 0
	global_load_lds_dwordx4 v[224:225], off
	s_waitcnt vmcnt(8)
	s_waitcnt lgkmcnt(0)
	s_barrier
	s_setprio 1
	s_waitcnt lgkmcnt(0)
	v_mfma_f32_16x16x32_bf16 v[126:129], v[130:133], v[162:165], v[126:129]
	v_mfma_f32_16x16x32_bf16 v[122:125], v[138:141], v[162:165], v[122:125]
	v_mfma_f32_16x16x32_bf16 v[118:121], v[130:133], v[170:173], v[118:121]
	v_mfma_f32_16x16x32_bf16 v[114:117], v[138:141], v[170:173], v[114:117]
	v_mfma_f32_16x16x32_bf16 v[102:105], v[130:133], v[178:181], v[102:105]
	v_mfma_f32_16x16x32_bf16 v[98:101], v[138:141], v[178:181], v[98:101]
	v_mfma_f32_16x16x32_bf16 v[86:89], v[130:133], v[186:189], v[86:89]
	v_mfma_f32_16x16x32_bf16 v[82:85], v[138:141], v[186:189], v[82:85]
	v_mfma_f32_16x16x32_bf16 v[126:129], v[134:137], v[166:169], v[126:129]
	v_mfma_f32_16x16x32_bf16 v[122:125], v[142:145], v[166:169], v[122:125]
	v_mfma_f32_16x16x32_bf16 v[118:121], v[134:137], v[174:177], v[118:121]
	v_mfma_f32_16x16x32_bf16 v[114:117], v[142:145], v[174:177], v[114:117]
	v_mfma_f32_16x16x32_bf16 v[102:105], v[134:137], v[182:185], v[102:105]
	v_mfma_f32_16x16x32_bf16 v[98:101], v[142:145], v[182:185], v[98:101]
	v_mfma_f32_16x16x32_bf16 v[86:89], v[134:137], v[190:193], v[86:89]
	v_mfma_f32_16x16x32_bf16 v[82:85], v[142:145], v[190:193], v[82:85]
	s_setprio 0
	s_setprio 1
	v_mfma_f32_16x16x32_bf16 v[110:113], v[146:149], v[162:165], v[110:113]
	v_mfma_f32_16x16x32_bf16 v[106:109], v[154:157], v[162:165], v[106:109]
	v_mfma_f32_16x16x32_bf16 v[94:97], v[146:149], v[170:173], v[94:97]
	v_mfma_f32_16x16x32_bf16 v[90:93], v[154:157], v[170:173], v[90:93]
	v_mfma_f32_16x16x32_bf16 v[78:81], v[146:149], v[178:181], v[78:81]
	v_mfma_f32_16x16x32_bf16 v[74:77], v[154:157], v[178:181], v[74:77]
	v_mfma_f32_16x16x32_bf16 v[70:73], v[146:149], v[186:189], v[70:73]
	v_mfma_f32_16x16x32_bf16 v[66:69], v[154:157], v[186:189], v[66:69]
	v_mfma_f32_16x16x32_bf16 v[110:113], v[150:153], v[166:169], v[110:113]
	v_mfma_f32_16x16x32_bf16 v[106:109], v[158:161], v[166:169], v[106:109]
	v_mfma_f32_16x16x32_bf16 v[94:97], v[150:153], v[174:177], v[94:97]
	v_mfma_f32_16x16x32_bf16 v[90:93], v[158:161], v[174:177], v[90:93]
	v_mfma_f32_16x16x32_bf16 v[78:81], v[150:153], v[182:185], v[78:81]
	v_mfma_f32_16x16x32_bf16 v[74:77], v[158:161], v[182:185], v[74:77]
	v_mfma_f32_16x16x32_bf16 v[70:73], v[150:153], v[190:193], v[70:73]
	v_mfma_f32_16x16x32_bf16 v[66:69], v[158:161], v[190:193], v[66:69]
	s_setprio 0
	s_barrier
	s_mov_b32 m0, s42
	v_lshl_add_u64 v[210:211], v[210:211], 0, s[4:5]
	s_add_u32 s12, s12, 0x80080
	ds_read_b128 v[162:165], v222 offset:49152
	ds_read_b128 v[166:169], v222 offset:50176
	ds_read_b128 v[170:173], v222 offset:51200
	ds_read_b128 v[174:177], v222 offset:52224
	ds_read_b128 v[178:181], v222 offset:53248
	ds_read_b128 v[182:185], v222 offset:54272
	ds_read_b128 v[186:189], v222 offset:55296
	ds_read_b128 v[190:193], v222 offset:56320
	global_load_lds_dwordx4 v[210:211], off
	v_lshl_add_u64 v[210:211], v[212:213], 0, s[4:5]
	s_mov_b32 m0, s43
	s_addc_u32 s13, s13, 0
	global_load_lds_dwordx4 v[210:211], off
	v_lshl_add_u64 v[210:211], s[12:13], 0, v[200:201]
	s_mov_b32 m0, s44
	s_nop 0
	global_load_lds_dwordx4 v[210:211], off
	v_lshl_add_u64 v[210:211], s[12:13], 0, v[204:205]
	s_mov_b32 m0, s45
	s_nop 0
	global_load_lds_dwordx4 v[210:211], off
	v_lshl_add_u64 v[210:211], v[214:215], 0, s[4:5]
	s_mov_b32 m0, s30
	s_nop 0
	global_load_lds_dwordx4 v[210:211], off
	v_lshl_add_u64 v[210:211], v[216:217], 0, s[4:5]
	s_mov_b32 m0, s31
	s_nop 0
	global_load_lds_dwordx4 v[210:211], off
	s_waitcnt vmcnt(8)
	s_waitcnt lgkmcnt(0)
	s_barrier
	s_setprio 1
	s_waitcnt lgkmcnt(0)
	v_mfma_f32_16x16x32_bf16 v[62:65], v[130:133], v[162:165], v[62:65]
	v_mfma_f32_16x16x32_bf16 v[58:61], v[138:141], v[162:165], v[58:61]
	v_mfma_f32_16x16x32_bf16 v[54:57], v[130:133], v[170:173], v[54:57]
	v_mfma_f32_16x16x32_bf16 v[50:53], v[138:141], v[170:173], v[50:53]
	v_mfma_f32_16x16x32_bf16 v[38:41], v[130:133], v[178:181], v[38:41]
	v_mfma_f32_16x16x32_bf16 v[34:37], v[138:141], v[178:181], v[34:37]
	v_mfma_f32_16x16x32_bf16 v[22:25], v[130:133], v[186:189], v[22:25]
	v_mfma_f32_16x16x32_bf16 v[18:21], v[138:141], v[186:189], v[18:21]
	v_mfma_f32_16x16x32_bf16 v[62:65], v[134:137], v[166:169], v[62:65]
	v_mfma_f32_16x16x32_bf16 v[58:61], v[142:145], v[166:169], v[58:61]
	v_mfma_f32_16x16x32_bf16 v[54:57], v[134:137], v[174:177], v[54:57]
	v_mfma_f32_16x16x32_bf16 v[50:53], v[142:145], v[174:177], v[50:53]
	v_mfma_f32_16x16x32_bf16 v[38:41], v[134:137], v[182:185], v[38:41]
	v_mfma_f32_16x16x32_bf16 v[34:37], v[142:145], v[182:185], v[34:37]
	v_mfma_f32_16x16x32_bf16 v[22:25], v[134:137], v[190:193], v[22:25]
	v_mfma_f32_16x16x32_bf16 v[18:21], v[142:145], v[190:193], v[18:21]
	s_setprio 0
	s_setprio 1
	v_mfma_f32_16x16x32_bf16 v[46:49], v[146:149], v[162:165], v[46:49]
	v_mfma_f32_16x16x32_bf16 v[42:45], v[154:157], v[162:165], v[42:45]
	v_mfma_f32_16x16x32_bf16 v[30:33], v[146:149], v[170:173], v[30:33]
	v_mfma_f32_16x16x32_bf16 v[26:29], v[154:157], v[170:173], v[26:29]
	v_mfma_f32_16x16x32_bf16 v[14:17], v[146:149], v[178:181], v[14:17]
	v_mfma_f32_16x16x32_bf16 v[10:13], v[154:157], v[178:181], v[10:13]
	v_mfma_f32_16x16x32_bf16 v[6:9], v[146:149], v[186:189], v[6:9]
	v_mfma_f32_16x16x32_bf16 v[2:5], v[154:157], v[186:189], v[2:5]
	v_mfma_f32_16x16x32_bf16 v[46:49], v[150:153], v[166:169], v[46:49]
	v_mfma_f32_16x16x32_bf16 v[42:45], v[158:161], v[166:169], v[42:45]
	v_mfma_f32_16x16x32_bf16 v[30:33], v[150:153], v[174:177], v[30:33]
	v_mfma_f32_16x16x32_bf16 v[26:29], v[158:161], v[174:177], v[26:29]
	v_mfma_f32_16x16x32_bf16 v[14:17], v[150:153], v[182:185], v[14:17]
	v_mfma_f32_16x16x32_bf16 v[10:13], v[158:161], v[182:185], v[10:13]
	v_mfma_f32_16x16x32_bf16 v[6:9], v[150:153], v[190:193], v[6:9]
	v_mfma_f32_16x16x32_bf16 v[2:5], v[158:161], v[190:193], v[2:5]
	s_setprio 0
	s_barrier
	s_add_i32 s35, s35, 2
	s_add_u32 s10, s10, 0x100
	s_addc_u32 s11, s11, 0
	s_cmp_gt_u32 s35, 29
	s_cbranch_scc1 .LBB0_188

.LBB0_262:
	s_setprio 0
	s_barrier
	v_add_u32_e32 v142, s38, v219
	v_add_u32_e32 v158, s39, v219
	ds_read_b128 v[130:133], v142
	ds_read_b128 v[134:137], v142 offset:1024
	ds_read_b128 v[138:141], v142 offset:2048
	ds_read_b128 v[142:145], v142 offset:3072
	ds_read_b128 v[146:149], v158
	ds_read_b128 v[150:153], v158 offset:1024
	ds_read_b128 v[154:157], v158 offset:2048
	ds_read_b128 v[158:161], v158 offset:3072
	s_add_u32 s14, s14, 0x80000
	s_addc_u32 s15, s15, 0
	s_mov_b32 m0, s25
	v_lshl_add_u64 v[224:225], s[14:15], 0, v[204:205]
	ds_read_b128 v[162:165], v222 offset:32768
	ds_read_b128 v[166:169], v222 offset:33792
	ds_read_b128 v[170:173], v222 offset:34816
	ds_read_b128 v[174:177], v222 offset:35840
	ds_read_b128 v[178:181], v222 offset:36864
	ds_read_b128 v[182:185], v222 offset:37888
	ds_read_b128 v[186:189], v222 offset:38912
	ds_read_b128 v[190:193], v222 offset:39936
	global_load_lds_dwordx4 v[224:225], off
	v_lshl_add_u64 v[224:225], s[14:15], 0, v[200:201]
	s_mov_b32 m0, s26
	s_nop 0
	global_load_lds_dwordx4 v[224:225], off
	s_waitcnt vmcnt(8)
	s_waitcnt lgkmcnt(0)
	s_barrier
	s_setprio 1
	s_waitcnt lgkmcnt(0)
	v_mfma_f32_16x16x32_bf16 v[126:129], v[130:133], v[162:165], v[126:129]
	v_mfma_f32_16x16x32_bf16 v[122:125], v[138:141], v[162:165], v[122:125]
	v_mfma_f32_16x16x32_bf16 v[118:121], v[130:133], v[170:173], v[118:121]
	v_mfma_f32_16x16x32_bf16 v[114:117], v[138:141], v[170:173], v[114:117]
	v_mfma_f32_16x16x32_bf16 v[102:105], v[130:133], v[178:181], v[102:105]
	v_mfma_f32_16x16x32_bf16 v[98:101], v[138:141], v[178:181], v[98:101]
	v_mfma_f32_16x16x32_bf16 v[86:89], v[130:133], v[186:189], v[86:89]
	v_mfma_f32_16x16x32_bf16 v[82:85], v[138:141], v[186:189], v[82:85]
	v_mfma_f32_16x16x32_bf16 v[126:129], v[134:137], v[166:169], v[126:129]
	v_mfma_f32_16x16x32_bf16 v[122:125], v[142:145], v[166:169], v[122:125]
	v_mfma_f32_16x16x32_bf16 v[118:121], v[134:137], v[174:177], v[118:121]
	v_mfma_f32_16x16x32_bf16 v[114:117], v[142:145], v[174:177], v[114:117]
	v_mfma_f32_16x16x32_bf16 v[102:105], v[134:137], v[182:185], v[102:105]
	v_mfma_f32_16x16x32_bf16 v[98:101], v[142:145], v[182:185], v[98:101]
	v_mfma_f32_16x16x32_bf16 v[86:89], v[134:137], v[190:193], v[86:89]
	v_mfma_f32_16x16x32_bf16 v[82:85], v[142:145], v[190:193], v[82:85]
	s_setprio 0
	s_setprio 1
	v_mfma_f32_16x16x32_bf16 v[110:113], v[146:149], v[162:165], v[110:113]
	v_mfma_f32_16x16x32_bf16 v[106:109], v[154:157], v[162:165], v[106:109]
	v_mfma_f32_16x16x32_bf16 v[94:97], v[146:149], v[170:173], v[94:97]
	v_mfma_f32_16x16x32_bf16 v[90:93], v[154:157], v[170:173], v[90:93]
	v_mfma_f32_16x16x32_bf16 v[78:81], v[146:149], v[178:181], v[78:81]
	v_mfma_f32_16x16x32_bf16 v[74:77], v[154:157], v[178:181], v[74:77]
	v_mfma_f32_16x16x32_bf16 v[70:73], v[146:149], v[186:189], v[70:73]
	v_mfma_f32_16x16x32_bf16 v[66:69], v[154:157], v[186:189], v[66:69]
	v_mfma_f32_16x16x32_bf16 v[110:113], v[150:153], v[166:169], v[110:113]
	v_mfma_f32_16x16x32_bf16 v[106:109], v[158:161], v[166:169], v[106:109]
	v_mfma_f32_16x16x32_bf16 v[94:97], v[150:153], v[174:177], v[94:97]
	v_mfma_f32_16x16x32_bf16 v[90:93], v[158:161], v[174:177], v[90:93]
	v_mfma_f32_16x16x32_bf16 v[78:81], v[150:153], v[182:185], v[78:81]
	v_mfma_f32_16x16x32_bf16 v[74:77], v[158:161], v[182:185], v[74:77]
	v_mfma_f32_16x16x32_bf16 v[70:73], v[150:153], v[190:193], v[70:73]
	v_mfma_f32_16x16x32_bf16 v[66:69], v[158:161], v[190:193], v[66:69]
	s_setprio 0
	s_barrier
	s_mov_b32 m0, s40
	v_lshl_add_u64 v[210:211], v[210:211], 0, s[6:7]
	s_add_u32 s12, s12, 0x80080
	ds_read_b128 v[162:165], v222 offset:49152
	ds_read_b128 v[166:169], v222 offset:50176
	ds_read_b128 v[170:173], v222 offset:51200
	ds_read_b128 v[174:177], v222 offset:52224
	ds_read_b128 v[178:181], v222 offset:53248
	ds_read_b128 v[182:185], v222 offset:54272
	ds_read_b128 v[186:189], v222 offset:55296
	ds_read_b128 v[190:193], v222 offset:56320
	global_load_lds_dwordx4 v[210:211], off
	v_lshl_add_u64 v[210:211], v[212:213], 0, s[6:7]
	s_mov_b32 m0, s41
	s_addc_u32 s13, s13, 0
	global_load_lds_dwordx4 v[210:211], off
	v_lshl_add_u64 v[210:211], s[12:13], 0, v[202:203]
	s_mov_b32 m0, s42
	s_nop 0
	global_load_lds_dwordx4 v[210:211], off
	v_lshl_add_u64 v[210:211], s[12:13], 0, v[198:199]
	s_mov_b32 m0, s43
	s_nop 0
	global_load_lds_dwordx4 v[210:211], off
	v_lshl_add_u64 v[210:211], v[214:215], 0, s[6:7]
	s_mov_b32 m0, s28
	s_nop 0
	global_load_lds_dwordx4 v[210:211], off
	v_lshl_add_u64 v[210:211], v[216:217], 0, s[6:7]
	s_mov_b32 m0, s29
	s_nop 0
	global_load_lds_dwordx4 v[210:211], off
	s_waitcnt vmcnt(8)
	s_waitcnt lgkmcnt(0)
	s_barrier
	s_setprio 1
	s_waitcnt lgkmcnt(0)
	v_mfma_f32_16x16x32_bf16 v[62:65], v[130:133], v[162:165], v[62:65]
	v_mfma_f32_16x16x32_bf16 v[58:61], v[138:141], v[162:165], v[58:61]
	v_mfma_f32_16x16x32_bf16 v[54:57], v[130:133], v[170:173], v[54:57]
	v_mfma_f32_16x16x32_bf16 v[50:53], v[138:141], v[170:173], v[50:53]
	v_mfma_f32_16x16x32_bf16 v[38:41], v[130:133], v[178:181], v[38:41]
	v_mfma_f32_16x16x32_bf16 v[34:37], v[138:141], v[178:181], v[34:37]
	v_mfma_f32_16x16x32_bf16 v[22:25], v[130:133], v[186:189], v[22:25]
	v_mfma_f32_16x16x32_bf16 v[18:21], v[138:141], v[186:189], v[18:21]
	v_mfma_f32_16x16x32_bf16 v[62:65], v[134:137], v[166:169], v[62:65]
	v_mfma_f32_16x16x32_bf16 v[58:61], v[142:145], v[166:169], v[58:61]
	v_mfma_f32_16x16x32_bf16 v[54:57], v[134:137], v[174:177], v[54:57]
	v_mfma_f32_16x16x32_bf16 v[50:53], v[142:145], v[174:177], v[50:53]
	v_mfma_f32_16x16x32_bf16 v[38:41], v[134:137], v[182:185], v[38:41]
	v_mfma_f32_16x16x32_bf16 v[34:37], v[142:145], v[182:185], v[34:37]
	v_mfma_f32_16x16x32_bf16 v[22:25], v[134:137], v[190:193], v[22:25]
	v_mfma_f32_16x16x32_bf16 v[18:21], v[142:145], v[190:193], v[18:21]
	s_setprio 0
	s_setprio 1
	v_mfma_f32_16x16x32_bf16 v[46:49], v[146:149], v[162:165], v[46:49]
	v_mfma_f32_16x16x32_bf16 v[42:45], v[154:157], v[162:165], v[42:45]
	v_mfma_f32_16x16x32_bf16 v[30:33], v[146:149], v[170:173], v[30:33]
	v_mfma_f32_16x16x32_bf16 v[26:29], v[154:157], v[170:173], v[26:29]
	v_mfma_f32_16x16x32_bf16 v[14:17], v[146:149], v[178:181], v[14:17]
	v_mfma_f32_16x16x32_bf16 v[10:13], v[154:157], v[178:181], v[10:13]
	v_mfma_f32_16x16x32_bf16 v[6:9], v[146:149], v[186:189], v[6:9]
	v_mfma_f32_16x16x32_bf16 v[2:5], v[154:157], v[186:189], v[2:5]
	v_mfma_f32_16x16x32_bf16 v[46:49], v[150:153], v[166:169], v[46:49]
	v_mfma_f32_16x16x32_bf16 v[42:45], v[158:161], v[166:169], v[42:45]
	v_mfma_f32_16x16x32_bf16 v[30:33], v[150:153], v[174:177], v[30:33]
	v_mfma_f32_16x16x32_bf16 v[26:29], v[158:161], v[174:177], v[26:29]
	v_mfma_f32_16x16x32_bf16 v[14:17], v[150:153], v[182:185], v[14:17]
	v_mfma_f32_16x16x32_bf16 v[10:13], v[158:161], v[182:185], v[10:13]
	v_mfma_f32_16x16x32_bf16 v[6:9], v[150:153], v[190:193], v[6:9]
	v_mfma_f32_16x16x32_bf16 v[2:5], v[158:161], v[190:193], v[2:5]
	s_setprio 0
	s_barrier
	s_add_i32 s33, s33, 2
	s_add_u32 s10, s10, 0x100
	s_addc_u32 s11, s11, 0
	s_cmp_gt_u32 s33, 29
	s_cbranch_scc1 .LBB0_270

.LBB0_490:
	s_setprio 0
	s_barrier
	s_add_i32 s38, 0, 0x18000
	s_add_i32 s39, 0, 0x1c000
	v_add_u32_e32 v142, s38, v244
	v_add_u32_e32 v158, s39, v244
	ds_read_b128 v[130:133], v142
	ds_read_b128 v[134:137], v142 offset:1024
	ds_read_b128 v[138:141], v142 offset:2048
	ds_read_b128 v[142:145], v142 offset:3072
	ds_read_b128 v[146:149], v158
	ds_read_b128 v[150:153], v158 offset:1024
	ds_read_b128 v[154:157], v158 offset:2048
	ds_read_b128 v[158:161], v158 offset:3072
	s_add_u32 s34, s34, 0x80000
	s_addc_u32 s35, s35, 0
	s_mov_b32 m0, s64
	v_lshl_add_u64 v[234:235], s[34:35], 0, v[198:199]
	ds_read_b128 v[162:165], v247 offset:32768
	ds_read_b128 v[166:169], v247 offset:33792
	ds_read_b128 v[170:173], v247 offset:34816
	ds_read_b128 v[174:177], v247 offset:35840
	ds_read_b128 v[178:181], v247 offset:36864
	ds_read_b128 v[182:185], v247 offset:37888
	ds_read_b128 v[186:189], v247 offset:38912
	ds_read_b128 v[190:193], v247 offset:39936
	global_load_lds_dwordx4 v[234:235], off
	v_lshl_add_u64 v[234:235], s[34:35], 0, v[202:203]
	s_mov_b32 m0, s65
	s_nop 0
	global_load_lds_dwordx4 v[234:235], off
	s_waitcnt vmcnt(8)
	s_waitcnt lgkmcnt(0)
	s_barrier
	s_setprio 1
	s_waitcnt lgkmcnt(0)
	v_mfma_f32_16x16x32_bf16 v[126:129], v[130:133], v[162:165], v[126:129]
	v_mfma_f32_16x16x32_bf16 v[122:125], v[138:141], v[162:165], v[122:125]
	v_mfma_f32_16x16x32_bf16 v[118:121], v[130:133], v[170:173], v[118:121]
	v_mfma_f32_16x16x32_bf16 v[114:117], v[138:141], v[170:173], v[114:117]
	v_mfma_f32_16x16x32_bf16 v[110:113], v[130:133], v[178:181], v[110:113]
	v_mfma_f32_16x16x32_bf16 v[106:109], v[138:141], v[178:181], v[106:109]
	v_mfma_f32_16x16x32_bf16 v[102:105], v[130:133], v[186:189], v[102:105]
	v_mfma_f32_16x16x32_bf16 v[98:101], v[138:141], v[186:189], v[98:101]
	v_mfma_f32_16x16x32_bf16 v[126:129], v[134:137], v[166:169], v[126:129]
	v_mfma_f32_16x16x32_bf16 v[122:125], v[142:145], v[166:169], v[122:125]
	v_mfma_f32_16x16x32_bf16 v[118:121], v[134:137], v[174:177], v[118:121]
	v_mfma_f32_16x16x32_bf16 v[114:117], v[142:145], v[174:177], v[114:117]
	v_mfma_f32_16x16x32_bf16 v[110:113], v[134:137], v[182:185], v[110:113]
	v_mfma_f32_16x16x32_bf16 v[106:109], v[142:145], v[182:185], v[106:109]
	v_mfma_f32_16x16x32_bf16 v[102:105], v[134:137], v[190:193], v[102:105]
	v_mfma_f32_16x16x32_bf16 v[98:101], v[142:145], v[190:193], v[98:101]
	s_setprio 0
	s_setprio 1
	v_mfma_f32_16x16x32_bf16 v[94:97], v[146:149], v[162:165], v[94:97]
	v_mfma_f32_16x16x32_bf16 v[90:93], v[154:157], v[162:165], v[90:93]
	v_mfma_f32_16x16x32_bf16 v[86:89], v[146:149], v[170:173], v[86:89]
	v_mfma_f32_16x16x32_bf16 v[82:85], v[154:157], v[170:173], v[82:85]
	v_mfma_f32_16x16x32_bf16 v[78:81], v[146:149], v[178:181], v[78:81]
	v_mfma_f32_16x16x32_bf16 v[74:77], v[154:157], v[178:181], v[74:77]
	v_mfma_f32_16x16x32_bf16 v[70:73], v[146:149], v[186:189], v[70:73]
	v_mfma_f32_16x16x32_bf16 v[66:69], v[154:157], v[186:189], v[66:69]
	v_mfma_f32_16x16x32_bf16 v[94:97], v[150:153], v[166:169], v[94:97]
	v_mfma_f32_16x16x32_bf16 v[90:93], v[158:161], v[166:169], v[90:93]
	v_mfma_f32_16x16x32_bf16 v[86:89], v[150:153], v[174:177], v[86:89]
	v_mfma_f32_16x16x32_bf16 v[82:85], v[158:161], v[174:177], v[82:85]
	v_mfma_f32_16x16x32_bf16 v[78:81], v[150:153], v[182:185], v[78:81]
	v_mfma_f32_16x16x32_bf16 v[74:77], v[158:161], v[182:185], v[74:77]
	v_mfma_f32_16x16x32_bf16 v[70:73], v[150:153], v[190:193], v[70:73]
	v_mfma_f32_16x16x32_bf16 v[66:69], v[158:161], v[190:193], v[66:69]
	s_setprio 0
	s_barrier
	s_add_i32 s34, s38, s57
	v_lshl_add_u64 v[224:225], v[224:225], 0, s[18:19]
	s_mov_b32 m0, s34
	ds_read_b128 v[162:165], v247 offset:49152
	ds_read_b128 v[166:169], v247 offset:50176
	ds_read_b128 v[170:173], v247 offset:51200
	ds_read_b128 v[174:177], v247 offset:52224
	ds_read_b128 v[178:181], v247 offset:53248
	ds_read_b128 v[182:185], v247 offset:54272
	ds_read_b128 v[186:189], v247 offset:55296
	ds_read_b128 v[190:193], v247 offset:56320
	global_load_lds_dwordx4 v[224:225], off
	s_add_i32 m0, s34, 0x2000
	s_add_u32 s30, s30, 0x80080
	v_lshl_add_u64 v[222:223], v[222:223], 0, s[18:19]
	s_addc_u32 s31, s31, 0
	s_add_i32 s34, s39, s57
	global_load_lds_dwordx4 v[222:223], off
	v_lshl_add_u64 v[222:223], s[30:31], 0, v[200:201]
	s_mov_b32 m0, s34
	v_lshl_add_u64 v[218:219], v[218:219], 0, s[18:19]
	global_load_lds_dwordx4 v[222:223], off
	v_lshl_add_u64 v[222:223], s[30:31], 0, v[204:205]
	s_add_i32 m0, s34, 0x2000
	s_nop 0
	global_load_lds_dwordx4 v[222:223], off
	s_mov_b32 m0, s68
	s_nop 0
	global_load_lds_dwordx4 v[218:219], off
	v_lshl_add_u64 v[218:219], v[220:221], 0, s[18:19]
	s_mov_b32 m0, s69
	s_nop 0
	global_load_lds_dwordx4 v[218:219], off
	s_waitcnt vmcnt(8)
	s_waitcnt lgkmcnt(0)
	s_barrier
	s_setprio 1
	s_waitcnt lgkmcnt(0)
	v_mfma_f32_16x16x32_bf16 v[62:65], v[130:133], v[162:165], v[62:65]
	v_mfma_f32_16x16x32_bf16 v[58:61], v[138:141], v[162:165], v[58:61]
	v_mfma_f32_16x16x32_bf16 v[54:57], v[130:133], v[170:173], v[54:57]
	v_mfma_f32_16x16x32_bf16 v[50:53], v[138:141], v[170:173], v[50:53]
	v_mfma_f32_16x16x32_bf16 v[46:49], v[130:133], v[178:181], v[46:49]
	v_mfma_f32_16x16x32_bf16 v[42:45], v[138:141], v[178:181], v[42:45]
	v_mfma_f32_16x16x32_bf16 v[38:41], v[130:133], v[186:189], v[38:41]
	v_mfma_f32_16x16x32_bf16 v[34:37], v[138:141], v[186:189], v[34:37]
	v_mfma_f32_16x16x32_bf16 v[62:65], v[134:137], v[166:169], v[62:65]
	v_mfma_f32_16x16x32_bf16 v[58:61], v[142:145], v[166:169], v[58:61]
	v_mfma_f32_16x16x32_bf16 v[54:57], v[134:137], v[174:177], v[54:57]
	v_mfma_f32_16x16x32_bf16 v[50:53], v[142:145], v[174:177], v[50:53]
	v_mfma_f32_16x16x32_bf16 v[46:49], v[134:137], v[182:185], v[46:49]
	v_mfma_f32_16x16x32_bf16 v[42:45], v[142:145], v[182:185], v[42:45]
	v_mfma_f32_16x16x32_bf16 v[38:41], v[134:137], v[190:193], v[38:41]
	v_mfma_f32_16x16x32_bf16 v[34:37], v[142:145], v[190:193], v[34:37]
	s_setprio 0
	s_setprio 1
	v_mfma_f32_16x16x32_bf16 v[30:33], v[146:149], v[162:165], v[30:33]
	v_mfma_f32_16x16x32_bf16 v[26:29], v[154:157], v[162:165], v[26:29]
	v_mfma_f32_16x16x32_bf16 v[22:25], v[146:149], v[170:173], v[22:25]
	v_mfma_f32_16x16x32_bf16 v[18:21], v[154:157], v[170:173], v[18:21]
	v_mfma_f32_16x16x32_bf16 v[14:17], v[146:149], v[178:181], v[14:17]
	v_mfma_f32_16x16x32_bf16 v[10:13], v[154:157], v[178:181], v[10:13]
	v_mfma_f32_16x16x32_bf16 v[6:9], v[146:149], v[186:189], v[6:9]
	v_mfma_f32_16x16x32_bf16 v[2:5], v[154:157], v[186:189], v[2:5]
	v_mfma_f32_16x16x32_bf16 v[30:33], v[150:153], v[166:169], v[30:33]
	v_mfma_f32_16x16x32_bf16 v[26:29], v[158:161], v[166:169], v[26:29]
	v_mfma_f32_16x16x32_bf16 v[22:25], v[150:153], v[174:177], v[22:25]
	v_mfma_f32_16x16x32_bf16 v[18:21], v[158:161], v[174:177], v[18:21]
	v_mfma_f32_16x16x32_bf16 v[14:17], v[150:153], v[182:185], v[14:17]
	v_mfma_f32_16x16x32_bf16 v[10:13], v[158:161], v[182:185], v[10:13]
	v_mfma_f32_16x16x32_bf16 v[6:9], v[150:153], v[190:193], v[6:9]
	v_mfma_f32_16x16x32_bf16 v[2:5], v[158:161], v[190:193], v[2:5]
	s_setprio 0
	s_barrier
	s_add_i32 s73, s73, 2
	s_add_u32 s28, s28, 0x100
	s_addc_u32 s29, s29, 0
	s_cmp_gt_u32 s73, 29
	s_cbranch_scc1 .LBB0_498

.LBB0_529:
	s_setprio 0
	s_barrier
	v_add_u32_e32 v142, s38, v243
	v_add_u32_e32 v158, s39, v243
	ds_read_b128 v[130:133], v142
	ds_read_b128 v[134:137], v142 offset:1024
	ds_read_b128 v[138:141], v142 offset:2048
	ds_read_b128 v[142:145], v142 offset:3072
	ds_read_b128 v[146:149], v158
	ds_read_b128 v[150:153], v158 offset:1024
	ds_read_b128 v[154:157], v158 offset:2048
	ds_read_b128 v[158:161], v158 offset:3072
	s_add_u32 s24, s24, 0x80000
	s_addc_u32 s25, s25, 0
	s_mov_b32 m0, s60
	v_lshl_add_u64 v[232:233], s[24:25], 0, v[198:199]
	ds_read_b128 v[162:165], v246 offset:32768
	ds_read_b128 v[166:169], v246 offset:33792
	ds_read_b128 v[170:173], v246 offset:34816
	ds_read_b128 v[174:177], v246 offset:35840
	ds_read_b128 v[178:181], v246 offset:36864
	ds_read_b128 v[182:185], v246 offset:37888
	ds_read_b128 v[186:189], v246 offset:38912
	ds_read_b128 v[190:193], v246 offset:39936
	global_load_lds_dwordx4 v[232:233], off
	v_lshl_add_u64 v[232:233], s[24:25], 0, v[202:203]
	s_mov_b32 m0, s61
	s_nop 0
	global_load_lds_dwordx4 v[232:233], off
	s_waitcnt vmcnt(8)
	s_waitcnt lgkmcnt(0)
	s_barrier
	s_setprio 1
	s_waitcnt lgkmcnt(0)
	v_mfma_f32_16x16x32_bf16 v[126:129], v[130:133], v[162:165], v[126:129]
	v_mfma_f32_16x16x32_bf16 v[122:125], v[138:141], v[162:165], v[122:125]
	v_mfma_f32_16x16x32_bf16 v[118:121], v[130:133], v[170:173], v[118:121]
	v_mfma_f32_16x16x32_bf16 v[114:117], v[138:141], v[170:173], v[114:117]
	v_mfma_f32_16x16x32_bf16 v[102:105], v[130:133], v[178:181], v[102:105]
	v_mfma_f32_16x16x32_bf16 v[98:101], v[138:141], v[178:181], v[98:101]
	v_mfma_f32_16x16x32_bf16 v[86:89], v[130:133], v[186:189], v[86:89]
	v_mfma_f32_16x16x32_bf16 v[82:85], v[138:141], v[186:189], v[82:85]
	v_mfma_f32_16x16x32_bf16 v[126:129], v[134:137], v[166:169], v[126:129]
	v_mfma_f32_16x16x32_bf16 v[122:125], v[142:145], v[166:169], v[122:125]
	v_mfma_f32_16x16x32_bf16 v[118:121], v[134:137], v[174:177], v[118:121]
	v_mfma_f32_16x16x32_bf16 v[114:117], v[142:145], v[174:177], v[114:117]
	v_mfma_f32_16x16x32_bf16 v[102:105], v[134:137], v[182:185], v[102:105]
	v_mfma_f32_16x16x32_bf16 v[98:101], v[142:145], v[182:185], v[98:101]
	v_mfma_f32_16x16x32_bf16 v[86:89], v[134:137], v[190:193], v[86:89]
	v_mfma_f32_16x16x32_bf16 v[82:85], v[142:145], v[190:193], v[82:85]
	s_setprio 0
	s_setprio 1
	v_mfma_f32_16x16x32_bf16 v[110:113], v[146:149], v[162:165], v[110:113]
	v_mfma_f32_16x16x32_bf16 v[106:109], v[154:157], v[162:165], v[106:109]
	v_mfma_f32_16x16x32_bf16 v[94:97], v[146:149], v[170:173], v[94:97]
	v_mfma_f32_16x16x32_bf16 v[90:93], v[154:157], v[170:173], v[90:93]
	v_mfma_f32_16x16x32_bf16 v[78:81], v[146:149], v[178:181], v[78:81]
	v_mfma_f32_16x16x32_bf16 v[74:77], v[154:157], v[178:181], v[74:77]
	v_mfma_f32_16x16x32_bf16 v[70:73], v[146:149], v[186:189], v[70:73]
	v_mfma_f32_16x16x32_bf16 v[66:69], v[154:157], v[186:189], v[66:69]
	v_mfma_f32_16x16x32_bf16 v[110:113], v[150:153], v[166:169], v[110:113]
	v_mfma_f32_16x16x32_bf16 v[106:109], v[158:161], v[166:169], v[106:109]
	v_mfma_f32_16x16x32_bf16 v[94:97], v[150:153], v[174:177], v[94:97]
	v_mfma_f32_16x16x32_bf16 v[90:93], v[158:161], v[174:177], v[90:93]
	v_mfma_f32_16x16x32_bf16 v[78:81], v[150:153], v[182:185], v[78:81]
	v_mfma_f32_16x16x32_bf16 v[74:77], v[158:161], v[182:185], v[74:77]
	v_mfma_f32_16x16x32_bf16 v[70:73], v[150:153], v[190:193], v[70:73]
	v_mfma_f32_16x16x32_bf16 v[66:69], v[158:161], v[190:193], v[66:69]
	s_setprio 0
	s_barrier
	s_add_i32 s24, s38, s31
	v_lshl_add_u64 v[224:225], v[224:225], 0, s[12:13]
	s_mov_b32 m0, s24
	ds_read_b128 v[162:165], v246 offset:49152
	ds_read_b128 v[166:169], v246 offset:50176
	ds_read_b128 v[170:173], v246 offset:51200
	ds_read_b128 v[174:177], v246 offset:52224
	ds_read_b128 v[178:181], v246 offset:53248
	ds_read_b128 v[182:185], v246 offset:54272
	ds_read_b128 v[186:189], v246 offset:55296
	ds_read_b128 v[190:193], v246 offset:56320
	global_load_lds_dwordx4 v[224:225], off
	s_add_i32 m0, s24, 0x2000
	s_add_u32 s22, s22, 0x80080
	v_lshl_add_u64 v[222:223], v[222:223], 0, s[12:13]
	s_addc_u32 s23, s23, 0
	s_add_i32 s24, s39, s31
	global_load_lds_dwordx4 v[222:223], off
	v_lshl_add_u64 v[222:223], s[22:23], 0, v[200:201]
	s_mov_b32 m0, s24
	v_lshl_add_u64 v[218:219], v[218:219], 0, s[12:13]
	global_load_lds_dwordx4 v[222:223], off
	v_lshl_add_u64 v[222:223], s[22:23], 0, v[204:205]
	s_add_i32 m0, s24, 0x2000
	s_nop 0
	global_load_lds_dwordx4 v[222:223], off
	s_mov_b32 m0, s65
	s_nop 0
	global_load_lds_dwordx4 v[218:219], off
	v_lshl_add_u64 v[218:219], v[220:221], 0, s[12:13]
	s_mov_b32 m0, s66
	s_nop 0
	global_load_lds_dwordx4 v[218:219], off
	s_waitcnt vmcnt(8)
	s_waitcnt lgkmcnt(0)
	s_barrier
	s_setprio 1
	s_waitcnt lgkmcnt(0)
	v_mfma_f32_16x16x32_bf16 v[62:65], v[130:133], v[162:165], v[62:65]
	v_mfma_f32_16x16x32_bf16 v[58:61], v[138:141], v[162:165], v[58:61]
	v_mfma_f32_16x16x32_bf16 v[54:57], v[130:133], v[170:173], v[54:57]
	v_mfma_f32_16x16x32_bf16 v[50:53], v[138:141], v[170:173], v[50:53]
	v_mfma_f32_16x16x32_bf16 v[38:41], v[130:133], v[178:181], v[38:41]
	v_mfma_f32_16x16x32_bf16 v[34:37], v[138:141], v[178:181], v[34:37]
	v_mfma_f32_16x16x32_bf16 v[22:25], v[130:133], v[186:189], v[22:25]
	v_mfma_f32_16x16x32_bf16 v[18:21], v[138:141], v[186:189], v[18:21]
	v_mfma_f32_16x16x32_bf16 v[62:65], v[134:137], v[166:169], v[62:65]
	v_mfma_f32_16x16x32_bf16 v[58:61], v[142:145], v[166:169], v[58:61]
	v_mfma_f32_16x16x32_bf16 v[54:57], v[134:137], v[174:177], v[54:57]
	v_mfma_f32_16x16x32_bf16 v[50:53], v[142:145], v[174:177], v[50:53]
	v_mfma_f32_16x16x32_bf16 v[38:41], v[134:137], v[182:185], v[38:41]
	v_mfma_f32_16x16x32_bf16 v[34:37], v[142:145], v[182:185], v[34:37]
	v_mfma_f32_16x16x32_bf16 v[22:25], v[134:137], v[190:193], v[22:25]
	v_mfma_f32_16x16x32_bf16 v[18:21], v[142:145], v[190:193], v[18:21]
	s_setprio 0
	s_setprio 1
	v_mfma_f32_16x16x32_bf16 v[46:49], v[146:149], v[162:165], v[46:49]
	v_mfma_f32_16x16x32_bf16 v[42:45], v[154:157], v[162:165], v[42:45]
	v_mfma_f32_16x16x32_bf16 v[30:33], v[146:149], v[170:173], v[30:33]
	v_mfma_f32_16x16x32_bf16 v[26:29], v[154:157], v[170:173], v[26:29]
	v_mfma_f32_16x16x32_bf16 v[14:17], v[146:149], v[178:181], v[14:17]
	v_mfma_f32_16x16x32_bf16 v[10:13], v[154:157], v[178:181], v[10:13]
	v_mfma_f32_16x16x32_bf16 v[6:9], v[146:149], v[186:189], v[6:9]
	v_mfma_f32_16x16x32_bf16 v[2:5], v[154:157], v[186:189], v[2:5]
	v_mfma_f32_16x16x32_bf16 v[46:49], v[150:153], v[166:169], v[46:49]
	v_mfma_f32_16x16x32_bf16 v[42:45], v[158:161], v[166:169], v[42:45]
	v_mfma_f32_16x16x32_bf16 v[30:33], v[150:153], v[174:177], v[30:33]
	v_mfma_f32_16x16x32_bf16 v[26:29], v[158:161], v[174:177], v[26:29]
	v_mfma_f32_16x16x32_bf16 v[14:17], v[150:153], v[182:185], v[14:17]
	v_mfma_f32_16x16x32_bf16 v[10:13], v[158:161], v[182:185], v[10:13]
	v_mfma_f32_16x16x32_bf16 v[6:9], v[150:153], v[190:193], v[6:9]
	v_mfma_f32_16x16x32_bf16 v[2:5], v[158:161], v[190:193], v[2:5]
	s_setprio 0
	s_barrier
	s_add_i32 s67, s67, 2
	s_add_u32 s20, s20, 0x100
	s_addc_u32 s21, s21, 0
	s_cmp_gt_u32 s67, 5
	s_cbranch_scc1 .LBB0_537
.LBB0_530:
	ds_read_b128 v[146:149], v244
	ds_read_b128 v[150:153], v244 offset:1024
	ds_read_b128 v[154:157], v244 offset:2048
	ds_read_b128 v[158:161], v244 offset:3072
	ds_read_b128 v[130:133], v245
	ds_read_b128 v[134:137], v245 offset:1024
	ds_read_b128 v[138:141], v245 offset:2048
	ds_read_b128 v[142:145], v245 offset:3072
	v_lshl_add_u64 v[218:219], v[214:215], 0, s[20:21]
	s_add_i32 m0, s33, 0xc000
	ds_read_b128 v[186:189], v246
	ds_read_b128 v[190:193], v246 offset:1024
	ds_read_b128 v[178:181], v246 offset:2048
	ds_read_b128 v[182:185], v246 offset:3072
	ds_read_b128 v[170:173], v246 offset:4096
	ds_read_b128 v[174:177], v246 offset:5120
	ds_read_b128 v[162:165], v246 offset:6144
	ds_read_b128 v[166:169], v246 offset:7168
	global_load_lds_dwordx4 v[218:219], off
	v_lshl_add_u64 v[218:219], v[216:217], 0, s[20:21]
	s_add_i32 m0, s33, 0xe000
	s_cmp_lg_u32 s20, 0
	global_load_lds_dwordx4 v[218:219], off
	s_waitcnt vmcnt(8)
	s_waitcnt lgkmcnt(0)
	s_cselect_b64 s[26:27], -1, 0
	s_barrier
	s_setprio 1
	s_and_b64 vcc, exec, s[26:27]
	s_cbranch_vccz .LBB0_535
	s_waitcnt lgkmcnt(0)
	v_mfma_f32_16x16x32_bf16 v[126:129], v[146:149], v[186:189], v[126:129]
	v_mfma_f32_16x16x32_bf16 v[122:125], v[154:157], v[186:189], v[122:125]
	v_mfma_f32_16x16x32_bf16 v[118:121], v[146:149], v[178:181], v[118:121]
	v_mfma_f32_16x16x32_bf16 v[114:117], v[154:157], v[178:181], v[114:117]
	v_mfma_f32_16x16x32_bf16 v[102:105], v[146:149], v[170:173], v[102:105]
	v_mfma_f32_16x16x32_bf16 v[98:101], v[154:157], v[170:173], v[98:101]
	v_mfma_f32_16x16x32_bf16 v[86:89], v[146:149], v[162:165], v[86:89]
	v_mfma_f32_16x16x32_bf16 v[82:85], v[154:157], v[162:165], v[82:85]
	v_mfma_f32_16x16x32_bf16 v[126:129], v[150:153], v[190:193], v[126:129]
	v_mfma_f32_16x16x32_bf16 v[122:125], v[158:161], v[190:193], v[122:125]
	v_mfma_f32_16x16x32_bf16 v[118:121], v[150:153], v[182:185], v[118:121]
	v_mfma_f32_16x16x32_bf16 v[114:117], v[158:161], v[182:185], v[114:117]
	v_mfma_f32_16x16x32_bf16 v[102:105], v[150:153], v[174:177], v[102:105]
	v_mfma_f32_16x16x32_bf16 v[98:101], v[158:161], v[174:177], v[98:101]
	v_mfma_f32_16x16x32_bf16 v[86:89], v[150:153], v[166:169], v[86:89]
	v_mfma_f32_16x16x32_bf16 v[82:85], v[158:161], v[166:169], v[82:85]
	s_setprio 0
	s_setprio 1
	v_mfma_f32_16x16x32_bf16 v[110:113], v[130:133], v[186:189], v[110:113]
	v_mfma_f32_16x16x32_bf16 v[106:109], v[138:141], v[186:189], v[106:109]
	v_mfma_f32_16x16x32_bf16 v[94:97], v[130:133], v[178:181], v[94:97]
	v_mfma_f32_16x16x32_bf16 v[90:93], v[138:141], v[178:181], v[90:93]
	v_mfma_f32_16x16x32_bf16 v[78:81], v[130:133], v[170:173], v[78:81]
	v_mfma_f32_16x16x32_bf16 v[74:77], v[138:141], v[170:173], v[74:77]
	v_mfma_f32_16x16x32_bf16 v[70:73], v[130:133], v[162:165], v[70:73]
	v_mfma_f32_16x16x32_bf16 v[66:69], v[138:141], v[162:165], v[66:69]
	v_mfma_f32_16x16x32_bf16 v[110:113], v[134:137], v[190:193], v[110:113]
	v_mfma_f32_16x16x32_bf16 v[106:109], v[142:145], v[190:193], v[106:109]
	v_mfma_f32_16x16x32_bf16 v[94:97], v[134:137], v[182:185], v[94:97]
	v_mfma_f32_16x16x32_bf16 v[90:93], v[142:145], v[182:185], v[90:93]
	v_mfma_f32_16x16x32_bf16 v[78:81], v[134:137], v[174:177], v[78:81]
	v_mfma_f32_16x16x32_bf16 v[74:77], v[142:145], v[174:177], v[74:77]
	v_mfma_f32_16x16x32_bf16 v[70:73], v[134:137], v[166:169], v[70:73]
	v_mfma_f32_16x16x32_bf16 v[66:69], v[142:145], v[166:169], v[66:69]
	s_cbranch_execnz .LBB0_533

.LBB0_553:
	s_add_i32 s60, s60, 2
	s_setprio 0
	s_barrier
	s_add_i32 s38, 0, 0x18000
	s_add_i32 s39, 0, 0x1c000
	v_add_u32_e32 v142, s38, v238
	v_add_u32_e32 v158, s39, v238
	ds_read_b128 v[130:133], v142
	ds_read_b128 v[134:137], v142 offset:1024
	ds_read_b128 v[138:141], v142 offset:2048
	ds_read_b128 v[142:145], v142 offset:3072
	ds_read_b128 v[146:149], v158
	ds_read_b128 v[150:153], v158 offset:1024
	ds_read_b128 v[154:157], v158 offset:2048
	ds_read_b128 v[158:161], v158 offset:3072
	s_add_u32 s34, s34, 0x80000
	s_addc_u32 s35, s35, 0
	s_mov_b32 m0, s56
	v_lshl_add_u64 v[228:229], s[34:35], 0, v[198:199]
	ds_read_b128 v[162:165], v197 offset:32768
	ds_read_b128 v[166:169], v197 offset:33792
	ds_read_b128 v[170:173], v197 offset:34816
	ds_read_b128 v[174:177], v197 offset:35840
	ds_read_b128 v[178:181], v197 offset:36864
	ds_read_b128 v[182:185], v197 offset:37888
	ds_read_b128 v[186:189], v197 offset:38912
	ds_read_b128 v[190:193], v197 offset:39936
	global_load_lds_dwordx4 v[228:229], off
	v_lshl_add_u64 v[228:229], s[34:35], 0, v[202:203]
	s_mov_b32 m0, s57
	s_nop 0
	global_load_lds_dwordx4 v[228:229], off
	s_waitcnt vmcnt(8)
	s_waitcnt lgkmcnt(0)
	s_barrier
	s_setprio 1
	s_waitcnt lgkmcnt(0)
	v_mfma_f32_16x16x32_bf16 v[126:129], v[130:133], v[162:165], v[126:129]
	v_mfma_f32_16x16x32_bf16 v[122:125], v[138:141], v[162:165], v[122:125]
	v_mfma_f32_16x16x32_bf16 v[118:121], v[130:133], v[170:173], v[118:121]
	v_mfma_f32_16x16x32_bf16 v[114:117], v[138:141], v[170:173], v[114:117]
	v_mfma_f32_16x16x32_bf16 v[110:113], v[130:133], v[178:181], v[110:113]
	v_mfma_f32_16x16x32_bf16 v[106:109], v[138:141], v[178:181], v[106:109]
	v_mfma_f32_16x16x32_bf16 v[102:105], v[130:133], v[186:189], v[102:105]
	v_mfma_f32_16x16x32_bf16 v[98:101], v[138:141], v[186:189], v[98:101]
	v_mfma_f32_16x16x32_bf16 v[126:129], v[134:137], v[166:169], v[126:129]
	v_mfma_f32_16x16x32_bf16 v[122:125], v[142:145], v[166:169], v[122:125]
	v_mfma_f32_16x16x32_bf16 v[118:121], v[134:137], v[174:177], v[118:121]
	v_mfma_f32_16x16x32_bf16 v[114:117], v[142:145], v[174:177], v[114:117]
	v_mfma_f32_16x16x32_bf16 v[110:113], v[134:137], v[182:185], v[110:113]
	v_mfma_f32_16x16x32_bf16 v[106:109], v[142:145], v[182:185], v[106:109]
	v_mfma_f32_16x16x32_bf16 v[102:105], v[134:137], v[190:193], v[102:105]
	v_mfma_f32_16x16x32_bf16 v[98:101], v[142:145], v[190:193], v[98:101]
	s_setprio 0
	s_setprio 1
	v_mfma_f32_16x16x32_bf16 v[94:97], v[146:149], v[162:165], v[94:97]
	v_mfma_f32_16x16x32_bf16 v[90:93], v[154:157], v[162:165], v[90:93]
	v_mfma_f32_16x16x32_bf16 v[86:89], v[146:149], v[170:173], v[86:89]
	v_mfma_f32_16x16x32_bf16 v[82:85], v[154:157], v[170:173], v[82:85]
	v_mfma_f32_16x16x32_bf16 v[78:81], v[146:149], v[178:181], v[78:81]
	v_mfma_f32_16x16x32_bf16 v[74:77], v[154:157], v[178:181], v[74:77]
	v_mfma_f32_16x16x32_bf16 v[70:73], v[146:149], v[186:189], v[70:73]
	v_mfma_f32_16x16x32_bf16 v[66:69], v[154:157], v[186:189], v[66:69]
	v_mfma_f32_16x16x32_bf16 v[94:97], v[150:153], v[166:169], v[94:97]
	v_mfma_f32_16x16x32_bf16 v[90:93], v[158:161], v[166:169], v[90:93]
	v_mfma_f32_16x16x32_bf16 v[86:89], v[150:153], v[174:177], v[86:89]
	v_mfma_f32_16x16x32_bf16 v[82:85], v[158:161], v[174:177], v[82:85]
	v_mfma_f32_16x16x32_bf16 v[78:81], v[150:153], v[182:185], v[78:81]
	v_mfma_f32_16x16x32_bf16 v[74:77], v[158:161], v[182:185], v[74:77]
	v_mfma_f32_16x16x32_bf16 v[70:73], v[150:153], v[190:193], v[70:73]
	v_mfma_f32_16x16x32_bf16 v[66:69], v[158:161], v[190:193], v[66:69]
	s_setprio 0
	s_barrier
	s_add_i32 s34, s38, s33
	v_lshl_add_u64 v[226:227], v[226:227], 0, s[12:13]
	s_mov_b32 m0, s34
	ds_read_b128 v[162:165], v197 offset:49152
	ds_read_b128 v[166:169], v197 offset:50176
	ds_read_b128 v[170:173], v197 offset:51200
	ds_read_b128 v[174:177], v197 offset:52224
	ds_read_b128 v[178:181], v197 offset:53248
	ds_read_b128 v[182:185], v197 offset:54272
	ds_read_b128 v[186:189], v197 offset:55296
	ds_read_b128 v[190:193], v197 offset:56320
	global_load_lds_dwordx4 v[226:227], off
	s_add_i32 m0, s34, 0x2000
	s_add_u32 s30, s30, 0x80080
	v_lshl_add_u64 v[224:225], v[224:225], 0, s[12:13]
	s_addc_u32 s31, s31, 0
	s_add_i32 s34, s39, s33
	global_load_lds_dwordx4 v[224:225], off
	v_lshl_add_u64 v[224:225], s[30:31], 0, v[200:201]
	s_mov_b32 m0, s34
	v_lshl_add_u64 v[220:221], v[220:221], 0, s[12:13]
	global_load_lds_dwordx4 v[224:225], off
	v_lshl_add_u64 v[224:225], s[30:31], 0, v[204:205]
	s_add_i32 m0, s34, 0x2000
	s_nop 0
	global_load_lds_dwordx4 v[224:225], off
	s_mov_b32 m0, s42
	s_nop 0
	global_load_lds_dwordx4 v[220:221], off
	v_lshl_add_u64 v[220:221], v[222:223], 0, s[12:13]
	s_mov_b32 m0, s43
	s_nop 0
	global_load_lds_dwordx4 v[220:221], off
	s_waitcnt vmcnt(8)
	s_waitcnt lgkmcnt(0)
	s_barrier
	s_setprio 1
	s_waitcnt lgkmcnt(0)
	v_mfma_f32_16x16x32_bf16 v[62:65], v[130:133], v[162:165], v[62:65]
	v_mfma_f32_16x16x32_bf16 v[58:61], v[138:141], v[162:165], v[58:61]
	v_mfma_f32_16x16x32_bf16 v[54:57], v[130:133], v[170:173], v[54:57]
	v_mfma_f32_16x16x32_bf16 v[50:53], v[138:141], v[170:173], v[50:53]
	v_mfma_f32_16x16x32_bf16 v[46:49], v[130:133], v[178:181], v[46:49]
	v_mfma_f32_16x16x32_bf16 v[42:45], v[138:141], v[178:181], v[42:45]
	v_mfma_f32_16x16x32_bf16 v[38:41], v[130:133], v[186:189], v[38:41]
	v_mfma_f32_16x16x32_bf16 v[34:37], v[138:141], v[186:189], v[34:37]
	v_mfma_f32_16x16x32_bf16 v[62:65], v[134:137], v[166:169], v[62:65]
	v_mfma_f32_16x16x32_bf16 v[58:61], v[142:145], v[166:169], v[58:61]
	v_mfma_f32_16x16x32_bf16 v[54:57], v[134:137], v[174:177], v[54:57]
	v_mfma_f32_16x16x32_bf16 v[50:53], v[142:145], v[174:177], v[50:53]
	v_mfma_f32_16x16x32_bf16 v[46:49], v[134:137], v[182:185], v[46:49]
	v_mfma_f32_16x16x32_bf16 v[42:45], v[142:145], v[182:185], v[42:45]
	v_mfma_f32_16x16x32_bf16 v[38:41], v[134:137], v[190:193], v[38:41]
	v_mfma_f32_16x16x32_bf16 v[34:37], v[142:145], v[190:193], v[34:37]
	s_setprio 0
	s_setprio 1
	v_mfma_f32_16x16x32_bf16 v[30:33], v[146:149], v[162:165], v[30:33]
	v_mfma_f32_16x16x32_bf16 v[26:29], v[154:157], v[162:165], v[26:29]
	v_mfma_f32_16x16x32_bf16 v[22:25], v[146:149], v[170:173], v[22:25]
	v_mfma_f32_16x16x32_bf16 v[18:21], v[154:157], v[170:173], v[18:21]
	v_mfma_f32_16x16x32_bf16 v[14:17], v[146:149], v[178:181], v[14:17]
	v_mfma_f32_16x16x32_bf16 v[10:13], v[154:157], v[178:181], v[10:13]
	v_mfma_f32_16x16x32_bf16 v[6:9], v[146:149], v[186:189], v[6:9]
	v_mfma_f32_16x16x32_bf16 v[2:5], v[154:157], v[186:189], v[2:5]
	v_mfma_f32_16x16x32_bf16 v[30:33], v[150:153], v[166:169], v[30:33]
	v_mfma_f32_16x16x32_bf16 v[26:29], v[158:161], v[166:169], v[26:29]
	v_mfma_f32_16x16x32_bf16 v[22:25], v[150:153], v[174:177], v[22:25]
	v_mfma_f32_16x16x32_bf16 v[18:21], v[158:161], v[174:177], v[18:21]
	v_mfma_f32_16x16x32_bf16 v[14:17], v[150:153], v[182:185], v[14:17]
	v_mfma_f32_16x16x32_bf16 v[10:13], v[158:161], v[182:185], v[10:13]
	v_mfma_f32_16x16x32_bf16 v[6:9], v[150:153], v[190:193], v[6:9]
	v_mfma_f32_16x16x32_bf16 v[2:5], v[158:161], v[190:193], v[2:5]
	s_setprio 0
	s_barrier
	s_add_u32 s28, s28, 0x100
	s_addc_u32 s29, s29, 0
	s_cmp_ge_u32 s60, s48
	s_cbranch_scc1 .LBB0_561

.LBB0_649:
	s_setprio 0
	s_barrier
	v_add_u32_e32 v142, s41, v221
	v_add_u32_e32 v158, s42, v221
	ds_read_b128 v[130:133], v142
	ds_read_b128 v[134:137], v142 offset:1024
	ds_read_b128 v[138:141], v142 offset:2048
	ds_read_b128 v[142:145], v142 offset:3072
	ds_read_b128 v[146:149], v158
	ds_read_b128 v[150:153], v158 offset:1024
	ds_read_b128 v[154:157], v158 offset:2048
	ds_read_b128 v[158:161], v158 offset:3072
	s_add_u32 s14, s14, 0x80000
	s_addc_u32 s15, s15, 0
	s_mov_b32 m0, s29
	v_lshl_add_u64 v[226:227], s[14:15], 0, v[200:201]
	ds_read_b128 v[162:165], v224 offset:32768
	ds_read_b128 v[166:169], v224 offset:33792
	ds_read_b128 v[170:173], v224 offset:34816
	ds_read_b128 v[174:177], v224 offset:35840
	ds_read_b128 v[178:181], v224 offset:36864
	ds_read_b128 v[182:185], v224 offset:37888
	ds_read_b128 v[186:189], v224 offset:38912
	ds_read_b128 v[190:193], v224 offset:39936
	global_load_lds_dwordx4 v[226:227], off
	v_lshl_add_u64 v[226:227], s[14:15], 0, v[204:205]
	s_mov_b32 m0, s30
	s_nop 0
	global_load_lds_dwordx4 v[226:227], off
	s_waitcnt vmcnt(8)
	s_waitcnt lgkmcnt(0)
	s_barrier
	s_setprio 1
	s_waitcnt lgkmcnt(0)
	v_mfma_f32_16x16x32_bf16 v[126:129], v[130:133], v[162:165], v[126:129]
	v_mfma_f32_16x16x32_bf16 v[122:125], v[138:141], v[162:165], v[122:125]
	v_mfma_f32_16x16x32_bf16 v[110:113], v[130:133], v[170:173], v[110:113]
	v_mfma_f32_16x16x32_bf16 v[106:109], v[138:141], v[170:173], v[106:109]
	v_mfma_f32_16x16x32_bf16 v[94:97], v[130:133], v[178:181], v[94:97]
	v_mfma_f32_16x16x32_bf16 v[90:93], v[138:141], v[178:181], v[90:93]
	v_mfma_f32_16x16x32_bf16 v[78:81], v[130:133], v[186:189], v[78:81]
	v_mfma_f32_16x16x32_bf16 v[74:77], v[138:141], v[186:189], v[74:77]
	v_mfma_f32_16x16x32_bf16 v[126:129], v[134:137], v[166:169], v[126:129]
	v_mfma_f32_16x16x32_bf16 v[122:125], v[142:145], v[166:169], v[122:125]
	v_mfma_f32_16x16x32_bf16 v[110:113], v[134:137], v[174:177], v[110:113]
	v_mfma_f32_16x16x32_bf16 v[106:109], v[142:145], v[174:177], v[106:109]
	v_mfma_f32_16x16x32_bf16 v[94:97], v[134:137], v[182:185], v[94:97]
	v_mfma_f32_16x16x32_bf16 v[90:93], v[142:145], v[182:185], v[90:93]
	v_mfma_f32_16x16x32_bf16 v[78:81], v[134:137], v[190:193], v[78:81]
	v_mfma_f32_16x16x32_bf16 v[74:77], v[142:145], v[190:193], v[74:77]
	s_setprio 0
	s_setprio 1
	v_mfma_f32_16x16x32_bf16 v[118:121], v[146:149], v[162:165], v[118:121]
	v_mfma_f32_16x16x32_bf16 v[114:117], v[154:157], v[162:165], v[114:117]
	v_mfma_f32_16x16x32_bf16 v[102:105], v[146:149], v[170:173], v[102:105]
	v_mfma_f32_16x16x32_bf16 v[98:101], v[154:157], v[170:173], v[98:101]
	v_mfma_f32_16x16x32_bf16 v[86:89], v[146:149], v[178:181], v[86:89]
	v_mfma_f32_16x16x32_bf16 v[82:85], v[154:157], v[178:181], v[82:85]
	v_mfma_f32_16x16x32_bf16 v[70:73], v[146:149], v[186:189], v[70:73]
	v_mfma_f32_16x16x32_bf16 v[66:69], v[154:157], v[186:189], v[66:69]
	v_mfma_f32_16x16x32_bf16 v[118:121], v[150:153], v[166:169], v[118:121]
	v_mfma_f32_16x16x32_bf16 v[114:117], v[158:161], v[166:169], v[114:117]
	v_mfma_f32_16x16x32_bf16 v[102:105], v[150:153], v[174:177], v[102:105]
	v_mfma_f32_16x16x32_bf16 v[98:101], v[158:161], v[174:177], v[98:101]
	v_mfma_f32_16x16x32_bf16 v[86:89], v[150:153], v[182:185], v[86:89]
	v_mfma_f32_16x16x32_bf16 v[82:85], v[158:161], v[182:185], v[82:85]
	v_mfma_f32_16x16x32_bf16 v[70:73], v[150:153], v[190:193], v[70:73]
	v_mfma_f32_16x16x32_bf16 v[66:69], v[158:161], v[190:193], v[66:69]
	s_setprio 0
	s_barrier
	s_mov_b32 m0, s43
	v_lshl_add_u64 v[212:213], v[212:213], 0, s[0:1]
	s_add_u32 s12, s12, 0x80080
	ds_read_b128 v[162:165], v224 offset:49152
	ds_read_b128 v[166:169], v224 offset:50176
	ds_read_b128 v[170:173], v224 offset:51200
	ds_read_b128 v[174:177], v224 offset:52224
	ds_read_b128 v[178:181], v224 offset:53248
	ds_read_b128 v[182:185], v224 offset:54272
	ds_read_b128 v[186:189], v224 offset:55296
	ds_read_b128 v[190:193], v224 offset:56320
	global_load_lds_dwordx4 v[212:213], off
	v_lshl_add_u64 v[212:213], v[214:215], 0, s[0:1]
	s_mov_b32 m0, s44
	s_addc_u32 s13, s13, 0
	global_load_lds_dwordx4 v[212:213], off
	v_lshl_add_u64 v[212:213], s[12:13], 0, v[202:203]
	s_mov_b32 m0, s45
	s_nop 0
	global_load_lds_dwordx4 v[212:213], off
	v_lshl_add_u64 v[212:213], s[12:13], 0, v[206:207]
	s_mov_b32 m0, s46
	s_nop 0
	global_load_lds_dwordx4 v[212:213], off
	v_lshl_add_u64 v[212:213], v[216:217], 0, s[0:1]
	s_mov_b32 m0, s34
	s_nop 0
	global_load_lds_dwordx4 v[212:213], off
	v_lshl_add_u64 v[212:213], v[218:219], 0, s[0:1]
	s_mov_b32 m0, s35
	s_nop 0
	global_load_lds_dwordx4 v[212:213], off
	s_waitcnt vmcnt(8)
	s_waitcnt lgkmcnt(0)
	s_barrier
	s_setprio 1
	s_waitcnt lgkmcnt(0)
	v_mfma_f32_16x16x32_bf16 v[62:65], v[130:133], v[162:165], v[62:65]
	v_mfma_f32_16x16x32_bf16 v[58:61], v[138:141], v[162:165], v[58:61]
	v_mfma_f32_16x16x32_bf16 v[46:49], v[130:133], v[170:173], v[46:49]
	v_mfma_f32_16x16x32_bf16 v[42:45], v[138:141], v[170:173], v[42:45]
	v_mfma_f32_16x16x32_bf16 v[30:33], v[130:133], v[178:181], v[30:33]
	v_mfma_f32_16x16x32_bf16 v[26:29], v[138:141], v[178:181], v[26:29]
	v_mfma_f32_16x16x32_bf16 v[14:17], v[130:133], v[186:189], v[14:17]
	v_mfma_f32_16x16x32_bf16 v[10:13], v[138:141], v[186:189], v[10:13]
	v_mfma_f32_16x16x32_bf16 v[62:65], v[134:137], v[166:169], v[62:65]
	v_mfma_f32_16x16x32_bf16 v[58:61], v[142:145], v[166:169], v[58:61]
	v_mfma_f32_16x16x32_bf16 v[46:49], v[134:137], v[174:177], v[46:49]
	v_mfma_f32_16x16x32_bf16 v[42:45], v[142:145], v[174:177], v[42:45]
	v_mfma_f32_16x16x32_bf16 v[30:33], v[134:137], v[182:185], v[30:33]
	v_mfma_f32_16x16x32_bf16 v[26:29], v[142:145], v[182:185], v[26:29]
	v_mfma_f32_16x16x32_bf16 v[14:17], v[134:137], v[190:193], v[14:17]
	v_mfma_f32_16x16x32_bf16 v[10:13], v[142:145], v[190:193], v[10:13]
	s_setprio 0
	s_setprio 1
	v_mfma_f32_16x16x32_bf16 v[54:57], v[146:149], v[162:165], v[54:57]
	v_mfma_f32_16x16x32_bf16 v[50:53], v[154:157], v[162:165], v[50:53]
	v_mfma_f32_16x16x32_bf16 v[38:41], v[146:149], v[170:173], v[38:41]
	v_mfma_f32_16x16x32_bf16 v[34:37], v[154:157], v[170:173], v[34:37]
	v_mfma_f32_16x16x32_bf16 v[22:25], v[146:149], v[178:181], v[22:25]
	v_mfma_f32_16x16x32_bf16 v[18:21], v[154:157], v[178:181], v[18:21]
	v_mfma_f32_16x16x32_bf16 v[6:9], v[146:149], v[186:189], v[6:9]
	v_mfma_f32_16x16x32_bf16 v[2:5], v[154:157], v[186:189], v[2:5]
	v_mfma_f32_16x16x32_bf16 v[54:57], v[150:153], v[166:169], v[54:57]
	v_mfma_f32_16x16x32_bf16 v[50:53], v[158:161], v[166:169], v[50:53]
	v_mfma_f32_16x16x32_bf16 v[38:41], v[150:153], v[174:177], v[38:41]
	v_mfma_f32_16x16x32_bf16 v[34:37], v[158:161], v[174:177], v[34:37]
	v_mfma_f32_16x16x32_bf16 v[22:25], v[150:153], v[182:185], v[22:25]
	v_mfma_f32_16x16x32_bf16 v[18:21], v[158:161], v[182:185], v[18:21]
	v_mfma_f32_16x16x32_bf16 v[6:9], v[150:153], v[190:193], v[6:9]
	v_mfma_f32_16x16x32_bf16 v[2:5], v[158:161], v[190:193], v[2:5]
	s_setprio 0
	s_barrier
	s_add_i32 s38, s38, 2
	s_add_u32 s10, s10, 0x100
	s_addc_u32 s11, s11, 0
	s_cmp_gt_u32 s38, 29
	s_cbranch_scc1 .LBB0_657
.LBB0_650:
	ds_read_b128 v[146:149], v222
	ds_read_b128 v[150:153], v222 offset:1024
	ds_read_b128 v[154:157], v222 offset:2048
	ds_read_b128 v[158:161], v222 offset:3072
	ds_read_b128 v[130:133], v223
	ds_read_b128 v[134:137], v223 offset:1024
	ds_read_b128 v[138:141], v223 offset:2048
	ds_read_b128 v[142:145], v223 offset:3072
	s_mov_b32 m0, s39
	v_lshl_add_u64 v[212:213], v[208:209], 0, s[10:11]
	ds_read_b128 v[186:189], v224
	ds_read_b128 v[190:193], v224 offset:1024
	ds_read_b128 v[178:181], v224 offset:2048
	ds_read_b128 v[182:185], v224 offset:3072
	ds_read_b128 v[170:173], v224 offset:4096
	ds_read_b128 v[174:177], v224 offset:5120
	ds_read_b128 v[162:165], v224 offset:6144
	ds_read_b128 v[166:169], v224 offset:7168
	global_load_lds_dwordx4 v[212:213], off
	v_lshl_add_u64 v[212:213], v[210:211], 0, s[10:11]
	s_mov_b32 m0, s40
	s_cmp_lg_u32 s10, 0
	global_load_lds_dwordx4 v[212:213], off
	s_waitcnt vmcnt(8)
	s_waitcnt lgkmcnt(0)
	s_cselect_b64 s[16:17], -1, 0
	s_barrier
	s_setprio 1
	s_and_b64 vcc, exec, s[16:17]
	s_cbranch_vccz .LBB0_655
	s_waitcnt lgkmcnt(0)
	v_mfma_f32_16x16x32_bf16 v[126:129], v[146:149], v[186:189], v[126:129]
	v_mfma_f32_16x16x32_bf16 v[122:125], v[154:157], v[186:189], v[122:125]
	v_mfma_f32_16x16x32_bf16 v[110:113], v[146:149], v[178:181], v[110:113]
	v_mfma_f32_16x16x32_bf16 v[106:109], v[154:157], v[178:181], v[106:109]
	v_mfma_f32_16x16x32_bf16 v[94:97], v[146:149], v[170:173], v[94:97]
	v_mfma_f32_16x16x32_bf16 v[90:93], v[154:157], v[170:173], v[90:93]
	v_mfma_f32_16x16x32_bf16 v[78:81], v[146:149], v[162:165], v[78:81]
	v_mfma_f32_16x16x32_bf16 v[74:77], v[154:157], v[162:165], v[74:77]
	v_mfma_f32_16x16x32_bf16 v[126:129], v[150:153], v[190:193], v[126:129]
	v_mfma_f32_16x16x32_bf16 v[122:125], v[158:161], v[190:193], v[122:125]
	v_mfma_f32_16x16x32_bf16 v[110:113], v[150:153], v[182:185], v[110:113]
	v_mfma_f32_16x16x32_bf16 v[106:109], v[158:161], v[182:185], v[106:109]
	v_mfma_f32_16x16x32_bf16 v[94:97], v[150:153], v[174:177], v[94:97]
	v_mfma_f32_16x16x32_bf16 v[90:93], v[158:161], v[174:177], v[90:93]
	v_mfma_f32_16x16x32_bf16 v[78:81], v[150:153], v[166:169], v[78:81]
	v_mfma_f32_16x16x32_bf16 v[74:77], v[158:161], v[166:169], v[74:77]
	s_setprio 0
	s_setprio 1
	v_mfma_f32_16x16x32_bf16 v[118:121], v[130:133], v[186:189], v[118:121]
	v_mfma_f32_16x16x32_bf16 v[114:117], v[138:141], v[186:189], v[114:117]
	v_mfma_f32_16x16x32_bf16 v[102:105], v[130:133], v[178:181], v[102:105]
	v_mfma_f32_16x16x32_bf16 v[98:101], v[138:141], v[178:181], v[98:101]
	v_mfma_f32_16x16x32_bf16 v[86:89], v[130:133], v[170:173], v[86:89]
	v_mfma_f32_16x16x32_bf16 v[82:85], v[138:141], v[170:173], v[82:85]
	v_mfma_f32_16x16x32_bf16 v[70:73], v[130:133], v[162:165], v[70:73]
	v_mfma_f32_16x16x32_bf16 v[66:69], v[138:141], v[162:165], v[66:69]
	v_mfma_f32_16x16x32_bf16 v[118:121], v[134:137], v[190:193], v[118:121]
	v_mfma_f32_16x16x32_bf16 v[114:117], v[142:145], v[190:193], v[114:117]
	v_mfma_f32_16x16x32_bf16 v[102:105], v[134:137], v[182:185], v[102:105]
	v_mfma_f32_16x16x32_bf16 v[98:101], v[142:145], v[182:185], v[98:101]
	v_mfma_f32_16x16x32_bf16 v[86:89], v[134:137], v[174:177], v[86:89]
	v_mfma_f32_16x16x32_bf16 v[82:85], v[142:145], v[174:177], v[82:85]
	v_mfma_f32_16x16x32_bf16 v[70:73], v[134:137], v[166:169], v[70:73]
	v_mfma_f32_16x16x32_bf16 v[66:69], v[142:145], v[166:169], v[66:69]
	s_cbranch_execnz .LBB0_653

.LBB0_764:
	s_setprio 0
	s_barrier
	v_add_u32_e32 v142, s40, v199
	v_add_u32_e32 v158, s41, v199
	ds_read_b128 v[130:133], v142
	ds_read_b128 v[134:137], v142 offset:1024
	ds_read_b128 v[138:141], v142 offset:2048
	ds_read_b128 v[142:145], v142 offset:3072
	ds_read_b128 v[146:149], v158
	ds_read_b128 v[150:153], v158 offset:1024
	ds_read_b128 v[154:157], v158 offset:2048
	ds_read_b128 v[158:161], v158 offset:3072
	s_add_u32 s16, s16, 0x40000
	s_addc_u32 s17, s17, 0
	s_mov_b32 m0, s27
	v_lshl_add_u64 v[224:225], s[16:17], 0, v[206:207]
	ds_read_b128 v[162:165], v223 offset:32768
	ds_read_b128 v[166:169], v223 offset:33792
	ds_read_b128 v[170:173], v223 offset:34816
	ds_read_b128 v[174:177], v223 offset:35840
	ds_read_b128 v[178:181], v223 offset:36864
	ds_read_b128 v[182:185], v223 offset:37888
	ds_read_b128 v[186:189], v223 offset:38912
	ds_read_b128 v[190:193], v223 offset:39936
	global_load_lds_dwordx4 v[224:225], off
	v_lshl_add_u64 v[224:225], s[16:17], 0, v[202:203]
	s_mov_b32 m0, s28
	s_nop 0
	global_load_lds_dwordx4 v[224:225], off
	s_waitcnt vmcnt(8)
	s_waitcnt lgkmcnt(0)
	s_barrier
	s_setprio 1
	s_waitcnt lgkmcnt(0)
	v_mfma_f32_16x16x32_bf16 v[126:129], v[130:133], v[162:165], v[126:129]
	v_mfma_f32_16x16x32_bf16 v[122:125], v[138:141], v[162:165], v[122:125]
	v_mfma_f32_16x16x32_bf16 v[114:117], v[130:133], v[170:173], v[114:117]
	v_mfma_f32_16x16x32_bf16 v[106:109], v[138:141], v[170:173], v[106:109]
	v_mfma_f32_16x16x32_bf16 v[98:101], v[130:133], v[178:181], v[98:101]
	v_mfma_f32_16x16x32_bf16 v[90:93], v[138:141], v[178:181], v[90:93]
	v_mfma_f32_16x16x32_bf16 v[82:85], v[130:133], v[186:189], v[82:85]
	v_mfma_f32_16x16x32_bf16 v[74:77], v[138:141], v[186:189], v[74:77]
	v_mfma_f32_16x16x32_bf16 v[126:129], v[134:137], v[166:169], v[126:129]
	v_mfma_f32_16x16x32_bf16 v[122:125], v[142:145], v[166:169], v[122:125]
	v_mfma_f32_16x16x32_bf16 v[114:117], v[134:137], v[174:177], v[114:117]
	v_mfma_f32_16x16x32_bf16 v[106:109], v[142:145], v[174:177], v[106:109]
	v_mfma_f32_16x16x32_bf16 v[98:101], v[134:137], v[182:185], v[98:101]
	v_mfma_f32_16x16x32_bf16 v[90:93], v[142:145], v[182:185], v[90:93]
	v_mfma_f32_16x16x32_bf16 v[82:85], v[134:137], v[190:193], v[82:85]
	v_mfma_f32_16x16x32_bf16 v[74:77], v[142:145], v[190:193], v[74:77]
	s_setprio 0
	s_setprio 1
	v_mfma_f32_16x16x32_bf16 v[118:121], v[146:149], v[162:165], v[118:121]
	v_mfma_f32_16x16x32_bf16 v[110:113], v[154:157], v[162:165], v[110:113]
	v_mfma_f32_16x16x32_bf16 v[102:105], v[146:149], v[170:173], v[102:105]
	v_mfma_f32_16x16x32_bf16 v[94:97], v[154:157], v[170:173], v[94:97]
	v_mfma_f32_16x16x32_bf16 v[86:89], v[146:149], v[178:181], v[86:89]
	v_mfma_f32_16x16x32_bf16 v[78:81], v[154:157], v[178:181], v[78:81]
	v_mfma_f32_16x16x32_bf16 v[70:73], v[146:149], v[186:189], v[70:73]
	v_mfma_f32_16x16x32_bf16 v[66:69], v[154:157], v[186:189], v[66:69]
	v_mfma_f32_16x16x32_bf16 v[118:121], v[150:153], v[166:169], v[118:121]
	v_mfma_f32_16x16x32_bf16 v[110:113], v[158:161], v[166:169], v[110:113]
	v_mfma_f32_16x16x32_bf16 v[102:105], v[150:153], v[174:177], v[102:105]
	v_mfma_f32_16x16x32_bf16 v[94:97], v[158:161], v[174:177], v[94:97]
	v_mfma_f32_16x16x32_bf16 v[86:89], v[150:153], v[182:185], v[86:89]
	v_mfma_f32_16x16x32_bf16 v[78:81], v[158:161], v[182:185], v[78:81]
	v_mfma_f32_16x16x32_bf16 v[70:73], v[150:153], v[190:193], v[70:73]
	v_mfma_f32_16x16x32_bf16 v[66:69], v[158:161], v[190:193], v[66:69]
	s_setprio 0
	s_barrier
	s_mov_b32 m0, s42
	v_lshl_add_u64 v[212:213], v[212:213], 0, s[8:9]
	s_add_u32 s14, s14, 0x40080
	ds_read_b128 v[162:165], v223 offset:49152
	ds_read_b128 v[166:169], v223 offset:50176
	ds_read_b128 v[170:173], v223 offset:51200
	ds_read_b128 v[174:177], v223 offset:52224
	ds_read_b128 v[178:181], v223 offset:53248
	ds_read_b128 v[182:185], v223 offset:54272
	ds_read_b128 v[186:189], v223 offset:55296
	ds_read_b128 v[190:193], v223 offset:56320
	global_load_lds_dwordx4 v[212:213], off
	v_lshl_add_u64 v[212:213], v[214:215], 0, s[8:9]
	s_mov_b32 m0, s43
	s_addc_u32 s15, s15, 0
	global_load_lds_dwordx4 v[212:213], off
	v_lshl_add_u64 v[212:213], s[14:15], 0, v[204:205]
	s_mov_b32 m0, s44
	s_nop 0
	global_load_lds_dwordx4 v[212:213], off
	v_lshl_add_u64 v[212:213], s[14:15], 0, v[200:201]
	s_mov_b32 m0, s45
	s_nop 0
	global_load_lds_dwordx4 v[212:213], off
	v_lshl_add_u64 v[212:213], v[216:217], 0, s[8:9]
	s_mov_b32 m0, s30
	s_nop 0
	global_load_lds_dwordx4 v[212:213], off
	v_lshl_add_u64 v[212:213], v[218:219], 0, s[8:9]
	s_mov_b32 m0, s31
	s_nop 0
	global_load_lds_dwordx4 v[212:213], off
	s_waitcnt vmcnt(8)
	s_waitcnt lgkmcnt(0)
	s_barrier
	s_setprio 1
	s_waitcnt lgkmcnt(0)
	v_mfma_f32_16x16x32_bf16 v[62:65], v[130:133], v[162:165], v[62:65]
	v_mfma_f32_16x16x32_bf16 v[58:61], v[138:141], v[162:165], v[58:61]
	v_mfma_f32_16x16x32_bf16 v[50:53], v[130:133], v[170:173], v[50:53]
	v_mfma_f32_16x16x32_bf16 v[42:45], v[138:141], v[170:173], v[42:45]
	v_mfma_f32_16x16x32_bf16 v[34:37], v[130:133], v[178:181], v[34:37]
	v_mfma_f32_16x16x32_bf16 v[26:29], v[138:141], v[178:181], v[26:29]
	v_mfma_f32_16x16x32_bf16 v[18:21], v[130:133], v[186:189], v[18:21]
	v_mfma_f32_16x16x32_bf16 v[10:13], v[138:141], v[186:189], v[10:13]
	v_mfma_f32_16x16x32_bf16 v[62:65], v[134:137], v[166:169], v[62:65]
	v_mfma_f32_16x16x32_bf16 v[58:61], v[142:145], v[166:169], v[58:61]
	v_mfma_f32_16x16x32_bf16 v[50:53], v[134:137], v[174:177], v[50:53]
	v_mfma_f32_16x16x32_bf16 v[42:45], v[142:145], v[174:177], v[42:45]
	v_mfma_f32_16x16x32_bf16 v[34:37], v[134:137], v[182:185], v[34:37]
	v_mfma_f32_16x16x32_bf16 v[26:29], v[142:145], v[182:185], v[26:29]
	v_mfma_f32_16x16x32_bf16 v[18:21], v[134:137], v[190:193], v[18:21]
	v_mfma_f32_16x16x32_bf16 v[10:13], v[142:145], v[190:193], v[10:13]
	s_setprio 0
	s_setprio 1
	v_mfma_f32_16x16x32_bf16 v[54:57], v[146:149], v[162:165], v[54:57]
	v_mfma_f32_16x16x32_bf16 v[46:49], v[154:157], v[162:165], v[46:49]
	v_mfma_f32_16x16x32_bf16 v[38:41], v[146:149], v[170:173], v[38:41]
	v_mfma_f32_16x16x32_bf16 v[30:33], v[154:157], v[170:173], v[30:33]
	v_mfma_f32_16x16x32_bf16 v[22:25], v[146:149], v[178:181], v[22:25]
	v_mfma_f32_16x16x32_bf16 v[14:17], v[154:157], v[178:181], v[14:17]
	v_mfma_f32_16x16x32_bf16 v[6:9], v[146:149], v[186:189], v[6:9]
	v_mfma_f32_16x16x32_bf16 v[2:5], v[154:157], v[186:189], v[2:5]
	v_mfma_f32_16x16x32_bf16 v[54:57], v[150:153], v[166:169], v[54:57]
	v_mfma_f32_16x16x32_bf16 v[46:49], v[158:161], v[166:169], v[46:49]
	v_mfma_f32_16x16x32_bf16 v[38:41], v[150:153], v[174:177], v[38:41]
	v_mfma_f32_16x16x32_bf16 v[30:33], v[158:161], v[174:177], v[30:33]
	v_mfma_f32_16x16x32_bf16 v[22:25], v[150:153], v[182:185], v[22:25]
	v_mfma_f32_16x16x32_bf16 v[14:17], v[158:161], v[182:185], v[14:17]
	v_mfma_f32_16x16x32_bf16 v[6:9], v[150:153], v[190:193], v[6:9]
	v_mfma_f32_16x16x32_bf16 v[2:5], v[158:161], v[190:193], v[2:5]
	s_setprio 0
	s_barrier
	s_add_i32 s35, s35, 2
	s_add_u32 s12, s12, 0x100
	s_addc_u32 s13, s13, 0
	s_cmp_gt_u32 s35, 13
	s_cbranch_scc1 .LBB0_772
.LBB0_765:
	ds_read_b128 v[146:149], v221
	ds_read_b128 v[150:153], v221 offset:1024
	ds_read_b128 v[154:157], v221 offset:2048
	ds_read_b128 v[158:161], v221 offset:3072
	ds_read_b128 v[130:133], v222
	ds_read_b128 v[134:137], v222 offset:1024
	ds_read_b128 v[138:141], v222 offset:2048
	ds_read_b128 v[142:145], v222 offset:3072
	s_mov_b32 m0, s38
	v_lshl_add_u64 v[212:213], v[208:209], 0, s[12:13]
	ds_read_b128 v[186:189], v223
	ds_read_b128 v[190:193], v223 offset:1024
	ds_read_b128 v[178:181], v223 offset:2048
	ds_read_b128 v[182:185], v223 offset:3072
	ds_read_b128 v[170:173], v223 offset:4096
	ds_read_b128 v[174:177], v223 offset:5120
	ds_read_b128 v[162:165], v223 offset:6144
	ds_read_b128 v[166:169], v223 offset:7168
	global_load_lds_dwordx4 v[212:213], off
	v_lshl_add_u64 v[212:213], v[210:211], 0, s[12:13]
	s_mov_b32 m0, s39
	s_cmp_lg_u32 s12, 0
	global_load_lds_dwordx4 v[212:213], off
	s_waitcnt vmcnt(8)
	s_waitcnt lgkmcnt(0)
	s_cselect_b64 s[18:19], -1, 0
	s_barrier
	s_setprio 1
	s_and_b64 vcc, exec, s[18:19]
	s_cbranch_vccz .LBB0_770
	s_waitcnt lgkmcnt(0)
	v_mfma_f32_16x16x32_bf16 v[126:129], v[146:149], v[186:189], v[126:129]
	v_mfma_f32_16x16x32_bf16 v[122:125], v[154:157], v[186:189], v[122:125]
	v_mfma_f32_16x16x32_bf16 v[114:117], v[146:149], v[178:181], v[114:117]
	v_mfma_f32_16x16x32_bf16 v[106:109], v[154:157], v[178:181], v[106:109]
	v_mfma_f32_16x16x32_bf16 v[98:101], v[146:149], v[170:173], v[98:101]
	v_mfma_f32_16x16x32_bf16 v[90:93], v[154:157], v[170:173], v[90:93]
	v_mfma_f32_16x16x32_bf16 v[82:85], v[146:149], v[162:165], v[82:85]
	v_mfma_f32_16x16x32_bf16 v[74:77], v[154:157], v[162:165], v[74:77]
	v_mfma_f32_16x16x32_bf16 v[126:129], v[150:153], v[190:193], v[126:129]
	v_mfma_f32_16x16x32_bf16 v[122:125], v[158:161], v[190:193], v[122:125]
	v_mfma_f32_16x16x32_bf16 v[114:117], v[150:153], v[182:185], v[114:117]
	v_mfma_f32_16x16x32_bf16 v[106:109], v[158:161], v[182:185], v[106:109]
	v_mfma_f32_16x16x32_bf16 v[98:101], v[150:153], v[174:177], v[98:101]
	v_mfma_f32_16x16x32_bf16 v[90:93], v[158:161], v[174:177], v[90:93]
	v_mfma_f32_16x16x32_bf16 v[82:85], v[150:153], v[166:169], v[82:85]
	v_mfma_f32_16x16x32_bf16 v[74:77], v[158:161], v[166:169], v[74:77]
	s_setprio 0
	s_setprio 1
	v_mfma_f32_16x16x32_bf16 v[118:121], v[130:133], v[186:189], v[118:121]
	v_mfma_f32_16x16x32_bf16 v[110:113], v[138:141], v[186:189], v[110:113]
	v_mfma_f32_16x16x32_bf16 v[102:105], v[130:133], v[178:181], v[102:105]
	v_mfma_f32_16x16x32_bf16 v[94:97], v[138:141], v[178:181], v[94:97]
	v_mfma_f32_16x16x32_bf16 v[86:89], v[130:133], v[170:173], v[86:89]
	v_mfma_f32_16x16x32_bf16 v[78:81], v[138:141], v[170:173], v[78:81]
	v_mfma_f32_16x16x32_bf16 v[70:73], v[130:133], v[162:165], v[70:73]
	v_mfma_f32_16x16x32_bf16 v[66:69], v[138:141], v[162:165], v[66:69]
	v_mfma_f32_16x16x32_bf16 v[118:121], v[134:137], v[190:193], v[118:121]
	v_mfma_f32_16x16x32_bf16 v[110:113], v[142:145], v[190:193], v[110:113]
	v_mfma_f32_16x16x32_bf16 v[102:105], v[134:137], v[182:185], v[102:105]
	v_mfma_f32_16x16x32_bf16 v[94:97], v[142:145], v[182:185], v[94:97]
	v_mfma_f32_16x16x32_bf16 v[86:89], v[134:137], v[174:177], v[86:89]
	v_mfma_f32_16x16x32_bf16 v[78:81], v[142:145], v[174:177], v[78:81]
	v_mfma_f32_16x16x32_bf16 v[70:73], v[134:137], v[166:169], v[70:73]
	v_mfma_f32_16x16x32_bf16 v[66:69], v[142:145], v[166:169], v[66:69]
	s_cbranch_execnz .LBB0_768

.LBB0_1289:
	v_add_u32_e32 v2, 0, v237
	v_add_u32_e32 v3, 0x10000, v2
	v_add_u32_e32 v6, 0x14000, v2
	ds_read_b128 v[26:29], v3
	ds_read_b128 v[30:33], v3 offset:1024
	ds_read_b128 v[18:21], v3 offset:2048
	ds_read_b128 v[22:25], v3 offset:3072
	ds_read_b128 v[10:13], v6
	ds_read_b128 v[14:17], v6 offset:1024
	ds_read_b128 v[2:5], v6 offset:2048
	ds_read_b128 v[6:9], v6 offset:3072
	s_lshl_b32 s35, s9, 7
	s_add_u32 s54, s40, s35
	s_addc_u32 s55, s41, 0
	v_mov_b32_e32 v211, v207
	v_lshl_add_u64 v[216:217], s[54:55], 0, v[210:211]
	v_lshl_add_u64 v[216:217], v[216:217], 0, s[16:17]
	s_add_i32 m0, s70, 0xc000
	v_mov_b32_e32 v213, v207
	ds_read_b128 v[58:61], v247
	ds_read_b128 v[62:65], v247 offset:1024
	ds_read_b128 v[50:53], v247 offset:2048
	ds_read_b128 v[54:57], v247 offset:3072
	ds_read_b128 v[42:45], v247 offset:4096
	ds_read_b128 v[46:49], v247 offset:5120
	ds_read_b128 v[34:37], v247 offset:6144
	ds_read_b128 v[38:41], v247 offset:7168
	s_add_u32 s100, s54, 0x80
	s_addc_u32 s101, s55, 0
	s_mov_b32 m0, s79
	s_nop 0
	global_load_lds_dwordx4 v206, s[100:101]
	s_mov_b32 m0, s80
	s_nop 0
	global_load_lds_dwordx4 v208, s[100:101]
	s_add_i32 m0, s70, 0xc000
	s_nop 0
	global_load_lds_dwordx4 v[216:217], off
	v_lshl_add_u64 v[216:217], s[54:55], 0, v[212:213]
	v_lshl_add_u64 v[216:217], v[216:217], 0, s[16:17]
	s_add_i32 m0, s70, 0xe000
	s_andn2_b64 vcc, exec, s[56:57]
	global_load_lds_dwordx4 v[216:217], off
	s_cbranch_vccnz .LBB0_1291
	ds_read2st64_b32 v[208:209], v249 offset1:2
	ds_read2st64_b32 v[210:211], v250 offset1:2
	s_waitcnt lgkmcnt(0)
	v_sub_u32_e32 v209, v209, v197
	v_sub_u32_e32 v206, v208, v197
	v_sub_u32_e32 v208, v210, v221
	v_lshl_add_u32 v210, v209, 11, v220
	v_sub_u32_e32 v209, v211, v221
	v_lshl_add_u32 v206, v206, 11, v220
	v_lshl_add_u32 v208, v208, 11, v222
	v_lshl_add_u32 v212, v209, 11, v222

.LBB0_1294:
	s_add_u32 s43, s54, 0x100
	s_addc_u32 s58, s55, 0
	s_and_b64 s[54:55], s[52:53], exec
	s_cselect_b32 s55, s58, s47
	s_cselect_b32 s54, s43, s46
	s_add_u32 s35, s38, s35
	s_addc_u32 s43, s39, 0
	s_add_u32 s35, s35, 0x100
	s_addc_u32 s43, s43, 0
	s_and_b64 s[52:53], s[52:53], exec
	s_cselect_b32 s53, s43, s45
	s_cselect_b32 s52, s35, s44
	s_setprio 0
	s_barrier
	s_mov_b32 m0, s71
	v_lshl_add_u64 v[218:219], s[52:53], 0, v[198:199]
	s_add_u32 s58, s52, 0x40000
	s_waitcnt lgkmcnt(0)
	ds_read_b128 v[34:37], v247 offset:16384
	ds_read_b128 v[38:41], v247 offset:17408
	ds_read_b128 v[42:45], v247 offset:18432
	ds_read_b128 v[46:49], v247 offset:19456
	ds_read_b128 v[50:53], v247 offset:20480
	ds_read_b128 v[54:57], v247 offset:21504
	ds_read_b128 v[58:61], v247 offset:22528
	ds_read_b128 v[62:65], v247 offset:23552
	global_load_lds_dwordx4 v[218:219], off
	v_lshl_add_u64 v[216:217], s[52:53], 0, v[200:201]
	s_mov_b32 m0, s72
	s_addc_u32 s59, s53, 0
	global_load_lds_dwordx4 v[216:217], off
	v_lshl_add_u64 v[230:231], s[58:59], 0, v[198:199]
	s_mov_b32 m0, s73
	s_nop 0
	global_load_lds_dwordx4 v[230:231], off
	v_lshl_add_u64 v[230:231], s[58:59], 0, v[200:201]
	s_mov_b32 m0, s74
	s_nop 0
	global_load_lds_dwordx4 v[230:231], off
	s_waitcnt vmcnt(6)
	s_waitcnt lgkmcnt(0)
	s_barrier
	s_setprio 1
	s_and_b64 vcc, exec, s[56:57]
	s_cbranch_vccz .LBB0_1300
	s_waitcnt lgkmcnt(0)
	v_mfma_f32_16x16x128_f8f6f4 v[66:69], v[26:33], v[34:41], v[66:69]
	v_mfma_f32_16x16x128_f8f6f4 v[70:73], v[18:25], v[34:41], v[70:73]
	v_mfma_f32_16x16x128_f8f6f4 v[74:77], v[26:33], v[42:49], v[74:77]
	v_mfma_f32_16x16x128_f8f6f4 v[78:81], v[18:25], v[42:49], v[78:81]
	v_mfma_f32_16x16x128_f8f6f4 v[82:85], v[26:33], v[50:57], v[82:85]
	v_mfma_f32_16x16x128_f8f6f4 v[86:89], v[18:25], v[50:57], v[86:89]
	v_mfma_f32_16x16x128_f8f6f4 v[94:97], v[26:33], v[58:65], v[94:97]
	v_mfma_f32_16x16x128_f8f6f4 v[98:101], v[18:25], v[58:65], v[98:101]
	s_setprio 0
	s_setprio 1
	v_mfma_f32_16x16x128_f8f6f4 v[110:113], v[10:17], v[34:41], v[110:113]
	v_mfma_f32_16x16x128_f8f6f4 v[118:121], v[2:9], v[34:41], v[118:121]
	v_mfma_f32_16x16x128_f8f6f4 v[126:129], v[10:17], v[42:49], v[126:129]
	v_mfma_f32_16x16x128_f8f6f4 v[134:137], v[2:9], v[42:49], v[134:137]
	v_mfma_f32_16x16x128_f8f6f4 v[142:145], v[10:17], v[50:57], v[142:145]
	v_mfma_f32_16x16x128_f8f6f4 v[150:153], v[2:9], v[50:57], v[150:153]
	v_mfma_f32_16x16x128_f8f6f4 v[154:157], v[10:17], v[58:65], v[154:157]
	v_mfma_f32_16x16x128_f8f6f4 v[158:161], v[2:9], v[58:65], v[158:161]
	s_cbranch_execnz .LBB0_1297

.LBB0_1297:
	v_mov_b32_e32 v209, v207
	v_lshl_add_u64 v[230:231], s[54:55], 0, v[206:207]
	v_lshl_add_u64 v[232:233], s[54:55], 0, v[208:209]
	s_setprio 0
	s_barrier
	s_add_i32 s35, 0, 0x18000
	s_add_i32 s43, 0, 0x1c000
	v_add_u32_e32 v2, s35, v237
	v_add_u32_e32 v30, s43, v237
	ds_read_b128 v[10:13], v2
	ds_read_b128 v[14:17], v2 offset:1024
	ds_read_b128 v[18:21], v2 offset:2048
	ds_read_b128 v[22:25], v2 offset:3072
	ds_read_b128 v[2:5], v30
	ds_read_b128 v[6:9], v30 offset:1024
	ds_read_b128 v[26:29], v30 offset:2048
	ds_read_b128 v[30:33], v30 offset:3072
	s_mov_b32 m0, s76
	ds_read_b128 v[34:37], v247 offset:32768
	ds_read_b128 v[38:41], v247 offset:33792
	ds_read_b128 v[42:45], v247 offset:34816
	ds_read_b128 v[46:49], v247 offset:35840
	ds_read_b128 v[50:53], v247 offset:36864
	ds_read_b128 v[54:57], v247 offset:37888
	ds_read_b128 v[58:61], v247 offset:38912
	ds_read_b128 v[62:65], v247 offset:39936
	s_mov_b32 m0, s70
	s_nop 0
	global_load_lds_dwordx4 v206, s[54:55]
	s_mov_b32 m0, s75
	s_nop 0
	global_load_lds_dwordx4 v208, s[54:55]
	s_mov_b32 m0, s76
	s_nop 0
	global_load_lds_dwordx4 v210, s[54:55]
	s_mov_b32 m0, s77
	s_nop 0
	global_load_lds_dwordx4 v212, s[54:55]
	s_waitcnt vmcnt(8)
	s_waitcnt lgkmcnt(0)
	s_barrier
	s_setprio 1
	s_waitcnt lgkmcnt(0)
	v_mfma_f32_16x16x128_f8f6f4 v[90:93], v[10:17], v[34:41], v[90:93]
	v_mfma_f32_16x16x128_f8f6f4 v[102:105], v[18:25], v[34:41], v[102:105]
	v_mfma_f32_16x16x128_f8f6f4 v[106:109], v[10:17], v[42:49], v[106:109]
	v_mfma_f32_16x16x128_f8f6f4 v[114:117], v[18:25], v[42:49], v[114:117]
	v_mfma_f32_16x16x128_f8f6f4 v[122:125], v[10:17], v[50:57], v[122:125]
	v_mfma_f32_16x16x128_f8f6f4 v[130:133], v[18:25], v[50:57], v[130:133]
	v_mfma_f32_16x16x128_f8f6f4 v[138:141], v[10:17], v[58:65], v[138:141]
	v_mfma_f32_16x16x128_f8f6f4 v[146:149], v[18:25], v[58:65], v[146:149]
	s_setprio 0
	s_setprio 1
	v_mfma_f32_16x16x128_f8f6f4 v[162:165], v[2:9], v[34:41], v[162:165]
	v_mfma_f32_16x16x128_f8f6f4 v[166:169], v[26:33], v[34:41], v[166:169]
	v_mfma_f32_16x16x128_f8f6f4 v[170:173], v[2:9], v[42:49], v[170:173]
	v_mfma_f32_16x16x128_f8f6f4 v[174:177], v[26:33], v[42:49], v[174:177]
	v_mfma_f32_16x16x128_f8f6f4 v[178:181], v[2:9], v[50:57], v[178:181]
	v_mfma_f32_16x16x128_f8f6f4 v[182:185], v[26:33], v[50:57], v[182:185]
	v_mfma_f32_16x16x128_f8f6f4 v[186:189], v[2:9], v[58:65], v[186:189]
	v_mfma_f32_16x16x128_f8f6f4 v[190:193], v[26:33], v[58:65], v[190:193]
	s_setprio 0
	s_barrier
	s_add_i32 s35, s35, s69
	v_lshl_add_u64 v[218:219], v[218:219], 0, s[16:17]
	s_mov_b32 m0, s35
	ds_read_b128 v[34:37], v247 offset:49152
	ds_read_b128 v[38:41], v247 offset:50176
	ds_read_b128 v[42:45], v247 offset:51200
	ds_read_b128 v[46:49], v247 offset:52224
	ds_read_b128 v[50:53], v247 offset:53248
	ds_read_b128 v[54:57], v247 offset:54272
	ds_read_b128 v[58:61], v247 offset:55296
	ds_read_b128 v[62:65], v247 offset:56320
	global_load_lds_dwordx4 v[218:219], off
	s_add_i32 m0, s35, 0x2000
	s_add_u32 s52, s52, 0x40080
	v_lshl_add_u64 v[216:217], v[216:217], 0, s[16:17]
	s_addc_u32 s53, s53, 0
	s_add_i32 s35, s43, s69
	global_load_lds_dwordx4 v[216:217], off
	v_lshl_add_u64 v[216:217], s[52:53], 0, v[198:199]
	s_mov_b32 m0, s35
	s_nop 0
	global_load_lds_dwordx4 v[216:217], off
	v_lshl_add_u64 v[216:217], s[52:53], 0, v[200:201]
	s_add_i32 m0, s35, 0x2000
	s_nop 0
	global_load_lds_dwordx4 v[216:217], off
	s_waitcnt vmcnt(6)
	s_waitcnt lgkmcnt(0)
	s_barrier
	s_setprio 1
	s_waitcnt lgkmcnt(0)
	v_mfma_f32_16x16x128_f8f6f4 v[66:69], v[10:17], v[34:41], v[66:69]
	v_mfma_f32_16x16x128_f8f6f4 v[70:73], v[18:25], v[34:41], v[70:73]
	v_mfma_f32_16x16x128_f8f6f4 v[74:77], v[10:17], v[42:49], v[74:77]
	v_mfma_f32_16x16x128_f8f6f4 v[78:81], v[18:25], v[42:49], v[78:81]
	v_mfma_f32_16x16x128_f8f6f4 v[82:85], v[10:17], v[50:57], v[82:85]
	v_mfma_f32_16x16x128_f8f6f4 v[86:89], v[18:25], v[50:57], v[86:89]
	v_mfma_f32_16x16x128_f8f6f4 v[94:97], v[10:17], v[58:65], v[94:97]
	v_mfma_f32_16x16x128_f8f6f4 v[98:101], v[18:25], v[58:65], v[98:101]
	s_setprio 0
	s_setprio 1
	v_mfma_f32_16x16x128_f8f6f4 v[110:113], v[2:9], v[34:41], v[110:113]
	v_mfma_f32_16x16x128_f8f6f4 v[118:121], v[26:33], v[34:41], v[118:121]
	v_mfma_f32_16x16x128_f8f6f4 v[126:129], v[2:9], v[42:49], v[126:129]
	v_mfma_f32_16x16x128_f8f6f4 v[134:137], v[26:33], v[42:49], v[134:137]
	v_mfma_f32_16x16x128_f8f6f4 v[142:145], v[2:9], v[50:57], v[142:145]
	v_mfma_f32_16x16x128_f8f6f4 v[150:153], v[26:33], v[50:57], v[150:153]
	v_mfma_f32_16x16x128_f8f6f4 v[154:157], v[2:9], v[58:65], v[154:157]
	v_mfma_f32_16x16x128_f8f6f4 v[158:161], v[26:33], v[58:65], v[158:161]
	s_setprio 0
	s_barrier
	s_add_i32 s35, s9, 2
	s_cmp_gt_u32 s9, 13
	s_cbranch_scc1 .LBB0_1301
	s_mov_b32 s9, s35
	s_branch .LBB0_1277

.LBB0_1398:
	v_mov_b32_e32 v207, v205
	v_lshl_add_u64 v[230:231], s[48:49], 0, v[204:205]
	v_lshl_add_u64 v[232:233], s[48:49], 0, v[206:207]
	s_setprio 0
	s_barrier
	s_add_i32 s13, 0, 0x18000
	s_add_i32 s27, 0, 0x1c000
	v_add_u32_e32 v2, s13, v217
	v_add_u32_e32 v30, s27, v217
	ds_read_b128 v[10:13], v2
	ds_read_b128 v[14:17], v2 offset:1024
	ds_read_b128 v[18:21], v2 offset:2048
	ds_read_b128 v[22:25], v2 offset:3072
	ds_read_b128 v[2:5], v30
	ds_read_b128 v[6:9], v30 offset:1024
	ds_read_b128 v[26:29], v30 offset:2048
	ds_read_b128 v[30:33], v30 offset:3072
	s_mov_b32 m0, s66
	ds_read_b128 v[34:37], v237 offset:32768
	ds_read_b128 v[38:41], v237 offset:33792
	ds_read_b128 v[42:45], v237 offset:34816
	ds_read_b128 v[46:49], v237 offset:35840
	ds_read_b128 v[50:53], v237 offset:36864
	ds_read_b128 v[54:57], v237 offset:37888
	ds_read_b128 v[58:61], v237 offset:38912
	ds_read_b128 v[62:65], v237 offset:39936
	global_load_lds_dwordx4 v208, s[48:49]
	s_mov_b32 m0, s67
	s_nop 0
	global_load_lds_dwordx4 v210, s[48:49]
	s_waitcnt vmcnt(8)
	s_waitcnt lgkmcnt(0)
	s_barrier
	s_setprio 1
	s_waitcnt lgkmcnt(0)
	v_mfma_f32_16x16x128_f8f6f4 v[90:93], v[10:17], v[34:41], v[90:93]
	v_mfma_f32_16x16x128_f8f6f4 v[102:105], v[18:25], v[34:41], v[102:105]
	v_mfma_f32_16x16x128_f8f6f4 v[106:109], v[10:17], v[42:49], v[106:109]
	v_mfma_f32_16x16x128_f8f6f4 v[114:117], v[18:25], v[42:49], v[114:117]
	v_mfma_f32_16x16x128_f8f6f4 v[122:125], v[10:17], v[50:57], v[122:125]
	v_mfma_f32_16x16x128_f8f6f4 v[130:133], v[18:25], v[50:57], v[130:133]
	v_mfma_f32_16x16x128_f8f6f4 v[138:141], v[10:17], v[58:65], v[138:141]
	v_mfma_f32_16x16x128_f8f6f4 v[146:149], v[18:25], v[58:65], v[146:149]
	s_setprio 0
	s_setprio 1
	v_mfma_f32_16x16x128_f8f6f4 v[162:165], v[2:9], v[34:41], v[162:165]
	v_mfma_f32_16x16x128_f8f6f4 v[166:169], v[26:33], v[34:41], v[166:169]
	v_mfma_f32_16x16x128_f8f6f4 v[170:173], v[2:9], v[42:49], v[170:173]
	v_mfma_f32_16x16x128_f8f6f4 v[174:177], v[26:33], v[42:49], v[174:177]
	v_mfma_f32_16x16x128_f8f6f4 v[178:181], v[2:9], v[50:57], v[178:181]
	v_mfma_f32_16x16x128_f8f6f4 v[182:185], v[26:33], v[50:57], v[182:185]
	v_mfma_f32_16x16x128_f8f6f4 v[186:189], v[2:9], v[58:65], v[186:189]
	v_mfma_f32_16x16x128_f8f6f4 v[190:193], v[26:33], v[58:65], v[190:193]
	s_setprio 0
	s_barrier
	s_add_i32 s13, s13, s54
	v_lshl_add_u64 v[214:215], v[214:215], 0, s[14:15]
	s_mov_b32 m0, s13
	ds_read_b128 v[34:37], v237 offset:49152
	ds_read_b128 v[38:41], v237 offset:50176
	ds_read_b128 v[42:45], v237 offset:51200
	ds_read_b128 v[46:49], v237 offset:52224
	ds_read_b128 v[50:53], v237 offset:53248
	ds_read_b128 v[54:57], v237 offset:54272
	ds_read_b128 v[58:61], v237 offset:55296
	ds_read_b128 v[62:65], v237 offset:56320
	global_load_lds_dwordx4 v[214:215], off
	s_add_i32 m0, s13, 0x2000
	s_add_u32 s46, s46, 0x40080
	v_lshl_add_u64 v[212:213], v[212:213], 0, s[14:15]
	s_addc_u32 s47, s47, 0
	s_add_i32 s13, s27, s54
	global_load_lds_dwordx4 v[212:213], off
	v_lshl_add_u64 v[212:213], s[46:47], 0, v[198:199]
	s_mov_b32 m0, s13
	s_nop 0
	global_load_lds_dwordx4 v[212:213], off
	v_lshl_add_u64 v[212:213], s[46:47], 0, v[200:201]
	s_add_i32 m0, s13, 0x2000
	s_nop 0
	global_load_lds_dwordx4 v[212:213], off
	v_lshl_add_u64 v[212:213], v[230:231], 0, s[14:15]
	s_mov_b32 m0, s68
	s_nop 0
	global_load_lds_dwordx4 v[212:213], off
	v_lshl_add_u64 v[212:213], v[232:233], 0, s[14:15]
	s_mov_b32 m0, s69
	s_nop 0
	global_load_lds_dwordx4 v[212:213], off
	s_waitcnt vmcnt(8)
	s_waitcnt lgkmcnt(0)
	s_barrier
	s_setprio 1
	s_waitcnt lgkmcnt(0)
	v_mfma_f32_16x16x128_f8f6f4 v[66:69], v[10:17], v[34:41], v[66:69]
	v_mfma_f32_16x16x128_f8f6f4 v[70:73], v[18:25], v[34:41], v[70:73]
	v_mfma_f32_16x16x128_f8f6f4 v[74:77], v[10:17], v[42:49], v[74:77]
	v_mfma_f32_16x16x128_f8f6f4 v[78:81], v[18:25], v[42:49], v[78:81]
	v_mfma_f32_16x16x128_f8f6f4 v[82:85], v[10:17], v[50:57], v[82:85]
	v_mfma_f32_16x16x128_f8f6f4 v[86:89], v[18:25], v[50:57], v[86:89]
	v_mfma_f32_16x16x128_f8f6f4 v[94:97], v[10:17], v[58:65], v[94:97]
	v_mfma_f32_16x16x128_f8f6f4 v[98:101], v[18:25], v[58:65], v[98:101]
	s_setprio 0
	s_setprio 1
	v_mfma_f32_16x16x128_f8f6f4 v[110:113], v[2:9], v[34:41], v[110:113]
	v_mfma_f32_16x16x128_f8f6f4 v[118:121], v[26:33], v[34:41], v[118:121]
	v_mfma_f32_16x16x128_f8f6f4 v[126:129], v[2:9], v[42:49], v[126:129]
	v_mfma_f32_16x16x128_f8f6f4 v[134:137], v[26:33], v[42:49], v[134:137]
	v_mfma_f32_16x16x128_f8f6f4 v[142:145], v[2:9], v[50:57], v[142:145]
	v_mfma_f32_16x16x128_f8f6f4 v[150:153], v[26:33], v[50:57], v[150:153]
	v_mfma_f32_16x16x128_f8f6f4 v[154:157], v[2:9], v[58:65], v[154:157]
	v_mfma_f32_16x16x128_f8f6f4 v[158:161], v[26:33], v[58:65], v[158:161]
	s_setprio 0
	s_barrier
	s_add_i32 s13, s5, 2
	s_cmp_gt_u32 s5, 13
	s_cbranch_scc1 .LBB0_1402
	s_mov_b32 s5, s13
	s_branch .LBB0_1378

.LBB0_1523:
	s_setprio 0
	s_barrier
	s_add_i32 s23, 0, 0x18000
	s_add_i32 s48, 0, 0x1c000
	v_add_u32_e32 v2, s23, v216
	v_add_u32_e32 v22, s48, v216
	ds_read_b128 v[10:13], v2
	ds_read_b128 v[14:17], v2 offset:1024
	ds_read_b128 v[26:29], v2 offset:2048
	ds_read_b128 v[30:33], v2 offset:3072
	ds_read_b128 v[2:5], v22
	ds_read_b128 v[6:9], v22 offset:1024
	ds_read_b128 v[18:21], v22 offset:2048
	ds_read_b128 v[22:25], v22 offset:3072
	s_add_u32 s46, s46, 0x40000
	s_addc_u32 s47, s47, 0
	s_mov_b32 m0, s69
	v_lshl_add_u64 v[230:231], s[46:47], 0, v[198:199]
	ds_read_b128 v[34:37], v228 offset:32768
	ds_read_b128 v[38:41], v228 offset:33792
	ds_read_b128 v[42:45], v228 offset:34816
	ds_read_b128 v[46:49], v228 offset:35840
	ds_read_b128 v[50:53], v228 offset:36864
	ds_read_b128 v[54:57], v228 offset:37888
	ds_read_b128 v[58:61], v228 offset:38912
	ds_read_b128 v[62:65], v228 offset:39936
	global_load_lds_dwordx4 v[230:231], off
	v_lshl_add_u64 v[230:231], s[46:47], 0, v[202:203]
	s_mov_b32 m0, s70
	s_nop 0
	global_load_lds_dwordx4 v[230:231], off
	s_waitcnt vmcnt(8)
	s_waitcnt lgkmcnt(0)
	s_barrier
	s_setprio 1
	s_waitcnt lgkmcnt(0)
	v_mfma_f32_16x16x128_f8f6f4 v[90:93], v[10:17], v[34:41], v[90:93]
	v_mfma_f32_16x16x128_f8f6f4 v[102:105], v[26:33], v[34:41], v[102:105]
	v_mfma_f32_16x16x128_f8f6f4 v[106:109], v[10:17], v[42:49], v[106:109]
	v_mfma_f32_16x16x128_f8f6f4 v[114:117], v[26:33], v[42:49], v[114:117]
	v_mfma_f32_16x16x128_f8f6f4 v[122:125], v[10:17], v[50:57], v[122:125]
	v_mfma_f32_16x16x128_f8f6f4 v[130:133], v[26:33], v[50:57], v[130:133]
	v_mfma_f32_16x16x128_f8f6f4 v[138:141], v[10:17], v[58:65], v[138:141]
	v_mfma_f32_16x16x128_f8f6f4 v[146:149], v[26:33], v[58:65], v[146:149]
	s_setprio 0
	s_setprio 1
	v_mfma_f32_16x16x128_f8f6f4 v[162:165], v[2:9], v[34:41], v[162:165]
	v_mfma_f32_16x16x128_f8f6f4 v[166:169], v[18:25], v[34:41], v[166:169]
	v_mfma_f32_16x16x128_f8f6f4 v[170:173], v[2:9], v[42:49], v[170:173]
	v_mfma_f32_16x16x128_f8f6f4 v[174:177], v[18:25], v[42:49], v[174:177]
	v_mfma_f32_16x16x128_f8f6f4 v[178:181], v[2:9], v[50:57], v[178:181]
	v_mfma_f32_16x16x128_f8f6f4 v[182:185], v[18:25], v[50:57], v[182:185]
	v_mfma_f32_16x16x128_f8f6f4 v[186:189], v[2:9], v[58:65], v[186:189]
	v_mfma_f32_16x16x128_f8f6f4 v[190:193], v[18:25], v[58:65], v[190:193]
	s_setprio 0
	s_barrier
	s_add_i32 s23, s23, s62
	v_lshl_add_u64 v[212:213], v[212:213], 0, s[14:15]
	s_mov_b32 m0, s23
	ds_read_b128 v[34:37], v228 offset:49152
	ds_read_b128 v[38:41], v228 offset:50176
	ds_read_b128 v[42:45], v228 offset:51200
	ds_read_b128 v[46:49], v228 offset:52224
	ds_read_b128 v[50:53], v228 offset:53248
	ds_read_b128 v[54:57], v228 offset:54272
	ds_read_b128 v[58:61], v228 offset:55296
	ds_read_b128 v[62:65], v228 offset:56320
	global_load_lds_dwordx4 v[212:213], off
	s_add_i32 m0, s23, 0x2000
	s_add_u32 s44, s44, 0x40080
	v_lshl_add_u64 v[210:211], v[210:211], 0, s[14:15]
	s_addc_u32 s45, s45, 0
	s_add_i32 s23, s48, s62
	global_load_lds_dwordx4 v[210:211], off
	v_lshl_add_u64 v[210:211], s[44:45], 0, v[200:201]
	s_mov_b32 m0, s23
	v_lshl_add_u64 v[206:207], v[206:207], 0, s[14:15]
	global_load_lds_dwordx4 v[210:211], off
	v_lshl_add_u64 v[210:211], s[44:45], 0, v[204:205]
	s_add_i32 m0, s23, 0x2000
	s_nop 0
	global_load_lds_dwordx4 v[210:211], off
	s_mov_b32 m0, s71
	s_nop 0
	global_load_lds_dwordx4 v[206:207], off
	v_lshl_add_u64 v[206:207], v[208:209], 0, s[14:15]
	s_mov_b32 m0, s72
	s_nop 0
	global_load_lds_dwordx4 v[206:207], off
	s_waitcnt vmcnt(8)
	s_waitcnt lgkmcnt(0)
	s_barrier
	s_setprio 1
	s_waitcnt lgkmcnt(0)
	v_mfma_f32_16x16x128_f8f6f4 v[66:69], v[10:17], v[34:41], v[66:69]
	v_mfma_f32_16x16x128_f8f6f4 v[70:73], v[26:33], v[34:41], v[70:73]
	v_mfma_f32_16x16x128_f8f6f4 v[74:77], v[10:17], v[42:49], v[74:77]
	v_mfma_f32_16x16x128_f8f6f4 v[78:81], v[26:33], v[42:49], v[78:81]
	v_mfma_f32_16x16x128_f8f6f4 v[82:85], v[10:17], v[50:57], v[82:85]
	v_mfma_f32_16x16x128_f8f6f4 v[86:89], v[26:33], v[50:57], v[86:89]
	v_mfma_f32_16x16x128_f8f6f4 v[94:97], v[10:17], v[58:65], v[94:97]
	v_mfma_f32_16x16x128_f8f6f4 v[98:101], v[26:33], v[58:65], v[98:101]
	s_setprio 0
	s_setprio 1
	v_mfma_f32_16x16x128_f8f6f4 v[110:113], v[2:9], v[34:41], v[110:113]
	v_mfma_f32_16x16x128_f8f6f4 v[118:121], v[18:25], v[34:41], v[118:121]
	v_mfma_f32_16x16x128_f8f6f4 v[126:129], v[2:9], v[42:49], v[126:129]
	v_mfma_f32_16x16x128_f8f6f4 v[134:137], v[18:25], v[42:49], v[134:137]
	v_mfma_f32_16x16x128_f8f6f4 v[142:145], v[2:9], v[50:57], v[142:145]
	v_mfma_f32_16x16x128_f8f6f4 v[150:153], v[18:25], v[50:57], v[150:153]
	v_mfma_f32_16x16x128_f8f6f4 v[154:157], v[2:9], v[58:65], v[154:157]
	v_mfma_f32_16x16x128_f8f6f4 v[158:161], v[18:25], v[58:65], v[158:161]
	s_setprio 0
	s_barrier
	s_add_i32 s23, s21, 2
	s_cmp_gt_u32 s21, 13
	s_cbranch_scc1 .LBB0_1527
	s_mov_b32 s21, s23
	s_branch .LBB0_1505

.LBB0_1529:
	s_ashr_i32 s23, s22, 31
	s_lshl_b64 s[22:23], s[22:23], 13
	s_add_u32 s28, s88, s22
	s_addc_u32 s29, s89, s23
	s_ashr_i32 s21, s20, 31
	s_lshl_b64 s[22:23], s[20:21], 2
	s_add_u32 s21, s28, s22
	v_add_u32_e32 v22, s8, v215
	s_addc_u32 s23, s29, s23
	v_add_u32_e32 v18, 16, v22
	s_add_u32 s22, s21, s55
	v_ashrrev_i32_e32 v19, 31, v18
	s_addc_u32 s23, s23, 0
	v_lshlrev_b32_e32 v6, 2, v214
	v_lshl_add_u64 v[18:19], v[18:19], 2, s[6:7]
	global_load_dwordx4 v[10:13], v6, s[22:23] offset:16
	global_load_dwordx4 v[14:17], v6, s[22:23]
	global_load_dwordx4 v[2:5], v6, s[22:23] offset:528
	s_nop 0
	global_load_dwordx4 v[6:9], v6, s[22:23] offset:512
	v_add_u32_e32 v20, s20, v217
	global_load_dword v30, v[18:19], off
	v_add_u32_e32 v18, 32, v22
	v_ashrrev_i32_e32 v19, 31, v18
	v_lshl_add_u64 v[18:19], v[18:19], 2, s[6:7]
	global_load_dword v29, v[18:19], off
	v_add_u32_e32 v18, 48, v22
	v_ashrrev_i32_e32 v19, 31, v18
	v_lshl_add_u64 v[18:19], v[18:19], 2, s[6:7]
	global_load_dword v28, v[18:19], off
	v_add_u32_e32 v18, 0x80, v22
	v_ashrrev_i32_e32 v19, 31, v18
	v_lshl_add_u64 v[18:19], v[18:19], 2, s[6:7]
	global_load_dword v27, v[18:19], off
	v_add_u32_e32 v18, 0x90, v22
	v_ashrrev_i32_e32 v19, 31, v18
	v_lshl_add_u64 v[18:19], v[18:19], 2, s[6:7]
	global_load_dword v26, v[18:19], off
	v_add_u32_e32 v18, 0xa0, v22
	v_ashrrev_i32_e32 v19, 31, v18
	v_lshl_add_u64 v[18:19], v[18:19], 2, s[6:7]
	global_load_dword v25, v[18:19], off
	v_add_u32_e32 v18, 0xb0, v22
	v_ashrrev_i32_e32 v19, 31, v18
	v_lshl_add_u64 v[18:19], v[18:19], 2, s[6:7]
	global_load_dword v24, v[18:19], off
	v_add_u32_e32 v18, s20, v218
	v_cmp_gt_i32_e32 vcc, s9, v215
	v_ashrrev_i32_e32 v21, 31, v20
	v_ashrrev_i32_e32 v19, 31, v18
	v_ashrrev_i32_e32 v23, 31, v22
	v_lshl_add_u64 v[32:33], v[22:23], 2, s[6:7]
	global_load_dword v31, v[32:33], off
	s_waitcnt vmcnt(0)
	s_and_saveexec_b64 s[20:21], vcc
	s_cbranch_execz .LBB0_1538
	v_mov_b32_e32 v32, 0
	v_mov_b32_e32 v33, 0
	v_mov_b32_e32 v34, 0
	v_mov_b32_e32 v35, 0
	v_lshlrev_b64 v[22:23], 11, v[22:23]
	v_lshl_add_u64 v[22:23], s[24:25], 0, v[22:23]
	v_mul_f32_e32 v36, 0x41800000, v31
	v_mul_f32_e32 v38, 0x3c800000, v36
	v_pk_mul_f32 v[42:43], v[90:91], v[38:39] op_sel_hi:[1,0]
	v_pk_mul_f32 v[46:47], v[102:103], v[38:39] op_sel_hi:[1,0]
	v_pk_mul_f32 v[40:41], v[92:93], v[38:39] op_sel_hi:[1,0]
	v_pk_mul_f32 v[44:45], v[104:105], v[38:39] op_sel_hi:[1,0]
	v_pk_mul_f32 v[48:49], v[164:165], v[38:39] op_sel_hi:[1,0]
	v_pk_mul_f32 v[50:51], v[162:163], v[38:39] op_sel_hi:[1,0]
	v_pk_mul_f32 v[52:53], v[168:169], v[38:39] op_sel_hi:[1,0]
	v_pk_mul_f32 v[38:39], v[166:167], v[38:39] op_sel_hi:[1,0]
	v_pk_fma_f32 v[42:43], v[14:15], v[36:37], v[42:43] op_sel_hi:[1,0,1]
	v_pk_fma_f32 v[46:47], v[10:11], v[36:37], v[46:47] op_sel_hi:[1,0,1]
	v_pk_fma_f32 v[40:41], v[16:17], v[36:37], v[40:41] op_sel_hi:[1,0,1]
	v_pk_fma_f32 v[44:45], v[12:13], v[36:37], v[44:45] op_sel_hi:[1,0,1]
	v_pk_fma_f32 v[48:49], v[8:9], v[36:37], v[48:49] op_sel_hi:[1,0,1]
	v_pk_fma_f32 v[50:51], v[6:7], v[36:37], v[50:51] op_sel_hi:[1,0,1]
	v_pk_fma_f32 v[52:53], v[4:5], v[36:37], v[52:53] op_sel_hi:[1,0,1]
	v_pk_fma_f32 v[36:37], v[2:3], v[36:37], v[38:39] op_sel_hi:[1,0,1]
	v_cvt_pk_fp8_f32 v32, v42, v43
	v_cvt_pk_fp8_f32 v33, v46, v47
	v_cvt_pk_fp8_f32 v34, v50, v51
	v_cvt_pk_fp8_f32 v35, v36, v37
	v_cvt_pk_fp8_f32 v32, v40, v41 op_sel:[0,0,1]
	v_cvt_pk_fp8_f32 v33, v44, v45 op_sel:[0,0,1]
	v_cvt_pk_fp8_f32 v34, v48, v49 op_sel:[0,0,1]
	v_cvt_pk_fp8_f32 v35, v52, v53 op_sel:[0,0,1]
	v_lshl_add_u64 v[36:37], v[22:23], 0, v[20:21]
	v_lshl_add_u64 v[22:23], v[22:23], 0, v[18:19]
	global_store_dwordx2 v[36:37], v[32:33], off
	global_store_dwordx2 v[22:23], v[34:35], off
	s_or_b64 exec, exec, s[20:21]
	v_cmp_gt_i32_e32 vcc, s9, v219
	s_and_saveexec_b64 s[20:21], vcc
	s_cbranch_execnz .LBB0_1539

.LBB0_1532:
	v_mul_f32_e32 v22, 0x41800000, v29
	v_mul_f32_e32 v30, 0x3c800000, v22
	v_pk_mul_f32 v[34:35], v[122:123], v[30:31] op_sel_hi:[1,0]
	v_pk_mul_f32 v[36:37], v[130:131], v[30:31] op_sel_hi:[1,0]
	v_pk_fma_f32 v[34:35], v[14:15], v[22:23], v[34:35] op_sel_hi:[1,0,1]
	v_pk_fma_f32 v[36:37], v[10:11], v[22:23], v[36:37] op_sel_hi:[1,0,1]
	v_mov_b32_e32 v38, 0
	v_mov_b32_e32 v39, 0
	v_cvt_pk_fp8_f32 v38, v34, v35
	v_cvt_pk_fp8_f32 v39, v36, v37
	v_pk_mul_f32 v[36:37], v[178:179], v[30:31] op_sel_hi:[1,0]
	v_pk_mul_f32 v[40:41], v[182:183], v[30:31] op_sel_hi:[1,0]
	v_pk_fma_f32 v[36:37], v[6:7], v[22:23], v[36:37] op_sel_hi:[1,0,1]
	v_pk_fma_f32 v[40:41], v[2:3], v[22:23], v[40:41] op_sel_hi:[1,0,1]
	v_mov_b32_e32 v42, 0
	v_mov_b32_e32 v43, 0
	v_pk_mul_f32 v[32:33], v[124:125], v[30:31] op_sel_hi:[1,0]
	v_pk_mul_f32 v[34:35], v[132:133], v[30:31] op_sel_hi:[1,0]
	v_cvt_pk_fp8_f32 v42, v36, v37
	v_cvt_pk_fp8_f32 v43, v40, v41
	v_pk_fma_f32 v[32:33], v[16:17], v[22:23], v[32:33] op_sel_hi:[1,0,1]
	v_pk_fma_f32 v[34:35], v[12:13], v[22:23], v[34:35] op_sel_hi:[1,0,1]
	v_cvt_pk_fp8_f32 v38, v32, v33 op_sel:[0,0,1]
	v_cvt_pk_fp8_f32 v39, v34, v35 op_sel:[0,0,1]
	v_add_u32_e32 v32, s8, v220
	v_pk_mul_f32 v[34:35], v[180:181], v[30:31] op_sel_hi:[1,0]
	v_pk_mul_f32 v[30:31], v[184:185], v[30:31] op_sel_hi:[1,0]
	v_ashrrev_i32_e32 v33, 31, v32
	v_pk_fma_f32 v[34:35], v[8:9], v[22:23], v[34:35] op_sel_hi:[1,0,1]
	v_pk_fma_f32 v[22:23], v[4:5], v[22:23], v[30:31] op_sel_hi:[1,0,1]
	v_lshlrev_b64 v[32:33], 11, v[32:33]
	v_cvt_pk_fp8_f32 v42, v34, v35 op_sel:[0,0,1]
	v_cvt_pk_fp8_f32 v43, v22, v23 op_sel:[0,0,1]
	v_lshl_add_u64 v[32:33], s[24:25], 0, v[32:33]
	v_lshl_add_u64 v[22:23], v[32:33], 0, v[20:21]
	global_store_dwordx2 v[22:23], v[38:39], off
	v_lshl_add_u64 v[22:23], v[32:33], 0, v[18:19]
	global_store_dwordx2 v[22:23], v[42:43], off
	s_or_b64 exec, exec, s[20:21]
	v_cmp_gt_i32_e32 vcc, s9, v221
	s_and_saveexec_b64 s[20:21], vcc
	s_cbranch_execnz .LBB0_1541

.LBB0_1534:
	v_mul_f32_e32 v22, 0x41800000, v27
	v_mul_f32_e32 v28, 0x3c800000, v22
	v_pk_mul_f32 v[32:33], v[66:67], v[28:29] op_sel_hi:[1,0]
	v_pk_mul_f32 v[34:35], v[70:71], v[28:29] op_sel_hi:[1,0]
	v_pk_fma_f32 v[32:33], v[14:15], v[22:23], v[32:33] op_sel_hi:[1,0,1]
	v_pk_fma_f32 v[34:35], v[10:11], v[22:23], v[34:35] op_sel_hi:[1,0,1]
	v_mov_b32_e32 v36, 0
	v_mov_b32_e32 v37, 0
	v_cvt_pk_fp8_f32 v36, v32, v33
	v_cvt_pk_fp8_f32 v37, v34, v35
	v_pk_mul_f32 v[34:35], v[110:111], v[28:29] op_sel_hi:[1,0]
	v_pk_mul_f32 v[38:39], v[118:119], v[28:29] op_sel_hi:[1,0]
	v_pk_fma_f32 v[34:35], v[6:7], v[22:23], v[34:35] op_sel_hi:[1,0,1]
	v_pk_fma_f32 v[38:39], v[2:3], v[22:23], v[38:39] op_sel_hi:[1,0,1]
	v_mov_b32_e32 v40, 0
	v_mov_b32_e32 v41, 0
	v_pk_mul_f32 v[30:31], v[68:69], v[28:29] op_sel_hi:[1,0]
	v_pk_mul_f32 v[32:33], v[72:73], v[28:29] op_sel_hi:[1,0]
	v_cvt_pk_fp8_f32 v40, v34, v35
	v_cvt_pk_fp8_f32 v41, v38, v39
	v_pk_fma_f32 v[30:31], v[16:17], v[22:23], v[30:31] op_sel_hi:[1,0,1]
	v_pk_fma_f32 v[32:33], v[12:13], v[22:23], v[32:33] op_sel_hi:[1,0,1]
	v_cvt_pk_fp8_f32 v36, v30, v31 op_sel:[0,0,1]
	v_cvt_pk_fp8_f32 v37, v32, v33 op_sel:[0,0,1]
	v_add_u32_e32 v30, s8, v222
	v_pk_mul_f32 v[32:33], v[112:113], v[28:29] op_sel_hi:[1,0]
	v_pk_mul_f32 v[28:29], v[120:121], v[28:29] op_sel_hi:[1,0]
	v_ashrrev_i32_e32 v31, 31, v30
	v_pk_fma_f32 v[32:33], v[8:9], v[22:23], v[32:33] op_sel_hi:[1,0,1]
	v_pk_fma_f32 v[22:23], v[4:5], v[22:23], v[28:29] op_sel_hi:[1,0,1]
	v_lshlrev_b64 v[30:31], 11, v[30:31]
	v_cvt_pk_fp8_f32 v40, v32, v33 op_sel:[0,0,1]
	v_cvt_pk_fp8_f32 v41, v22, v23 op_sel:[0,0,1]
	v_lshl_add_u64 v[30:31], s[24:25], 0, v[30:31]
	v_lshl_add_u64 v[22:23], v[30:31], 0, v[20:21]
	global_store_dwordx2 v[22:23], v[36:37], off
	v_lshl_add_u64 v[22:23], v[30:31], 0, v[18:19]
	global_store_dwordx2 v[22:23], v[40:41], off
	s_or_b64 exec, exec, s[20:21]
	v_cmp_gt_i32_e32 vcc, s9, v223
	s_and_saveexec_b64 s[20:21], vcc
	s_cbranch_execnz .LBB0_1543

.LBB0_1536:
	v_mul_f32_e32 v22, 0x41800000, v25
	v_mul_f32_e32 v26, 0x3c800000, v22
	v_pk_mul_f32 v[30:31], v[82:83], v[26:27] op_sel_hi:[1,0]
	v_pk_mul_f32 v[32:33], v[86:87], v[26:27] op_sel_hi:[1,0]
	v_pk_fma_f32 v[30:31], v[14:15], v[22:23], v[30:31] op_sel_hi:[1,0,1]
	v_pk_fma_f32 v[32:33], v[10:11], v[22:23], v[32:33] op_sel_hi:[1,0,1]
	v_mov_b32_e32 v34, 0
	v_mov_b32_e32 v35, 0
	v_cvt_pk_fp8_f32 v34, v30, v31
	v_cvt_pk_fp8_f32 v35, v32, v33
	v_pk_mul_f32 v[32:33], v[142:143], v[26:27] op_sel_hi:[1,0]
	v_pk_mul_f32 v[36:37], v[150:151], v[26:27] op_sel_hi:[1,0]
	v_pk_fma_f32 v[32:33], v[6:7], v[22:23], v[32:33] op_sel_hi:[1,0,1]
	v_pk_fma_f32 v[36:37], v[2:3], v[22:23], v[36:37] op_sel_hi:[1,0,1]
	v_mov_b32_e32 v38, 0
	v_mov_b32_e32 v39, 0
	v_pk_mul_f32 v[28:29], v[84:85], v[26:27] op_sel_hi:[1,0]
	v_pk_mul_f32 v[30:31], v[88:89], v[26:27] op_sel_hi:[1,0]
	v_cvt_pk_fp8_f32 v38, v32, v33
	v_cvt_pk_fp8_f32 v39, v36, v37
	v_pk_fma_f32 v[28:29], v[16:17], v[22:23], v[28:29] op_sel_hi:[1,0,1]
	v_pk_fma_f32 v[30:31], v[12:13], v[22:23], v[30:31] op_sel_hi:[1,0,1]
	v_cvt_pk_fp8_f32 v34, v28, v29 op_sel:[0,0,1]
	v_cvt_pk_fp8_f32 v35, v30, v31 op_sel:[0,0,1]
	v_add_u32_e32 v28, s8, v224
	v_pk_mul_f32 v[30:31], v[144:145], v[26:27] op_sel_hi:[1,0]
	v_pk_mul_f32 v[26:27], v[152:153], v[26:27] op_sel_hi:[1,0]
	v_ashrrev_i32_e32 v29, 31, v28
	v_pk_fma_f32 v[30:31], v[8:9], v[22:23], v[30:31] op_sel_hi:[1,0,1]
	v_pk_fma_f32 v[22:23], v[4:5], v[22:23], v[26:27] op_sel_hi:[1,0,1]
	v_lshlrev_b64 v[28:29], 11, v[28:29]
	v_cvt_pk_fp8_f32 v38, v30, v31 op_sel:[0,0,1]
	v_cvt_pk_fp8_f32 v39, v22, v23 op_sel:[0,0,1]
	v_lshl_add_u64 v[28:29], s[24:25], 0, v[28:29]
	v_lshl_add_u64 v[22:23], v[28:29], 0, v[20:21]
	global_store_dwordx2 v[22:23], v[34:35], off
	v_lshl_add_u64 v[22:23], v[28:29], 0, v[18:19]
	global_store_dwordx2 v[22:23], v[38:39], off
	s_or_b64 exec, exec, s[20:21]
	v_cmp_gt_i32_e32 vcc, s9, v225
	s_and_saveexec_b64 s[20:21], vcc
	s_cbranch_execnz .LBB0_1545

.LBB0_1539:
	v_mul_f32_e32 v22, 0x41800000, v30
	v_mul_f32_e32 v30, 0x3c800000, v22
	v_pk_mul_f32 v[34:35], v[106:107], v[30:31] op_sel_hi:[1,0]
	v_pk_mul_f32 v[36:37], v[114:115], v[30:31] op_sel_hi:[1,0]
	v_pk_fma_f32 v[34:35], v[14:15], v[22:23], v[34:35] op_sel_hi:[1,0,1]
	v_pk_fma_f32 v[36:37], v[10:11], v[22:23], v[36:37] op_sel_hi:[1,0,1]
	v_mov_b32_e32 v38, 0
	v_mov_b32_e32 v39, 0
	v_cvt_pk_fp8_f32 v38, v34, v35
	v_cvt_pk_fp8_f32 v39, v36, v37
	v_pk_mul_f32 v[36:37], v[170:171], v[30:31] op_sel_hi:[1,0]
	v_pk_mul_f32 v[40:41], v[174:175], v[30:31] op_sel_hi:[1,0]
	v_pk_fma_f32 v[36:37], v[6:7], v[22:23], v[36:37] op_sel_hi:[1,0,1]
	v_pk_fma_f32 v[40:41], v[2:3], v[22:23], v[40:41] op_sel_hi:[1,0,1]
	v_mov_b32_e32 v42, 0
	v_mov_b32_e32 v43, 0
	v_pk_mul_f32 v[32:33], v[108:109], v[30:31] op_sel_hi:[1,0]
	v_pk_mul_f32 v[34:35], v[116:117], v[30:31] op_sel_hi:[1,0]
	v_cvt_pk_fp8_f32 v42, v36, v37
	v_cvt_pk_fp8_f32 v43, v40, v41
	v_pk_fma_f32 v[32:33], v[16:17], v[22:23], v[32:33] op_sel_hi:[1,0,1]
	v_pk_fma_f32 v[34:35], v[12:13], v[22:23], v[34:35] op_sel_hi:[1,0,1]
	v_cvt_pk_fp8_f32 v38, v32, v33 op_sel:[0,0,1]
	v_cvt_pk_fp8_f32 v39, v34, v35 op_sel:[0,0,1]
	v_add_u32_e32 v32, s8, v219
	v_pk_mul_f32 v[34:35], v[172:173], v[30:31] op_sel_hi:[1,0]
	v_pk_mul_f32 v[30:31], v[176:177], v[30:31] op_sel_hi:[1,0]
	v_ashrrev_i32_e32 v33, 31, v32
	v_pk_fma_f32 v[34:35], v[8:9], v[22:23], v[34:35] op_sel_hi:[1,0,1]
	v_pk_fma_f32 v[22:23], v[4:5], v[22:23], v[30:31] op_sel_hi:[1,0,1]
	v_lshlrev_b64 v[32:33], 11, v[32:33]
	v_cvt_pk_fp8_f32 v42, v34, v35 op_sel:[0,0,1]
	v_cvt_pk_fp8_f32 v43, v22, v23 op_sel:[0,0,1]
	v_lshl_add_u64 v[32:33], s[24:25], 0, v[32:33]
	v_lshl_add_u64 v[22:23], v[32:33], 0, v[20:21]
	global_store_dwordx2 v[22:23], v[38:39], off
	v_lshl_add_u64 v[22:23], v[32:33], 0, v[18:19]
	global_store_dwordx2 v[22:23], v[42:43], off
	s_or_b64 exec, exec, s[20:21]
	v_cmp_gt_i32_e32 vcc, s9, v220
	s_and_saveexec_b64 s[20:21], vcc
	s_cbranch_execnz .LBB0_1532

.LBB0_1541:
	v_mul_f32_e32 v22, 0x41800000, v28
	v_mul_f32_e32 v28, 0x3c800000, v22
	v_pk_mul_f32 v[32:33], v[138:139], v[28:29] op_sel_hi:[1,0]
	v_pk_mul_f32 v[34:35], v[146:147], v[28:29] op_sel_hi:[1,0]
	v_pk_fma_f32 v[32:33], v[14:15], v[22:23], v[32:33] op_sel_hi:[1,0,1]
	v_pk_fma_f32 v[34:35], v[10:11], v[22:23], v[34:35] op_sel_hi:[1,0,1]
	v_mov_b32_e32 v36, 0
	v_mov_b32_e32 v37, 0
	v_cvt_pk_fp8_f32 v36, v32, v33
	v_cvt_pk_fp8_f32 v37, v34, v35
	v_pk_mul_f32 v[34:35], v[186:187], v[28:29] op_sel_hi:[1,0]
	v_pk_mul_f32 v[38:39], v[190:191], v[28:29] op_sel_hi:[1,0]
	v_pk_fma_f32 v[34:35], v[6:7], v[22:23], v[34:35] op_sel_hi:[1,0,1]
	v_pk_fma_f32 v[38:39], v[2:3], v[22:23], v[38:39] op_sel_hi:[1,0,1]
	v_mov_b32_e32 v40, 0
	v_mov_b32_e32 v41, 0
	v_pk_mul_f32 v[30:31], v[140:141], v[28:29] op_sel_hi:[1,0]
	v_pk_mul_f32 v[32:33], v[148:149], v[28:29] op_sel_hi:[1,0]
	v_cvt_pk_fp8_f32 v40, v34, v35
	v_cvt_pk_fp8_f32 v41, v38, v39
	v_pk_fma_f32 v[30:31], v[16:17], v[22:23], v[30:31] op_sel_hi:[1,0,1]
	v_pk_fma_f32 v[32:33], v[12:13], v[22:23], v[32:33] op_sel_hi:[1,0,1]
	v_cvt_pk_fp8_f32 v36, v30, v31 op_sel:[0,0,1]
	v_cvt_pk_fp8_f32 v37, v32, v33 op_sel:[0,0,1]
	v_add_u32_e32 v30, s8, v221
	v_pk_mul_f32 v[32:33], v[188:189], v[28:29] op_sel_hi:[1,0]
	v_pk_mul_f32 v[28:29], v[192:193], v[28:29] op_sel_hi:[1,0]
	v_ashrrev_i32_e32 v31, 31, v30
	v_pk_fma_f32 v[32:33], v[8:9], v[22:23], v[32:33] op_sel_hi:[1,0,1]
	v_pk_fma_f32 v[22:23], v[4:5], v[22:23], v[28:29] op_sel_hi:[1,0,1]
	v_lshlrev_b64 v[30:31], 11, v[30:31]
	v_cvt_pk_fp8_f32 v40, v32, v33 op_sel:[0,0,1]
	v_cvt_pk_fp8_f32 v41, v22, v23 op_sel:[0,0,1]
	v_lshl_add_u64 v[30:31], s[24:25], 0, v[30:31]
	v_lshl_add_u64 v[22:23], v[30:31], 0, v[20:21]
	global_store_dwordx2 v[22:23], v[36:37], off
	v_lshl_add_u64 v[22:23], v[30:31], 0, v[18:19]
	global_store_dwordx2 v[22:23], v[40:41], off
	s_or_b64 exec, exec, s[20:21]
	v_cmp_gt_i32_e32 vcc, s9, v222
	s_and_saveexec_b64 s[20:21], vcc
	s_cbranch_execnz .LBB0_1534

.LBB0_1543:
	v_mul_f32_e32 v22, 0x41800000, v26
	v_mul_f32_e32 v26, 0x3c800000, v22
	v_pk_mul_f32 v[30:31], v[74:75], v[26:27] op_sel_hi:[1,0]
	v_pk_mul_f32 v[32:33], v[78:79], v[26:27] op_sel_hi:[1,0]
	v_pk_fma_f32 v[30:31], v[14:15], v[22:23], v[30:31] op_sel_hi:[1,0,1]
	v_pk_fma_f32 v[32:33], v[10:11], v[22:23], v[32:33] op_sel_hi:[1,0,1]
	v_mov_b32_e32 v34, 0
	v_mov_b32_e32 v35, 0
	v_cvt_pk_fp8_f32 v34, v30, v31
	v_cvt_pk_fp8_f32 v35, v32, v33
	v_pk_mul_f32 v[32:33], v[126:127], v[26:27] op_sel_hi:[1,0]
	v_pk_mul_f32 v[36:37], v[134:135], v[26:27] op_sel_hi:[1,0]
	v_pk_fma_f32 v[32:33], v[6:7], v[22:23], v[32:33] op_sel_hi:[1,0,1]
	v_pk_fma_f32 v[36:37], v[2:3], v[22:23], v[36:37] op_sel_hi:[1,0,1]
	v_mov_b32_e32 v38, 0
	v_mov_b32_e32 v39, 0
	v_pk_mul_f32 v[28:29], v[76:77], v[26:27] op_sel_hi:[1,0]
	v_pk_mul_f32 v[30:31], v[80:81], v[26:27] op_sel_hi:[1,0]
	v_cvt_pk_fp8_f32 v38, v32, v33
	v_cvt_pk_fp8_f32 v39, v36, v37
	v_pk_fma_f32 v[28:29], v[16:17], v[22:23], v[28:29] op_sel_hi:[1,0,1]
	v_pk_fma_f32 v[30:31], v[12:13], v[22:23], v[30:31] op_sel_hi:[1,0,1]
	v_cvt_pk_fp8_f32 v34, v28, v29 op_sel:[0,0,1]
	v_cvt_pk_fp8_f32 v35, v30, v31 op_sel:[0,0,1]
	v_add_u32_e32 v28, s8, v223
	v_pk_mul_f32 v[30:31], v[128:129], v[26:27] op_sel_hi:[1,0]
	v_pk_mul_f32 v[26:27], v[136:137], v[26:27] op_sel_hi:[1,0]
	v_ashrrev_i32_e32 v29, 31, v28
	v_pk_fma_f32 v[30:31], v[8:9], v[22:23], v[30:31] op_sel_hi:[1,0,1]
	v_pk_fma_f32 v[22:23], v[4:5], v[22:23], v[26:27] op_sel_hi:[1,0,1]
	v_lshlrev_b64 v[28:29], 11, v[28:29]
	v_cvt_pk_fp8_f32 v38, v30, v31 op_sel:[0,0,1]
	v_cvt_pk_fp8_f32 v39, v22, v23 op_sel:[0,0,1]
	v_lshl_add_u64 v[28:29], s[24:25], 0, v[28:29]
	v_lshl_add_u64 v[22:23], v[28:29], 0, v[20:21]
	global_store_dwordx2 v[22:23], v[34:35], off
	v_lshl_add_u64 v[22:23], v[28:29], 0, v[18:19]
	global_store_dwordx2 v[22:23], v[38:39], off
	s_or_b64 exec, exec, s[20:21]
	v_cmp_gt_i32_e32 vcc, s9, v224
	s_and_saveexec_b64 s[20:21], vcc
	s_cbranch_execnz .LBB0_1536

.LBB0_1545:
	v_mul_f32_e32 v22, 0x41800000, v24
	v_mul_f32_e32 v24, 0x3c800000, v22
	v_pk_mul_f32 v[26:27], v[96:97], v[24:25] op_sel_hi:[1,0]
	v_pk_mul_f32 v[28:29], v[94:95], v[24:25] op_sel_hi:[1,0]
	v_pk_fma_f32 v[16:17], v[16:17], v[22:23], v[26:27] op_sel_hi:[1,0,1]
	v_pk_mul_f32 v[26:27], v[98:99], v[24:25] op_sel_hi:[1,0]
	v_pk_fma_f32 v[14:15], v[14:15], v[22:23], v[28:29] op_sel_hi:[1,0,1]
	v_pk_fma_f32 v[10:11], v[10:11], v[22:23], v[26:27] op_sel_hi:[1,0,1]
	v_mov_b32_e32 v27, 0
	v_cvt_pk_fp8_f32 v27, v10, v11
	v_pk_mul_f32 v[10:11], v[100:101], v[24:25] op_sel_hi:[1,0]
	v_mov_b32_e32 v26, 0
	v_pk_fma_f32 v[10:11], v[12:13], v[22:23], v[10:11] op_sel_hi:[1,0,1]
	v_pk_mul_f32 v[12:13], v[156:157], v[24:25] op_sel_hi:[1,0]
	v_cvt_pk_fp8_f32 v26, v14, v15
	v_pk_mul_f32 v[14:15], v[154:155], v[24:25] op_sel_hi:[1,0]
	v_pk_fma_f32 v[8:9], v[8:9], v[22:23], v[12:13] op_sel_hi:[1,0,1]
	v_pk_mul_f32 v[12:13], v[158:159], v[24:25] op_sel_hi:[1,0]
	v_pk_fma_f32 v[6:7], v[6:7], v[22:23], v[14:15] op_sel_hi:[1,0,1]
	v_pk_fma_f32 v[2:3], v[2:3], v[22:23], v[12:13] op_sel_hi:[1,0,1]
	v_mov_b32_e32 v12, 0
	v_mov_b32_e32 v13, 0
	v_cvt_pk_fp8_f32 v12, v6, v7
	v_cvt_pk_fp8_f32 v13, v2, v3
	v_cvt_pk_fp8_f32 v27, v10, v11 op_sel:[0,0,1]
	v_add_u32_e32 v10, s8, v225
	v_pk_mul_f32 v[2:3], v[160:161], v[24:25] op_sel_hi:[1,0]
	v_cvt_pk_fp8_f32 v26, v16, v17 op_sel:[0,0,1]
	v_ashrrev_i32_e32 v11, 31, v10
	v_pk_fma_f32 v[2:3], v[4:5], v[22:23], v[2:3] op_sel_hi:[1,0,1]
	v_lshlrev_b64 v[10:11], 11, v[10:11]
	v_cvt_pk_fp8_f32 v12, v8, v9 op_sel:[0,0,1]
	v_cvt_pk_fp8_f32 v13, v2, v3 op_sel:[0,0,1]
	v_lshl_add_u64 v[10:11], s[24:25], 0, v[10:11]
	v_lshl_add_u64 v[2:3], v[10:11], 0, v[20:21]
	global_store_dwordx2 v[2:3], v[26:27], off
	v_lshl_add_u64 v[2:3], v[10:11], 0, v[18:19]
	global_store_dwordx2 v[2:3], v[12:13], off
	s_or_b64 exec, exec, s[20:21]
	s_andn2_b64 vcc, exec, s[18:19]
	s_mov_b64 s[8:9], -1
	s_cbranch_vccnz .LBB0_1501

.LBB0_1626:
	s_setprio 0
	s_barrier
	s_add_i32 s23, 0, 0x18000
	s_add_i32 s29, 0, 0x1c000
	v_add_u32_e32 v2, s23, v1
	v_add_u32_e32 v22, s29, v1
	ds_read_b128 v[10:13], v2
	ds_read_b128 v[14:17], v2 offset:1024
	ds_read_b128 v[26:29], v2 offset:2048
	ds_read_b128 v[30:33], v2 offset:3072
	ds_read_b128 v[2:5], v22
	ds_read_b128 v[6:9], v22 offset:1024
	ds_read_b128 v[18:21], v22 offset:2048
	ds_read_b128 v[22:25], v22 offset:3072
	s_add_u32 s40, s40, 0x40000
	s_addc_u32 s41, s41, 0
	s_mov_b32 m0, s54
	v_lshl_add_u64 v[226:227], s[40:41], 0, v[198:199]
	ds_read_b128 v[34:37], v224 offset:32768
	ds_read_b128 v[38:41], v224 offset:33792
	ds_read_b128 v[42:45], v224 offset:34816
	ds_read_b128 v[46:49], v224 offset:35840
	ds_read_b128 v[50:53], v224 offset:36864
	ds_read_b128 v[54:57], v224 offset:37888
	ds_read_b128 v[58:61], v224 offset:38912
	ds_read_b128 v[62:65], v224 offset:39936
	global_load_lds_dwordx4 v[226:227], off
	v_lshl_add_u64 v[226:227], s[40:41], 0, v[202:203]
	s_mov_b32 m0, s55
	s_nop 0
	global_load_lds_dwordx4 v[226:227], off
	s_waitcnt vmcnt(8)
	s_waitcnt lgkmcnt(0)
	s_barrier
	s_setprio 1
	s_waitcnt lgkmcnt(0)
	v_mfma_f32_16x16x128_f8f6f4 v[90:93], v[10:17], v[34:41], v[90:93]
	v_mfma_f32_16x16x128_f8f6f4 v[102:105], v[26:33], v[34:41], v[102:105]
	v_mfma_f32_16x16x128_f8f6f4 v[106:109], v[10:17], v[42:49], v[106:109]
	v_mfma_f32_16x16x128_f8f6f4 v[114:117], v[26:33], v[42:49], v[114:117]
	v_mfma_f32_16x16x128_f8f6f4 v[122:125], v[10:17], v[50:57], v[122:125]
	v_mfma_f32_16x16x128_f8f6f4 v[130:133], v[26:33], v[50:57], v[130:133]
	v_mfma_f32_16x16x128_f8f6f4 v[138:141], v[10:17], v[58:65], v[138:141]
	v_mfma_f32_16x16x128_f8f6f4 v[146:149], v[26:33], v[58:65], v[146:149]
	s_setprio 0
	s_setprio 1
	v_mfma_f32_16x16x128_f8f6f4 v[162:165], v[2:9], v[34:41], v[162:165]
	v_mfma_f32_16x16x128_f8f6f4 v[166:169], v[18:25], v[34:41], v[166:169]
	v_mfma_f32_16x16x128_f8f6f4 v[170:173], v[2:9], v[42:49], v[170:173]
	v_mfma_f32_16x16x128_f8f6f4 v[174:177], v[18:25], v[42:49], v[174:177]
	v_mfma_f32_16x16x128_f8f6f4 v[178:181], v[2:9], v[50:57], v[178:181]
	v_mfma_f32_16x16x128_f8f6f4 v[182:185], v[18:25], v[50:57], v[182:185]
	v_mfma_f32_16x16x128_f8f6f4 v[186:189], v[2:9], v[58:65], v[186:189]
	v_mfma_f32_16x16x128_f8f6f4 v[190:193], v[18:25], v[58:65], v[190:193]
	s_setprio 0
	s_barrier
	s_add_i32 s23, s23, s3
	v_lshl_add_u64 v[210:211], v[210:211], 0, s[12:13]
	s_mov_b32 m0, s23
	ds_read_b128 v[34:37], v224 offset:49152
	ds_read_b128 v[38:41], v224 offset:50176
	ds_read_b128 v[42:45], v224 offset:51200
	ds_read_b128 v[46:49], v224 offset:52224
	ds_read_b128 v[50:53], v224 offset:53248
	ds_read_b128 v[54:57], v224 offset:54272
	ds_read_b128 v[58:61], v224 offset:55296
	ds_read_b128 v[62:65], v224 offset:56320
	global_load_lds_dwordx4 v[210:211], off
	s_add_i32 m0, s23, 0x2000
	s_add_u32 s38, s38, 0x40080
	v_lshl_add_u64 v[208:209], v[208:209], 0, s[12:13]
	s_addc_u32 s39, s39, 0
	s_add_i32 s23, s29, s3
	global_load_lds_dwordx4 v[208:209], off
	v_lshl_add_u64 v[208:209], s[38:39], 0, v[200:201]
	s_mov_b32 m0, s23
	v_lshl_add_u64 v[196:197], v[196:197], 0, s[12:13]
	global_load_lds_dwordx4 v[208:209], off
	v_lshl_add_u64 v[208:209], s[38:39], 0, v[204:205]
	s_add_i32 m0, s23, 0x2000
	s_nop 0
	global_load_lds_dwordx4 v[208:209], off
	s_mov_b32 m0, s57
	s_nop 0
	global_load_lds_dwordx4 v[196:197], off
	v_lshl_add_u64 v[196:197], v[206:207], 0, s[12:13]
	s_mov_b32 m0, s58
	s_nop 0
	global_load_lds_dwordx4 v[196:197], off
	s_waitcnt vmcnt(8)
	s_waitcnt lgkmcnt(0)
	s_barrier
	s_setprio 1
	s_waitcnt lgkmcnt(0)
	v_mfma_f32_16x16x128_f8f6f4 v[66:69], v[10:17], v[34:41], v[66:69]
	v_mfma_f32_16x16x128_f8f6f4 v[70:73], v[26:33], v[34:41], v[70:73]
	v_mfma_f32_16x16x128_f8f6f4 v[74:77], v[10:17], v[42:49], v[74:77]
	v_mfma_f32_16x16x128_f8f6f4 v[78:81], v[26:33], v[42:49], v[78:81]
	v_mfma_f32_16x16x128_f8f6f4 v[82:85], v[10:17], v[50:57], v[82:85]
	v_mfma_f32_16x16x128_f8f6f4 v[86:89], v[26:33], v[50:57], v[86:89]
	v_mfma_f32_16x16x128_f8f6f4 v[94:97], v[10:17], v[58:65], v[94:97]
	v_mfma_f32_16x16x128_f8f6f4 v[98:101], v[26:33], v[58:65], v[98:101]
	s_setprio 0
	s_setprio 1
	v_mfma_f32_16x16x128_f8f6f4 v[110:113], v[2:9], v[34:41], v[110:113]
	v_mfma_f32_16x16x128_f8f6f4 v[118:121], v[18:25], v[34:41], v[118:121]
	v_mfma_f32_16x16x128_f8f6f4 v[126:129], v[2:9], v[42:49], v[126:129]
	v_mfma_f32_16x16x128_f8f6f4 v[134:137], v[18:25], v[42:49], v[134:137]
	v_mfma_f32_16x16x128_f8f6f4 v[142:145], v[2:9], v[50:57], v[142:145]
	v_mfma_f32_16x16x128_f8f6f4 v[150:153], v[18:25], v[50:57], v[150:153]
	v_mfma_f32_16x16x128_f8f6f4 v[154:157], v[2:9], v[58:65], v[154:157]
	v_mfma_f32_16x16x128_f8f6f4 v[158:161], v[18:25], v[58:65], v[158:161]
	s_setprio 0
	s_barrier
	s_add_i32 s23, s5, 2
	s_cmp_gt_u32 s5, 13
	s_cbranch_scc1 .LBB0_1630
	s_mov_b32 s5, s23
	s_branch .LBB0_1608

.LBB0_1632:
	s_ashr_i32 s23, s22, 31
	s_lshl_b64 s[22:23], s[22:23], 13
	s_add_u32 s5, s88, s22
	v_add_u32_e32 v22, s4, v212
	s_addc_u32 s30, s89, s23
	s_ashr_i32 s29, s28, 31
	v_add_u32_e32 v28, 0x90, v22
	s_lshl_b64 s[22:23], s[28:29], 2
	v_ashrrev_i32_e32 v29, 31, v28
	s_add_u32 s5, s5, s22
	v_lshl_add_u64 v[32:33], v[28:29], 2, s[6:7]
	v_add_u32_e32 v28, 0xa0, v22
	s_addc_u32 s23, s30, s23
	v_add_u32_e32 v18, 16, v22
	v_add_u32_e32 v24, 48, v22
	v_add_u32_e32 v26, 0x80, v22
	v_ashrrev_i32_e32 v29, 31, v28
	s_add_u32 s22, s5, s75
	v_ashrrev_i32_e32 v19, 31, v18
	v_add_u32_e32 v20, 32, v22
	v_ashrrev_i32_e32 v25, 31, v24
	v_ashrrev_i32_e32 v27, 31, v26
	v_lshl_add_u64 v[34:35], v[28:29], 2, s[6:7]
	v_add_u32_e32 v28, 0xb0, v22
	s_addc_u32 s23, s23, 0
	v_lshlrev_b32_e32 v6, 2, v214
	v_lshl_add_u64 v[18:19], v[18:19], 2, s[6:7]
	v_ashrrev_i32_e32 v21, 31, v20
	v_lshl_add_u64 v[24:25], v[24:25], 2, s[6:7]
	v_lshl_add_u64 v[26:27], v[26:27], 2, s[6:7]
	v_ashrrev_i32_e32 v29, 31, v28
	global_load_dwordx4 v[10:13], v6, s[22:23] offset:16
	global_load_dwordx4 v[14:17], v6, s[22:23]
	global_load_dwordx4 v[2:5], v6, s[22:23] offset:528
	s_nop 0
	global_load_dwordx4 v[6:9], v6, s[22:23] offset:512
	v_lshl_add_u64 v[20:21], v[20:21], 2, s[6:7]
	v_lshl_add_u64 v[36:37], v[28:29], 2, s[6:7]
	global_load_dword v30, v[18:19], off
	global_load_dword v29, v[20:21], off
	global_load_dword v28, v[24:25], off
	s_nop 0
	global_load_dword v27, v[26:27], off
	s_nop 0
	global_load_dword v26, v[32:33], off
	global_load_dword v25, v[34:35], off
	global_load_dword v24, v[36:37], off
	v_add_u32_e32 v20, s28, v195
	v_add_u32_e32 v18, s28, v213
	v_cmp_gt_i32_e32 vcc, s2, v212
	v_ashrrev_i32_e32 v21, 31, v20
	v_ashrrev_i32_e32 v19, 31, v18
	v_ashrrev_i32_e32 v23, 31, v22
	v_lshl_add_u64 v[32:33], v[22:23], 2, s[6:7]
	global_load_dword v31, v[32:33], off
	s_waitcnt vmcnt(0)
	s_and_saveexec_b64 s[22:23], vcc
	s_mov_b32 s43, s79
	s_cbranch_execz .LBB0_1641
	v_mov_b32_e32 v32, 0
	v_mov_b32_e32 v33, 0
	v_mov_b32_e32 v34, 0
	v_mov_b32_e32 v35, 0
	v_lshlrev_b64 v[22:23], 11, v[22:23]
	v_lshl_add_u64 v[22:23], s[24:25], 0, v[22:23]
	v_mul_f32_e32 v36, 0x41800000, v31
	v_mul_f32_e32 v38, 0x3c800000, v36
	v_pk_mul_f32 v[42:43], v[90:91], v[38:39] op_sel_hi:[1,0]
	v_pk_mul_f32 v[46:47], v[102:103], v[38:39] op_sel_hi:[1,0]
	v_pk_mul_f32 v[40:41], v[92:93], v[38:39] op_sel_hi:[1,0]
	v_pk_mul_f32 v[44:45], v[104:105], v[38:39] op_sel_hi:[1,0]
	v_pk_mul_f32 v[48:49], v[164:165], v[38:39] op_sel_hi:[1,0]
	v_pk_mul_f32 v[50:51], v[162:163], v[38:39] op_sel_hi:[1,0]
	v_pk_mul_f32 v[52:53], v[168:169], v[38:39] op_sel_hi:[1,0]
	v_pk_mul_f32 v[38:39], v[166:167], v[38:39] op_sel_hi:[1,0]
	v_pk_fma_f32 v[42:43], v[14:15], v[36:37], v[42:43] op_sel_hi:[1,0,1]
	v_pk_fma_f32 v[46:47], v[10:11], v[36:37], v[46:47] op_sel_hi:[1,0,1]
	v_pk_fma_f32 v[40:41], v[16:17], v[36:37], v[40:41] op_sel_hi:[1,0,1]
	v_pk_fma_f32 v[44:45], v[12:13], v[36:37], v[44:45] op_sel_hi:[1,0,1]
	v_pk_fma_f32 v[48:49], v[8:9], v[36:37], v[48:49] op_sel_hi:[1,0,1]
	v_pk_fma_f32 v[50:51], v[6:7], v[36:37], v[50:51] op_sel_hi:[1,0,1]
	v_pk_fma_f32 v[52:53], v[4:5], v[36:37], v[52:53] op_sel_hi:[1,0,1]
	v_pk_fma_f32 v[36:37], v[2:3], v[36:37], v[38:39] op_sel_hi:[1,0,1]
	v_cvt_pk_fp8_f32 v32, v42, v43
	v_cvt_pk_fp8_f32 v33, v46, v47
	v_cvt_pk_fp8_f32 v34, v50, v51
	v_cvt_pk_fp8_f32 v35, v36, v37
	v_cvt_pk_fp8_f32 v32, v40, v41 op_sel:[0,0,1]
	v_cvt_pk_fp8_f32 v33, v44, v45 op_sel:[0,0,1]
	v_cvt_pk_fp8_f32 v34, v48, v49 op_sel:[0,0,1]
	v_cvt_pk_fp8_f32 v35, v52, v53 op_sel:[0,0,1]
	v_lshl_add_u64 v[36:37], v[22:23], 0, v[20:21]
	v_lshl_add_u64 v[22:23], v[22:23], 0, v[18:19]
	global_store_dwordx2 v[36:37], v[32:33], off
	global_store_dwordx2 v[22:23], v[34:35], off
	s_or_b64 exec, exec, s[22:23]
	v_cmp_gt_i32_e32 vcc, s2, v215
	s_and_saveexec_b64 s[22:23], vcc
	s_cbranch_execnz .LBB0_1642

.LBB0_1635:
	v_mul_f32_e32 v22, 0x41800000, v29
	v_mul_f32_e32 v30, 0x3c800000, v22
	v_pk_mul_f32 v[34:35], v[122:123], v[30:31] op_sel_hi:[1,0]
	v_pk_mul_f32 v[36:37], v[130:131], v[30:31] op_sel_hi:[1,0]
	v_pk_fma_f32 v[34:35], v[14:15], v[22:23], v[34:35] op_sel_hi:[1,0,1]
	v_pk_fma_f32 v[36:37], v[10:11], v[22:23], v[36:37] op_sel_hi:[1,0,1]
	v_mov_b32_e32 v38, 0
	v_mov_b32_e32 v39, 0
	v_cvt_pk_fp8_f32 v38, v34, v35
	v_cvt_pk_fp8_f32 v39, v36, v37
	v_pk_mul_f32 v[36:37], v[178:179], v[30:31] op_sel_hi:[1,0]
	v_pk_mul_f32 v[40:41], v[182:183], v[30:31] op_sel_hi:[1,0]
	v_pk_fma_f32 v[36:37], v[6:7], v[22:23], v[36:37] op_sel_hi:[1,0,1]
	v_pk_fma_f32 v[40:41], v[2:3], v[22:23], v[40:41] op_sel_hi:[1,0,1]
	v_mov_b32_e32 v42, 0
	v_mov_b32_e32 v43, 0
	v_pk_mul_f32 v[32:33], v[124:125], v[30:31] op_sel_hi:[1,0]
	v_pk_mul_f32 v[34:35], v[132:133], v[30:31] op_sel_hi:[1,0]
	v_cvt_pk_fp8_f32 v42, v36, v37
	v_cvt_pk_fp8_f32 v43, v40, v41
	v_pk_fma_f32 v[32:33], v[16:17], v[22:23], v[32:33] op_sel_hi:[1,0,1]
	v_pk_fma_f32 v[34:35], v[12:13], v[22:23], v[34:35] op_sel_hi:[1,0,1]
	v_cvt_pk_fp8_f32 v38, v32, v33 op_sel:[0,0,1]
	v_cvt_pk_fp8_f32 v39, v34, v35 op_sel:[0,0,1]
	v_add_u32_e32 v32, s4, v216
	v_pk_mul_f32 v[34:35], v[180:181], v[30:31] op_sel_hi:[1,0]
	v_pk_mul_f32 v[30:31], v[184:185], v[30:31] op_sel_hi:[1,0]
	v_ashrrev_i32_e32 v33, 31, v32
	v_pk_fma_f32 v[34:35], v[8:9], v[22:23], v[34:35] op_sel_hi:[1,0,1]
	v_pk_fma_f32 v[22:23], v[4:5], v[22:23], v[30:31] op_sel_hi:[1,0,1]
	v_lshlrev_b64 v[32:33], 11, v[32:33]
	v_cvt_pk_fp8_f32 v42, v34, v35 op_sel:[0,0,1]
	v_cvt_pk_fp8_f32 v43, v22, v23 op_sel:[0,0,1]
	v_lshl_add_u64 v[32:33], s[24:25], 0, v[32:33]
	v_lshl_add_u64 v[22:23], v[32:33], 0, v[20:21]
	global_store_dwordx2 v[22:23], v[38:39], off
	v_lshl_add_u64 v[22:23], v[32:33], 0, v[18:19]
	global_store_dwordx2 v[22:23], v[42:43], off
	s_or_b64 exec, exec, s[22:23]
	v_cmp_gt_i32_e32 vcc, s2, v217
	s_and_saveexec_b64 s[22:23], vcc
	s_cbranch_execnz .LBB0_1644

.LBB0_1637:
	v_mul_f32_e32 v22, 0x41800000, v27
	v_mul_f32_e32 v28, 0x3c800000, v22
	v_pk_mul_f32 v[32:33], v[66:67], v[28:29] op_sel_hi:[1,0]
	v_pk_mul_f32 v[34:35], v[70:71], v[28:29] op_sel_hi:[1,0]
	v_pk_fma_f32 v[32:33], v[14:15], v[22:23], v[32:33] op_sel_hi:[1,0,1]
	v_pk_fma_f32 v[34:35], v[10:11], v[22:23], v[34:35] op_sel_hi:[1,0,1]
	v_mov_b32_e32 v36, 0
	v_mov_b32_e32 v37, 0
	v_cvt_pk_fp8_f32 v36, v32, v33
	v_cvt_pk_fp8_f32 v37, v34, v35
	v_pk_mul_f32 v[34:35], v[110:111], v[28:29] op_sel_hi:[1,0]
	v_pk_mul_f32 v[38:39], v[118:119], v[28:29] op_sel_hi:[1,0]
	v_pk_fma_f32 v[34:35], v[6:7], v[22:23], v[34:35] op_sel_hi:[1,0,1]
	v_pk_fma_f32 v[38:39], v[2:3], v[22:23], v[38:39] op_sel_hi:[1,0,1]
	v_mov_b32_e32 v40, 0
	v_mov_b32_e32 v41, 0
	v_pk_mul_f32 v[30:31], v[68:69], v[28:29] op_sel_hi:[1,0]
	v_pk_mul_f32 v[32:33], v[72:73], v[28:29] op_sel_hi:[1,0]
	v_cvt_pk_fp8_f32 v40, v34, v35
	v_cvt_pk_fp8_f32 v41, v38, v39
	v_pk_fma_f32 v[30:31], v[16:17], v[22:23], v[30:31] op_sel_hi:[1,0,1]
	v_pk_fma_f32 v[32:33], v[12:13], v[22:23], v[32:33] op_sel_hi:[1,0,1]
	v_cvt_pk_fp8_f32 v36, v30, v31 op_sel:[0,0,1]
	v_cvt_pk_fp8_f32 v37, v32, v33 op_sel:[0,0,1]
	v_add_u32_e32 v30, s4, v218
	v_pk_mul_f32 v[32:33], v[112:113], v[28:29] op_sel_hi:[1,0]
	v_pk_mul_f32 v[28:29], v[120:121], v[28:29] op_sel_hi:[1,0]
	v_ashrrev_i32_e32 v31, 31, v30
	v_pk_fma_f32 v[32:33], v[8:9], v[22:23], v[32:33] op_sel_hi:[1,0,1]
	v_pk_fma_f32 v[22:23], v[4:5], v[22:23], v[28:29] op_sel_hi:[1,0,1]
	v_lshlrev_b64 v[30:31], 11, v[30:31]
	v_cvt_pk_fp8_f32 v40, v32, v33 op_sel:[0,0,1]
	v_cvt_pk_fp8_f32 v41, v22, v23 op_sel:[0,0,1]
	v_lshl_add_u64 v[30:31], s[24:25], 0, v[30:31]
	v_lshl_add_u64 v[22:23], v[30:31], 0, v[20:21]
	global_store_dwordx2 v[22:23], v[36:37], off
	v_lshl_add_u64 v[22:23], v[30:31], 0, v[18:19]
	global_store_dwordx2 v[22:23], v[40:41], off
	s_or_b64 exec, exec, s[22:23]
	v_cmp_gt_i32_e32 vcc, s2, v219
	s_and_saveexec_b64 s[22:23], vcc
	s_cbranch_execnz .LBB0_1646

.LBB0_1639:
	v_mul_f32_e32 v22, 0x41800000, v25
	v_mul_f32_e32 v26, 0x3c800000, v22
	v_pk_mul_f32 v[30:31], v[82:83], v[26:27] op_sel_hi:[1,0]
	v_pk_mul_f32 v[32:33], v[86:87], v[26:27] op_sel_hi:[1,0]
	v_pk_fma_f32 v[30:31], v[14:15], v[22:23], v[30:31] op_sel_hi:[1,0,1]
	v_pk_fma_f32 v[32:33], v[10:11], v[22:23], v[32:33] op_sel_hi:[1,0,1]
	v_mov_b32_e32 v34, 0
	v_mov_b32_e32 v35, 0
	v_cvt_pk_fp8_f32 v34, v30, v31
	v_cvt_pk_fp8_f32 v35, v32, v33
	v_pk_mul_f32 v[32:33], v[142:143], v[26:27] op_sel_hi:[1,0]
	v_pk_mul_f32 v[36:37], v[150:151], v[26:27] op_sel_hi:[1,0]
	v_pk_fma_f32 v[32:33], v[6:7], v[22:23], v[32:33] op_sel_hi:[1,0,1]
	v_pk_fma_f32 v[36:37], v[2:3], v[22:23], v[36:37] op_sel_hi:[1,0,1]
	v_mov_b32_e32 v38, 0
	v_mov_b32_e32 v39, 0
	v_pk_mul_f32 v[28:29], v[84:85], v[26:27] op_sel_hi:[1,0]
	v_pk_mul_f32 v[30:31], v[88:89], v[26:27] op_sel_hi:[1,0]
	v_cvt_pk_fp8_f32 v38, v32, v33
	v_cvt_pk_fp8_f32 v39, v36, v37
	v_pk_fma_f32 v[28:29], v[16:17], v[22:23], v[28:29] op_sel_hi:[1,0,1]
	v_pk_fma_f32 v[30:31], v[12:13], v[22:23], v[30:31] op_sel_hi:[1,0,1]
	v_cvt_pk_fp8_f32 v34, v28, v29 op_sel:[0,0,1]
	v_cvt_pk_fp8_f32 v35, v30, v31 op_sel:[0,0,1]
	v_add_u32_e32 v28, s4, v220
	v_pk_mul_f32 v[30:31], v[144:145], v[26:27] op_sel_hi:[1,0]
	v_pk_mul_f32 v[26:27], v[152:153], v[26:27] op_sel_hi:[1,0]
	v_ashrrev_i32_e32 v29, 31, v28
	v_pk_fma_f32 v[30:31], v[8:9], v[22:23], v[30:31] op_sel_hi:[1,0,1]
	v_pk_fma_f32 v[22:23], v[4:5], v[22:23], v[26:27] op_sel_hi:[1,0,1]
	v_lshlrev_b64 v[28:29], 11, v[28:29]
	v_cvt_pk_fp8_f32 v38, v30, v31 op_sel:[0,0,1]
	v_cvt_pk_fp8_f32 v39, v22, v23 op_sel:[0,0,1]
	v_lshl_add_u64 v[28:29], s[24:25], 0, v[28:29]
	v_lshl_add_u64 v[22:23], v[28:29], 0, v[20:21]
	global_store_dwordx2 v[22:23], v[34:35], off
	v_lshl_add_u64 v[22:23], v[28:29], 0, v[18:19]
	global_store_dwordx2 v[22:23], v[38:39], off
	s_or_b64 exec, exec, s[22:23]
	v_cmp_gt_i32_e32 vcc, s2, v221
	s_and_saveexec_b64 s[22:23], vcc
	s_cbranch_execnz .LBB0_1648

.LBB0_1642:
	v_mul_f32_e32 v22, 0x41800000, v30
	v_mul_f32_e32 v30, 0x3c800000, v22
	v_pk_mul_f32 v[34:35], v[106:107], v[30:31] op_sel_hi:[1,0]
	v_pk_mul_f32 v[36:37], v[114:115], v[30:31] op_sel_hi:[1,0]
	v_pk_fma_f32 v[34:35], v[14:15], v[22:23], v[34:35] op_sel_hi:[1,0,1]
	v_pk_fma_f32 v[36:37], v[10:11], v[22:23], v[36:37] op_sel_hi:[1,0,1]
	v_mov_b32_e32 v38, 0
	v_mov_b32_e32 v39, 0
	v_cvt_pk_fp8_f32 v38, v34, v35
	v_cvt_pk_fp8_f32 v39, v36, v37
	v_pk_mul_f32 v[36:37], v[170:171], v[30:31] op_sel_hi:[1,0]
	v_pk_mul_f32 v[40:41], v[174:175], v[30:31] op_sel_hi:[1,0]
	v_pk_fma_f32 v[36:37], v[6:7], v[22:23], v[36:37] op_sel_hi:[1,0,1]
	v_pk_fma_f32 v[40:41], v[2:3], v[22:23], v[40:41] op_sel_hi:[1,0,1]
	v_mov_b32_e32 v42, 0
	v_mov_b32_e32 v43, 0
	v_pk_mul_f32 v[32:33], v[108:109], v[30:31] op_sel_hi:[1,0]
	v_pk_mul_f32 v[34:35], v[116:117], v[30:31] op_sel_hi:[1,0]
	v_cvt_pk_fp8_f32 v42, v36, v37
	v_cvt_pk_fp8_f32 v43, v40, v41
	v_pk_fma_f32 v[32:33], v[16:17], v[22:23], v[32:33] op_sel_hi:[1,0,1]
	v_pk_fma_f32 v[34:35], v[12:13], v[22:23], v[34:35] op_sel_hi:[1,0,1]
	v_cvt_pk_fp8_f32 v38, v32, v33 op_sel:[0,0,1]
	v_cvt_pk_fp8_f32 v39, v34, v35 op_sel:[0,0,1]
	v_add_u32_e32 v32, s4, v215
	v_pk_mul_f32 v[34:35], v[172:173], v[30:31] op_sel_hi:[1,0]
	v_pk_mul_f32 v[30:31], v[176:177], v[30:31] op_sel_hi:[1,0]
	v_ashrrev_i32_e32 v33, 31, v32
	v_pk_fma_f32 v[34:35], v[8:9], v[22:23], v[34:35] op_sel_hi:[1,0,1]
	v_pk_fma_f32 v[22:23], v[4:5], v[22:23], v[30:31] op_sel_hi:[1,0,1]
	v_lshlrev_b64 v[32:33], 11, v[32:33]
	v_cvt_pk_fp8_f32 v42, v34, v35 op_sel:[0,0,1]
	v_cvt_pk_fp8_f32 v43, v22, v23 op_sel:[0,0,1]
	v_lshl_add_u64 v[32:33], s[24:25], 0, v[32:33]
	v_lshl_add_u64 v[22:23], v[32:33], 0, v[20:21]
	global_store_dwordx2 v[22:23], v[38:39], off
	v_lshl_add_u64 v[22:23], v[32:33], 0, v[18:19]
	global_store_dwordx2 v[22:23], v[42:43], off
	s_or_b64 exec, exec, s[22:23]
	v_cmp_gt_i32_e32 vcc, s2, v216
	s_and_saveexec_b64 s[22:23], vcc
	s_cbranch_execnz .LBB0_1635

.LBB0_1644:
	v_mul_f32_e32 v22, 0x41800000, v28
	v_mul_f32_e32 v28, 0x3c800000, v22
	v_pk_mul_f32 v[32:33], v[138:139], v[28:29] op_sel_hi:[1,0]
	v_pk_mul_f32 v[34:35], v[146:147], v[28:29] op_sel_hi:[1,0]
	v_pk_fma_f32 v[32:33], v[14:15], v[22:23], v[32:33] op_sel_hi:[1,0,1]
	v_pk_fma_f32 v[34:35], v[10:11], v[22:23], v[34:35] op_sel_hi:[1,0,1]
	v_mov_b32_e32 v36, 0
	v_mov_b32_e32 v37, 0
	v_cvt_pk_fp8_f32 v36, v32, v33
	v_cvt_pk_fp8_f32 v37, v34, v35
	v_pk_mul_f32 v[34:35], v[186:187], v[28:29] op_sel_hi:[1,0]
	v_pk_mul_f32 v[38:39], v[190:191], v[28:29] op_sel_hi:[1,0]
	v_pk_fma_f32 v[34:35], v[6:7], v[22:23], v[34:35] op_sel_hi:[1,0,1]
	v_pk_fma_f32 v[38:39], v[2:3], v[22:23], v[38:39] op_sel_hi:[1,0,1]
	v_mov_b32_e32 v40, 0
	v_mov_b32_e32 v41, 0
	v_pk_mul_f32 v[30:31], v[140:141], v[28:29] op_sel_hi:[1,0]
	v_pk_mul_f32 v[32:33], v[148:149], v[28:29] op_sel_hi:[1,0]
	v_cvt_pk_fp8_f32 v40, v34, v35
	v_cvt_pk_fp8_f32 v41, v38, v39
	v_pk_fma_f32 v[30:31], v[16:17], v[22:23], v[30:31] op_sel_hi:[1,0,1]
	v_pk_fma_f32 v[32:33], v[12:13], v[22:23], v[32:33] op_sel_hi:[1,0,1]
	v_cvt_pk_fp8_f32 v36, v30, v31 op_sel:[0,0,1]
	v_cvt_pk_fp8_f32 v37, v32, v33 op_sel:[0,0,1]
	v_add_u32_e32 v30, s4, v217
	v_pk_mul_f32 v[32:33], v[188:189], v[28:29] op_sel_hi:[1,0]
	v_pk_mul_f32 v[28:29], v[192:193], v[28:29] op_sel_hi:[1,0]
	v_ashrrev_i32_e32 v31, 31, v30
	v_pk_fma_f32 v[32:33], v[8:9], v[22:23], v[32:33] op_sel_hi:[1,0,1]
	v_pk_fma_f32 v[22:23], v[4:5], v[22:23], v[28:29] op_sel_hi:[1,0,1]
	v_lshlrev_b64 v[30:31], 11, v[30:31]
	v_cvt_pk_fp8_f32 v40, v32, v33 op_sel:[0,0,1]
	v_cvt_pk_fp8_f32 v41, v22, v23 op_sel:[0,0,1]
	v_lshl_add_u64 v[30:31], s[24:25], 0, v[30:31]
	v_lshl_add_u64 v[22:23], v[30:31], 0, v[20:21]
	global_store_dwordx2 v[22:23], v[36:37], off
	v_lshl_add_u64 v[22:23], v[30:31], 0, v[18:19]
	global_store_dwordx2 v[22:23], v[40:41], off
	s_or_b64 exec, exec, s[22:23]
	v_cmp_gt_i32_e32 vcc, s2, v218
	s_and_saveexec_b64 s[22:23], vcc
	s_cbranch_execnz .LBB0_1637

.LBB0_1646:
	v_mul_f32_e32 v22, 0x41800000, v26
	v_mul_f32_e32 v26, 0x3c800000, v22
	v_pk_mul_f32 v[30:31], v[74:75], v[26:27] op_sel_hi:[1,0]
	v_pk_mul_f32 v[32:33], v[78:79], v[26:27] op_sel_hi:[1,0]
	v_pk_fma_f32 v[30:31], v[14:15], v[22:23], v[30:31] op_sel_hi:[1,0,1]
	v_pk_fma_f32 v[32:33], v[10:11], v[22:23], v[32:33] op_sel_hi:[1,0,1]
	v_mov_b32_e32 v34, 0
	v_mov_b32_e32 v35, 0
	v_cvt_pk_fp8_f32 v34, v30, v31
	v_cvt_pk_fp8_f32 v35, v32, v33
	v_pk_mul_f32 v[32:33], v[126:127], v[26:27] op_sel_hi:[1,0]
	v_pk_mul_f32 v[36:37], v[134:135], v[26:27] op_sel_hi:[1,0]
	v_pk_fma_f32 v[32:33], v[6:7], v[22:23], v[32:33] op_sel_hi:[1,0,1]
	v_pk_fma_f32 v[36:37], v[2:3], v[22:23], v[36:37] op_sel_hi:[1,0,1]
	v_mov_b32_e32 v38, 0
	v_mov_b32_e32 v39, 0
	v_pk_mul_f32 v[28:29], v[76:77], v[26:27] op_sel_hi:[1,0]
	v_pk_mul_f32 v[30:31], v[80:81], v[26:27] op_sel_hi:[1,0]
	v_cvt_pk_fp8_f32 v38, v32, v33
	v_cvt_pk_fp8_f32 v39, v36, v37
	v_pk_fma_f32 v[28:29], v[16:17], v[22:23], v[28:29] op_sel_hi:[1,0,1]
	v_pk_fma_f32 v[30:31], v[12:13], v[22:23], v[30:31] op_sel_hi:[1,0,1]
	v_cvt_pk_fp8_f32 v34, v28, v29 op_sel:[0,0,1]
	v_cvt_pk_fp8_f32 v35, v30, v31 op_sel:[0,0,1]
	v_add_u32_e32 v28, s4, v219
	v_pk_mul_f32 v[30:31], v[128:129], v[26:27] op_sel_hi:[1,0]
	v_pk_mul_f32 v[26:27], v[136:137], v[26:27] op_sel_hi:[1,0]
	v_ashrrev_i32_e32 v29, 31, v28
	v_pk_fma_f32 v[30:31], v[8:9], v[22:23], v[30:31] op_sel_hi:[1,0,1]
	v_pk_fma_f32 v[22:23], v[4:5], v[22:23], v[26:27] op_sel_hi:[1,0,1]
	v_lshlrev_b64 v[28:29], 11, v[28:29]
	v_cvt_pk_fp8_f32 v38, v30, v31 op_sel:[0,0,1]
	v_cvt_pk_fp8_f32 v39, v22, v23 op_sel:[0,0,1]
	v_lshl_add_u64 v[28:29], s[24:25], 0, v[28:29]
	v_lshl_add_u64 v[22:23], v[28:29], 0, v[20:21]
	global_store_dwordx2 v[22:23], v[34:35], off
	v_lshl_add_u64 v[22:23], v[28:29], 0, v[18:19]
	global_store_dwordx2 v[22:23], v[38:39], off
	s_or_b64 exec, exec, s[22:23]
	v_cmp_gt_i32_e32 vcc, s2, v220
	s_and_saveexec_b64 s[22:23], vcc
	s_cbranch_execnz .LBB0_1639

.LBB0_1648:
	v_mul_f32_e32 v22, 0x41800000, v24
	v_mul_f32_e32 v24, 0x3c800000, v22
	v_pk_mul_f32 v[26:27], v[96:97], v[24:25] op_sel_hi:[1,0]
	v_pk_mul_f32 v[28:29], v[94:95], v[24:25] op_sel_hi:[1,0]
	v_pk_fma_f32 v[16:17], v[16:17], v[22:23], v[26:27] op_sel_hi:[1,0,1]
	v_pk_mul_f32 v[26:27], v[98:99], v[24:25] op_sel_hi:[1,0]
	v_pk_fma_f32 v[14:15], v[14:15], v[22:23], v[28:29] op_sel_hi:[1,0,1]
	v_pk_fma_f32 v[10:11], v[10:11], v[22:23], v[26:27] op_sel_hi:[1,0,1]
	v_mov_b32_e32 v27, 0
	v_cvt_pk_fp8_f32 v27, v10, v11
	v_pk_mul_f32 v[10:11], v[100:101], v[24:25] op_sel_hi:[1,0]
	v_mov_b32_e32 v26, 0
	v_pk_fma_f32 v[10:11], v[12:13], v[22:23], v[10:11] op_sel_hi:[1,0,1]
	v_pk_mul_f32 v[12:13], v[156:157], v[24:25] op_sel_hi:[1,0]
	v_cvt_pk_fp8_f32 v26, v14, v15
	v_pk_mul_f32 v[14:15], v[154:155], v[24:25] op_sel_hi:[1,0]
	v_pk_fma_f32 v[8:9], v[8:9], v[22:23], v[12:13] op_sel_hi:[1,0,1]
	v_pk_mul_f32 v[12:13], v[158:159], v[24:25] op_sel_hi:[1,0]
	v_pk_fma_f32 v[6:7], v[6:7], v[22:23], v[14:15] op_sel_hi:[1,0,1]
	v_pk_fma_f32 v[2:3], v[2:3], v[22:23], v[12:13] op_sel_hi:[1,0,1]
	v_mov_b32_e32 v12, 0
	v_mov_b32_e32 v13, 0
	v_cvt_pk_fp8_f32 v12, v6, v7
	v_cvt_pk_fp8_f32 v13, v2, v3
	v_cvt_pk_fp8_f32 v27, v10, v11 op_sel:[0,0,1]
	v_add_u32_e32 v10, s4, v221
	v_pk_mul_f32 v[2:3], v[160:161], v[24:25] op_sel_hi:[1,0]
	v_cvt_pk_fp8_f32 v26, v16, v17 op_sel:[0,0,1]
	v_ashrrev_i32_e32 v11, 31, v10
	v_pk_fma_f32 v[2:3], v[4:5], v[22:23], v[2:3] op_sel_hi:[1,0,1]
	v_lshlrev_b64 v[10:11], 11, v[10:11]
	v_cvt_pk_fp8_f32 v12, v8, v9 op_sel:[0,0,1]
	v_cvt_pk_fp8_f32 v13, v2, v3 op_sel:[0,0,1]
	v_lshl_add_u64 v[10:11], s[24:25], 0, v[10:11]
	v_lshl_add_u64 v[2:3], v[10:11], 0, v[20:21]
	global_store_dwordx2 v[2:3], v[26:27], off
	v_lshl_add_u64 v[2:3], v[10:11], 0, v[18:19]
	global_store_dwordx2 v[2:3], v[12:13], off
	s_or_b64 exec, exec, s[22:23]
	s_andn2_b64 vcc, exec, s[16:17]
	s_mov_b64 s[4:5], -1
	s_cbranch_vccnz .LBB0_1604

	.amdhsa_kernel _Z10fwd_kernel4Args
		.amdhsa_group_segment_fixed_size 0
		.amdhsa_private_segment_fixed_size 0
		.amdhsa_kernarg_size 456
		.amdhsa_user_sgpr_count 2
		.amdhsa_user_sgpr_dispatch_ptr 0
		.amdhsa_user_sgpr_queue_ptr 0
		.amdhsa_user_sgpr_kernarg_segment_ptr 1
		.amdhsa_user_sgpr_dispatch_id 0
		.amdhsa_user_sgpr_kernarg_preload_length 0
		.amdhsa_user_sgpr_kernarg_preload_offset 0
		.amdhsa_user_sgpr_private_segment_size 0
		.amdhsa_uses_dynamic_stack 0
		.amdhsa_enable_private_segment 0
		.amdhsa_system_sgpr_workgroup_id_x 1
		.amdhsa_system_sgpr_workgroup_id_y 0
		.amdhsa_system_sgpr_workgroup_id_z 0
		.amdhsa_system_sgpr_workgroup_info 0
		.amdhsa_system_vgpr_workitem_id 0
		.amdhsa_next_free_vgpr 256
		.amdhsa_next_free_sgpr 102
		.amdhsa_accum_offset 256
		.amdhsa_reserve_vcc 1
		.amdhsa_float_round_mode_32 0
		.amdhsa_float_round_mode_16_64 0
		.amdhsa_float_denorm_mode_32 3
		.amdhsa_float_denorm_mode_16_64 3
		.amdhsa_dx10_clamp 1
		.amdhsa_ieee_mode 1
		.amdhsa_fp16_overflow 0
		.amdhsa_tg_split 0
		.amdhsa_exception_fp_ieee_invalid_op 0
		.amdhsa_exception_fp_denorm_src 0
		.amdhsa_exception_fp_ieee_div_zero 0
		.amdhsa_exception_fp_ieee_overflow 0
		.amdhsa_exception_fp_ieee_underflow 0
		.amdhsa_exception_fp_ieee_inexact 0
		.amdhsa_exception_int_div_zero 0
	.end_amdhsa_kernel

amdhsa.kernels:
  - .agpr_count:     0
    .args:
      - .offset:         0
        .size:           200
        .value_kind:     by_value
      - .offset:         200
        .size:           4
        .value_kind:     hidden_block_count_x
      - .offset:         204
        .size:           4
        .value_kind:     hidden_block_count_y
      - .offset:         208
        .size:           4
        .value_kind:     hidden_block_count_z
      - .offset:         212
        .size:           2
        .value_kind:     hidden_group_size_x
      - .offset:         214
        .size:           2
        .value_kind:     hidden_group_size_y
      - .offset:         216
        .size:           2
        .value_kind:     hidden_group_size_z
      - .offset:         218
        .size:           2
        .value_kind:     hidden_remainder_x
      - .offset:         220
        .size:           2
        .value_kind:     hidden_remainder_y
      - .offset:         222
        .size:           2
        .value_kind:     hidden_remainder_z
      - .offset:         240
        .size:           8
        .value_kind:     hidden_global_offset_x
      - .offset:         248
        .size:           8
        .value_kind:     hidden_global_offset_y
      - .offset:         256
        .size:           8
        .value_kind:     hidden_global_offset_z
      - .offset:         264
        .size:           2
        .value_kind:     hidden_grid_dims
      - .offset:         320
        .size:           4
        .value_kind:     hidden_dynamic_lds_size
    .group_segment_fixed_size: 0
    .kernarg_segment_align: 8
    .kernarg_segment_size: 456
    .language:       OpenCL C
    .language_version:
      - 2
      - 0
    .max_flat_workgroup_size: 512
    .name:           _Z10fwd_kernel4Args
    .private_segment_fixed_size: 0
    .sgpr_count:     108
    .sgpr_spill_count: 115
    .symbol:         _Z10fwd_kernel4Args.kd
    .uniform_work_group_size: 1
    .uses_dynamic_stack: false
    .vgpr_count:     256
    .vgpr_spill_count: 0
    .wavefront_size: 64
